# defer work-queue dequeue atomic return to unit end (mixer + hyena conv queues) and drop vmcnt(0) drain at pool/hyprep/gmlp entry barriers
# baseline (speedup 1.0000x reference)
.LBB0_454:
	v_cndmask_b32_e64 v2, 0, 1, s[6:7]
	v_mov_b32_e32 v176, 0xab0
	v_cmp_ne_u32_e64 s[6:7], 1, v2
	v_mov_b32_e32 v177, 0x9b8
	s_and_saveexec_b64 s[8:9], s[4:5]
	s_cbranch_execz .LBB0_463
	s_and_b64 vcc, exec, s[6:7]
	v_mov_b32_e32 v176, 0xab0
	s_cbranch_vccnz .LBB0_459
	s_mov_b64 s[12:13], exec
	v_mbcnt_lo_u32_b32 v2, s12, 0
	v_mbcnt_hi_u32_b32 v2, s13, v2
	v_cmp_eq_u32_e32 vcc, 0, v2
	s_and_saveexec_b64 s[10:11], vcc
	s_cbranch_execz .LBB0_458
	s_bcnt1_i32_b64 s12, s[12:13]
	v_mov_b32_e32 v4, s12
	v_readlane_b32 s12, v242, 5
	v_readlane_b32 s13, v242, 6
	s_nop 4
	global_atomic_add v243, v3, v4, s[12:13] sc0
.LBB0_458:
	s_or_b64 exec, exec, s[10:11]
	v_mov_b32_e32 v176, -1

; #define LAS __attribute__((address_space(3)))
; __device__ __forceinline__ void hyprep_unit(Ctx& C, int l, int uidx) {
;     constexpr int RS = 528;
;     int seq, tb, cb, L, rowbase; bf16* T;
;     if (uidx < 1536) { seq = uidx / 384; const int rem = uidx % 384; tb = rem / 6; cb = rem % 6; L = SL; rowbase = seq * SL; T = WSP(bf16, WS_TL); }
;     else { const int v = uidx - 1536; seq = v / 24; const int rem = v % 24; tb = rem / 6; cb = rem % 6; L = CL; rowbase = NLAT + seq * CL; T = WSP(bf16, WS_TC); }
;     const int t0 = 64 * tb; const bf16* Z = WSP(bf16, WS_Z);
;     __syncthreads();
;     { u32x4 v[5];
; #pragma unroll
;         for (int i = 0; i < 5; ++i) { const int idx0 = C.tid + 512 * i, idx = idx0 < 66 * 32 ? idx0 : 66 * 32 - 1, r = idx >> 5, ch = idx & 31, t = t0 - 1 + r; const bool ok = t >= 0 && t < L;
;             const int tc = t < 0 ? 0 : (t < L ? t : L - 1);
;             v[i] = *(const u32x4*)(Z + (size_t)(rowbase + tc) * INW + 1280 + 256 * cb + 8 * ch); if (!ok) v[i] = (u32x4){0u, 0u, 0u, 0u}; }
; #pragma unroll
;         for (int i = 0; i < 5; ++i) { const int idx0 = C.tid + 512 * i, idx = idx0 < 66 * 32 ? idx0 : 66 * 32 - 1, r = idx >> 5, ch = idx & 31;
;             if (i < 4 || idx0 < 66 * 32) *(LAS u32x4*)(C.lds + r * RS + ch * 16) = v[i]; } }
.LBB0_474:
	s_and_b32 s9, 0xffff, s8
	s_mul_i32 s9, s9, 0xaaab
	s_lshr_b32 s9, s9, 18
	s_mul_i32 s11, s9, 6
	s_lshl_b32 s14, s9, 6
	v_min_i32_e32 v2, 0x63f, v178
	s_sub_i32 s18, s8, s11
	s_and_b32 s11, s14, 0xffc0
	v_add_u32_e32 v4, 0x200, v2
	s_add_i32 s11, s11, -1
	v_ashrrev_i32_e32 v26, 5, v4
	s_add_i32 s15, s12, -1
	v_add_u32_e32 v27, s11, v26
	v_min_i32_e32 v4, s15, v27
	v_cmp_lt_i32_e32 vcc, -1, v27
	v_mov_b64_e32 v[16:17], s[54:55]
	v_lshlrev_b32_e32 v2, 4, v2
	v_cndmask_b32_e32 v4, 0, v4, vcc
	v_add_u32_e32 v4, s10, v4
	v_mad_u64_u32 v[4:5], s[8:9], v4, s66, v[16:17]
	s_lshl_b32 s8, s18, 9
	s_and_b32 s38, s8, 0x1fe00
	v_lshl_add_u64 v[4:5], v[4:5], 0, s[38:39]
	v_and_b32_e32 v2, 0x1f0, v2
	v_min_i32_e32 v8, 0x43f, v178
	v_lshl_add_u64 v[4:5], v[4:5], 0, v[2:3]
	s_mov_b32 s19, 0x36000000
	v_add_u32_e32 v6, 0x400, v8
	v_add_co_u32_e32 v4, vcc, s19, v4
	v_ashrrev_i32_e32 v28, 5, v6
	s_nop 0
	v_addc_co_u32_e32 v5, vcc, 0, v5, vcc
	v_add_u32_e32 v29, s11, v28
	v_min_i32_e32 v6, s15, v29
	v_cmp_lt_i32_e32 vcc, -1, v29
	v_lshlrev_b32_e32 v8, 4, v8
	v_and_b32_e32 v20, 0x1f0, v8
	v_cndmask_b32_e32 v6, 0, v6, vcc
	v_add_u32_e32 v6, s10, v6
	v_mad_u64_u32 v[6:7], s[8:9], v6, s66, v[16:17]
	v_lshl_add_u64 v[6:7], v[6:7], 0, s[38:39]
	v_mov_b32_e32 v21, v3
	v_min_i32_e32 v14, 0x23f, v178
	v_lshl_add_u64 v[6:7], v[6:7], 0, v[20:21]
	v_add_u32_e32 v12, 0x600, v14
	v_add_co_u32_e32 v8, vcc, s19, v6
	v_ashrrev_i32_e32 v21, 5, v12
	s_nop 0
	v_addc_co_u32_e32 v9, vcc, 0, v7, vcc
	v_add_u32_e32 v30, s11, v21
	v_min_i32_e32 v12, s15, v30
	v_cmp_lt_i32_e32 vcc, -1, v30
	v_lshlrev_b32_e32 v14, 4, v14
	v_and_b32_e32 v22, 0x1f0, v14
	v_cndmask_b32_e32 v12, 0, v12, vcc
	v_add_u32_e32 v12, s10, v12
	v_mad_u64_u32 v[12:13], s[8:9], v12, s66, v[16:17]
	v_lshl_add_u64 v[12:13], v[12:13], 0, s[38:39]
	v_mov_b32_e32 v23, v3
	v_lshl_add_u64 v[12:13], v[12:13], 0, v[22:23]
	v_min_i32_e32 v18, 0x83f, v178
	v_add_co_u32_e32 v12, vcc, s19, v12
	v_ashrrev_i32_e32 v23, 5, v18
	s_nop 0
	v_addc_co_u32_e32 v13, vcc, 0, v13, vcc
	v_add_u32_e32 v31, s11, v23
	v_min_i32_e32 v19, s15, v31
	v_cmp_lt_i32_e32 vcc, -1, v31
	v_lshlrev_b32_e32 v18, 4, v18
	v_and_b32_e32 v24, 0x1f0, v18
	v_cndmask_b32_e32 v19, 0, v19, vcc
	v_add_u32_e32 v19, s10, v19
	v_mad_u64_u32 v[16:17], s[8:9], v19, s66, v[16:17]
	v_lshl_add_u64 v[16:17], v[16:17], 0, s[38:39]
	v_mov_b32_e32 v25, v3
	v_lshl_add_u64 v[16:17], v[16:17], 0, v[24:25]
	s_waitcnt lgkmcnt(0)
	s_barrier
	global_load_dwordx4 v[4:7], v[4:5], off offset:2560
	s_nop 0
	global_load_dwordx4 v[8:11], v[8:9], off offset:2560
	v_add_co_u32_e32 v16, vcc, s19, v16
	global_load_dwordx4 v[12:15], v[12:13], off offset:2560
	s_nop 0
	v_addc_co_u32_e32 v17, vcc, 0, v17, vcc
	global_load_dwordx4 v[16:19], v[16:17], off offset:2560
	v_cmp_gt_u32_e32 vcc, s12, v27
	v_mul_lo_u32 v23, v23, s36
	v_add3_u32 v23, 0, v23, v24
	s_mov_b32 s34, 0x36000000
	s_lshl_b32 s18, s18, 8
	s_waitcnt vmcnt(3)
	v_cndmask_b32_e32 v7, 0, v7, vcc
	v_cndmask_b32_e32 v6, 0, v6, vcc
	v_cndmask_b32_e32 v5, 0, v5, vcc
	v_cndmask_b32_e32 v4, 0, v4, vcc
	v_cmp_gt_u32_e32 vcc, s12, v29
	s_waitcnt vmcnt(2)
	s_nop 0
	v_cndmask_b32_e32 v11, 0, v11, vcc
	v_cndmask_b32_e32 v10, 0, v10, vcc
	v_cndmask_b32_e32 v9, 0, v9, vcc
	v_cndmask_b32_e32 v8, 0, v8, vcc
	v_cmp_gt_u32_e32 vcc, s12, v30
	s_waitcnt vmcnt(1)
	s_nop 0
	v_cndmask_b32_e32 v15, 0, v15, vcc
	v_cndmask_b32_e32 v14, 0, v14, vcc
	v_cndmask_b32_e32 v13, 0, v13, vcc
	v_cndmask_b32_e32 v12, 0, v12, vcc
	v_cmp_gt_u32_e32 vcc, s12, v31
	s_waitcnt vmcnt(0)
	s_nop 0
	v_cndmask_b32_e32 v19, 0, v19, vcc
	v_cndmask_b32_e32 v18, 0, v18, vcc
	v_cndmask_b32_e32 v17, 0, v17, vcc
	v_cndmask_b32_e32 v16, 0, v16, vcc
	ds_write_b128 v23, v[16:19]
	v_mul_lo_u32 v16, v26, s36
	v_add3_u32 v2, 0, v16, v2
	ds_write_b128 v2, v[4:7]
	v_mul_lo_u32 v2, v28, s36
	v_add3_u32 v2, 0, v2, v20
	ds_write_b128 v2, v[8:11]
	v_mul_lo_u32 v2, v21, s36
	v_add3_u32 v2, 0, v2, v22
	v_cmp_gt_i32_e32 vcc, 64, v178
	ds_write_b128 v2, v[12:15]
	s_and_saveexec_b64 s[8:9], vcc
	s_cbranch_execz .LBB0_476
	v_min_i32_e32 v2, 63, v178
	v_add_u32_e32 v4, 0x800, v2
	v_ashrrev_i32_e32 v4, 5, v4
	v_add_u32_e32 v8, s11, v4
	v_min_i32_e32 v4, s15, v8
	v_cmp_lt_i32_e32 vcc, -1, v8
	s_and_b32 s19, s18, 0xff00
	s_lshl_b32 s38, s19, 1
	v_cndmask_b32_e32 v4, 0, v4, vcc
	v_add_u32_e32 v6, s10, v4
	v_mov_b64_e32 v[4:5], s[54:55]
	v_mad_u64_u32 v[4:5], s[10:11], v6, s66, v[4:5]
	v_lshlrev_b32_e32 v2, 4, v2
	v_lshl_add_u64 v[4:5], v[4:5], 0, s[38:39]
	v_and_b32_e32 v2, 0x1f0, v2
	v_lshl_add_u64 v[4:5], v[4:5], 0, v[2:3]
	v_add_co_u32_e32 v4, vcc, s34, v4
	v_add_u32_e32 v2, 0x800, v178
	s_nop 0
	v_addc_co_u32_e32 v5, vcc, 0, v5, vcc
	global_load_dwordx4 v[4:7], v[4:5], off offset:2560
	v_cmp_gt_u32_e32 vcc, s12, v8
	v_ashrrev_i32_e32 v2, 5, v2
	v_lshlrev_b32_e32 v8, 4, v178
	v_mul_lo_u32 v2, v2, s36
	v_and_b32_e32 v8, 0x1f0, v8
	v_add3_u32 v2, 0, v2, v8
	s_waitcnt vmcnt(0)
	v_cndmask_b32_e32 v7, 0, v7, vcc
	v_cndmask_b32_e32 v6, 0, v6, vcc
	v_cndmask_b32_e32 v5, 0, v5, vcc
	v_cndmask_b32_e32 v4, 0, v4, vcc
	ds_write_b128 v2, v[4:7]

; #define LAS __attribute__((address_space(3)))
; __device__ __forceinline__ void pool_unit(Ctx& C, int l, int blk) {
;     ...
;     const int row0 = 32 * blk;
;     const int s0 = row0 < NLAT ? (row0 / SL) * SL : NLAT + ((row0 - NLAT) / CL) * CL, L = row0 < NLAT ? SL : CL, t0 = row0 - s0;
;     const bf16* Z = WSP(bf16, WS_Z);
;     __syncthreads();
;     { u32x4 v[6];
; #pragma unroll
;         for (int i = 0; i < 6; ++i) { const int idx = C.tid + 512 * i, r = idx >> 6, ch = idx & 63, t = t0 - 8 + r; const bool ok = t >= 0 && t < L; const int tc = t < 0 ? 0 : (t < L ? t : L - 1);
;             v[i] = *(const u32x4*)(Z + (size_t)(s0 + tc) * INW + 8 * ch); if (!ok) v[i] = (u32x4){0u, 0u, 0u, 0u}; }
; #pragma unroll
;         for (int i = 0; i < 6; ++i) { const int idx = C.tid + 512 * i, r = idx >> 6, ch = idx & 63; *(LAS u32x4*)(C.lds + r * RS + ch * 16) = v[i]; } }
;     __syncthreads();
;     {
;         const int c8 = C.tid & 63, tg = C.tid >> 6, hw = 1 << (c8 >> 4);
.LBB0_477:
	s_and_b64 vcc, exec, s[6:7]
	s_cbranch_vccz .LBB0_485
	s_add_i32 s6, s43, 0xfffffdd0
	s_lshl_b32 s10, s6, 5
	s_cmpk_lt_u32 s6, 0x200
	s_movk_i32 s6, 0x100
	s_cselect_b32 s11, 0x1000, s6
	s_movk_i32 s6, 0x7f00
	s_cselect_b32 s6, 0x3000, s6
	s_and_b32 s12, s6, s10
	s_sub_i32 s13, s10, s12
	v_lshlrev_b32_e32 v2, 4, v178
	s_add_i32 s8, s13, -8
	v_and_b32_e32 v2, 0x3f0, v2
	v_ashrrev_i32_e32 v28, 6, v178
	v_add_u32_e32 v6, 0x200, v178
	s_add_i32 s9, s11, -1
	v_lshl_add_u64 v[4:5], s[54:55], 0, v[2:3]
	s_mov_b64 s[6:7], 0x36000000
	v_add_u32_e32 v29, s8, v28
	v_ashrrev_i32_e32 v30, 6, v6
	v_lshl_add_u64 v[24:25], v[4:5], 0, s[6:7]
	v_min_i32_e32 v4, s9, v29
	v_cmp_lt_i32_e32 vcc, -1, v29
	v_add_u32_e32 v31, s8, v30
	v_min_i32_e32 v6, s9, v31
	v_cndmask_b32_e32 v4, 0, v4, vcc
	v_cmp_lt_i32_e32 vcc, -1, v31
	v_add_u32_e32 v12, 0x400, v178
	v_ashrrev_i32_e32 v32, 6, v12
	v_cndmask_b32_e32 v6, 0, v6, vcc
	v_add_u32_e32 v14, 0x600, v178
	v_add_u32_e32 v4, s12, v4
	v_add_u32_e32 v6, s12, v6
	v_add_u32_e32 v33, s8, v32
	v_ashrrev_i32_e32 v34, 6, v14
	v_mad_u64_u32 v[4:5], s[6:7], v4, s66, v[24:25]
	v_mad_u64_u32 v[8:9], s[6:7], v6, s66, v[24:25]
	v_min_i32_e32 v12, s9, v33
	v_cmp_lt_i32_e32 vcc, -1, v33
	v_add_u32_e32 v35, s8, v34
	s_waitcnt lgkmcnt(0)
	s_barrier
	global_load_dwordx4 v[4:7], v[4:5], off
	s_nop 0
	global_load_dwordx4 v[8:11], v[8:9], off
	v_cndmask_b32_e32 v12, 0, v12, vcc
	v_min_i32_e32 v14, s9, v35
	v_cmp_lt_i32_e32 vcc, -1, v35
	v_add_u32_e32 v20, 0x800, v178
	v_ashrrev_i32_e32 v36, 6, v20
	v_cndmask_b32_e32 v14, 0, v14, vcc
	v_add_u32_e32 v12, s12, v12
	v_add_u32_e32 v14, s12, v14
	v_add_u32_e32 v37, s8, v36
	v_add_u32_e32 v26, 0xa00, v178
	v_mad_u64_u32 v[12:13], s[6:7], v12, s66, v[24:25]
	v_mad_u64_u32 v[16:17], s[6:7], v14, s66, v[24:25]
	v_min_i32_e32 v20, s9, v37
	v_cmp_lt_i32_e32 vcc, -1, v37
	v_ashrrev_i32_e32 v38, 6, v26
	global_load_dwordx4 v[12:15], v[12:13], off
	s_nop 0
	global_load_dwordx4 v[16:19], v[16:17], off
	v_cndmask_b32_e32 v20, 0, v20, vcc
	v_add_u32_e32 v39, s8, v38
	v_add_u32_e32 v20, s12, v20
	v_min_i32_e32 v26, s9, v39
	v_cmp_lt_i32_e32 vcc, -1, v39
	v_mad_u64_u32 v[20:21], s[6:7], v20, s66, v[24:25]
	s_nop 0
	v_cndmask_b32_e32 v26, 0, v26, vcc
	global_load_dwordx4 v[20:23], v[20:21], off
	v_add_u32_e32 v26, s12, v26
	v_mad_u64_u32 v[24:25], s[6:7], v26, s66, v[24:25]
	global_load_dwordx4 v[24:27], v[24:25], off
	v_cmp_gt_u32_e32 vcc, s11, v29
	v_mul_lo_u32 v28, v28, s71
	v_add3_u32 v28, 0, v28, v2
	s_mul_i32 s6, s43, 0x8200
	s_mov_b32 s14, 0
	s_waitcnt vmcnt(5)
	v_cndmask_b32_e32 v7, 0, v7, vcc
	v_cndmask_b32_e32 v6, 0, v6, vcc
	v_cndmask_b32_e32 v5, 0, v5, vcc
	v_cndmask_b32_e32 v4, 0, v4, vcc
	v_cmp_gt_u32_e32 vcc, s11, v31
	ds_write_b128 v28, v[4:7]
	v_mul_lo_u32 v4, v30, s71
	s_waitcnt vmcnt(4)
	v_cndmask_b32_e32 v11, 0, v11, vcc
	v_cndmask_b32_e32 v10, 0, v10, vcc
	v_cndmask_b32_e32 v9, 0, v9, vcc
	v_cndmask_b32_e32 v8, 0, v8, vcc
	v_add3_u32 v4, 0, v4, v2
	v_cmp_gt_u32_e32 vcc, s11, v33
	ds_write_b128 v4, v[8:11]
	v_mul_lo_u32 v4, v32, s71
	v_add3_u32 v4, 0, v4, v2
	s_waitcnt vmcnt(3)
	v_cndmask_b32_e32 v15, 0, v15, vcc
	v_cndmask_b32_e32 v14, 0, v14, vcc
	v_cndmask_b32_e32 v13, 0, v13, vcc
	v_cndmask_b32_e32 v12, 0, v12, vcc
	v_cmp_gt_u32_e32 vcc, s11, v35
	ds_write_b128 v4, v[12:15]
	v_mul_lo_u32 v4, v34, s71
	s_waitcnt vmcnt(2)
	v_cndmask_b32_e32 v19, 0, v19, vcc
	v_cndmask_b32_e32 v18, 0, v18, vcc
	v_cndmask_b32_e32 v17, 0, v17, vcc
	v_cndmask_b32_e32 v16, 0, v16, vcc
	v_add3_u32 v4, 0, v4, v2
	v_cmp_gt_u32_e32 vcc, s11, v37
	ds_write_b128 v4, v[16:19]
	v_mul_lo_u32 v4, v36, s71
	s_waitcnt vmcnt(1)
	v_cndmask_b32_e32 v23, 0, v23, vcc
	v_cndmask_b32_e32 v22, 0, v22, vcc
	v_cndmask_b32_e32 v21, 0, v21, vcc
	v_cndmask_b32_e32 v20, 0, v20, vcc
	v_add3_u32 v4, 0, v4, v2
	v_cmp_gt_u32_e32 vcc, s11, v39
	ds_write_b128 v4, v[20:23]
	v_mul_lo_u32 v4, v38, s71
	s_waitcnt vmcnt(0)
	v_cndmask_b32_e32 v27, 0, v27, vcc
	v_cndmask_b32_e32 v26, 0, v26, vcc
	v_cndmask_b32_e32 v25, 0, v25, vcc
	v_cndmask_b32_e32 v24, 0, v24, vcc
	v_add3_u32 v2, 0, v4, v2
	ds_write_b128 v2, v[24:27]
	v_lshrrev_b32_e32 v2, 4, v162
	v_lshlrev_b32_e64 v5, v2, 1
	v_ashrrev_i32_e32 v2, 4, v178
	v_lshlrev_b32_e32 v4, 4, v162
	v_and_b32_e32 v16, -4, v2
	v_add_u32_e32 v2, 0, v4
	v_subrev_u32_e32 v4, s6, v4
	v_readlane_b32 s6, v242, 9
	s_waitcnt lgkmcnt(0)
	s_barrier
	v_add_u32_e32 v4, s6, v4
	s_lshl_b32 s6, s43, 5
	s_addk_i32 s6, 0xba00
	v_add_u32_e32 v6, s6, v16
	v_subrev_u32_e32 v6, s12, v6
	v_sub_u32_e32 v17, v6, v5
	s_branch .LBB0_480

; __device__ __forceinline__ void gmlp_unit(Ctx& C, int l, int uidx) {
;     ...
;     const int gl = C.wave >> 1, ph = C.wave & 1, g = 4 * hf + gl, r32 = C.lane & 31, h = C.lane >> 5;
;     bf16x8 Wf[2][8]; u32x2 upre[2][2][4];
;     { const bf16* wsb = WSP(bf16, WS_GWSB) + ((size_t)(l * 8 + g) * 128 + 64 * ph + r32) * 128 + 8 * h;
; #pragma unroll
;       for (int pb = 0; pb < 2; ++pb)
; #pragma unroll
;           for (int s = 0; s < 8; ++s) Wf[pb][s] = *(const bf16x8*)(wsb + (size_t)(32 * pb) * 128 + 16 * s);
; #pragma unroll
;       for (int pb = 0; pb < 2; ++pb) { const bf16* up = Z + (size_t)(row0 + 64 * ph + 32 * pb + r32) * INW + 2816 + 64 * g + 4 * h;
; #pragma unroll
;           for (int cb = 0; cb < 2; ++cb)
; #pragma unroll
;               for (int rg = 0; rg < 4; ++rg) upre[pb][cb][rg] = *(const u32x2*)(up + 32 * cb + 8 * rg); } }
;     __syncthreads();
;     {
;         const int tok = C.tid >> 2, part = C.tid & 3;
;         const bf16* zp = Z + (size_t)(row0 + tok) * INW + 3328 + 128 * part;
;         const bf16* zq = Z + (size_t)(row0 + tok) * INW + 3328 + 256 * hf + 64 * part;
;         u32x4 r1[16], r2[8];
; #pragma unroll
;         for (int c8 = 0; c8 < 16; ++c8) r1[c8] = *(const u32x4*)(zp + 8 * c8);
; #pragma unroll
;         for (int c8 = 0; c8 < 8; ++c8) r2[c8] = *(const u32x4*)(zq + 8 * c8);
.LBB0_495:
	s_andn2_b64 vcc, exec, s[6:7]
	s_cbranch_vccnz .LBB0_497
	s_and_b32 s6, s43, 1
	s_ashr_i32 s19, s51, 7
	s_lshl_b32 s8, s6, 2
	s_add_i32 s14, s19, s8
	s_ashr_i32 s15, s14, 31
	s_lshl_b64 s[8:9], s[14:15], 7
	s_and_b32 s15, s51, 64
	v_and_b32_e32 v159, 31, v178
	s_or_b32 s8, s8, s15
	v_or_b32_e32 v4, s8, v159
	v_mov_b32_e32 v5, s9
	v_lshrrev_b32_e32 v6, 5, v162
	v_lshlrev_b64 v[4:5], 8, v[4:5]
	v_lshl_add_u64 v[4:5], s[54:55], 0, v[4:5]
	v_lshlrev_b32_e32 v156, 4, v6
	v_mov_b32_e32 v157, v3
	v_lshl_add_u64 v[8:9], v[4:5], 0, v[156:157]
	s_mov_b64 s[8:9], 0x380000
	s_lshl_b32 s7, s43, 6
	v_lshl_add_u64 v[10:11], v[8:9], 0, s[8:9]
	s_mov_b32 s8, 0x380000
	s_addk_i32 s7, 0x3c00
	v_add_co_u32_e32 v4, vcc, s8, v8
	s_mov_b32 s8, 0x382000
	s_nop 0
	v_addc_co_u32_e32 v5, vcc, 0, v9, vcc
	s_and_b32 s18, s7, 0x7f80
	v_add_co_u32_e32 v12, vcc, s8, v8
	s_add_u32 s8, s54, 0x36000000
	s_nop 0
	v_addc_co_u32_e32 v13, vcc, 0, v9, vcc
	s_addc_u32 s9, s55, 0
	s_or_b32 s7, s18, s15
	v_lshlrev_b32_e32 v2, 3, v6
	global_load_dwordx4 v[116:119], v[10:11], off offset:32
	global_load_dwordx4 v[104:107], v[10:11], off offset:64
	global_load_dwordx4 v[100:103], v[10:11], off offset:96
	global_load_dwordx4 v[88:91], v[10:11], off offset:128
	global_load_dwordx4 v[84:87], v[10:11], off offset:160
	global_load_dwordx4 v[76:79], v[10:11], off offset:192
	s_nop 0
	global_load_dwordx4 v[4:7], v[4:5], off
	s_nop 0
	global_load_dwordx4 v[72:75], v[10:11], off offset:224
	s_nop 0
	global_load_dwordx4 v[8:11], v[12:13], off
	global_load_dwordx4 v[120:123], v[12:13], off offset:32
	global_load_dwordx4 v[112:115], v[12:13], off offset:64
	global_load_dwordx4 v[108:111], v[12:13], off offset:96
	global_load_dwordx4 v[96:99], v[12:13], off offset:128
	global_load_dwordx4 v[92:95], v[12:13], off offset:160
	global_load_dwordx4 v[80:83], v[12:13], off offset:192
	global_load_dwordx4 v[68:71], v[12:13], off offset:224
	v_or_b32_e32 v12, s7, v159
	s_lshl_b32 s10, s14, 6
	v_mul_u32_u24_e32 v12, 0xf00, v12
	s_ashr_i32 s11, s10, 31
	v_lshlrev_b32_e32 v12, 1, v12
	v_mov_b32_e32 v13, v3
	v_lshl_add_u64 v[12:13], s[8:9], 0, v[12:13]
	s_lshl_b64 s[12:13], s[10:11], 1
	v_lshl_add_u64 v[12:13], v[12:13], 0, s[12:13]
	v_lshl_add_u64 v[12:13], v[12:13], 0, v[2:3]
	s_movk_i32 s7, 0x1000
	s_mov_b64 s[10:11], 0x1600
	v_add_co_u32_e32 v16, vcc, s7, v12
	v_lshl_add_u64 v[14:15], v[12:13], 0, s[10:11]
	s_nop 0
	v_addc_co_u32_e32 v17, vcc, 0, v13, vcc
	s_mov_b64 s[10:11], 0x3d600
	s_mov_b32 s7, 0x3d000
	global_load_dwordx2 v[152:153], v[14:15], off offset:16
	global_load_dwordx2 v[150:151], v[14:15], off offset:32
	global_load_dwordx2 v[148:149], v[14:15], off offset:48
	global_load_dwordx2 v[146:147], v[14:15], off offset:64
	global_load_dwordx2 v[154:155], v[16:17], off offset:1536
	global_load_dwordx2 v[144:145], v[14:15], off offset:80
	global_load_dwordx2 v[142:143], v[14:15], off offset:96
	global_load_dwordx2 v[140:141], v[14:15], off offset:112
	v_lshl_add_u64 v[14:15], v[12:13], 0, s[10:11]
	v_add_co_u32_e32 v12, vcc, s7, v12
	v_ashrrev_i32_e32 v62, 2, v178
	s_nop 0
	v_addc_co_u32_e32 v13, vcc, 0, v13, vcc
	global_load_dwordx2 v[136:137], v[14:15], off offset:16
	global_load_dwordx2 v[134:135], v[14:15], off offset:32
	global_load_dwordx2 v[132:133], v[14:15], off offset:48
	global_load_dwordx2 v[130:131], v[14:15], off offset:64
	global_load_dwordx2 v[138:139], v[12:13], off offset:1536
	global_load_dwordx2 v[128:129], v[14:15], off offset:80
	global_load_dwordx2 v[126:127], v[14:15], off offset:96
	global_load_dwordx2 v[124:125], v[14:15], off offset:112
	v_add_u32_e32 v14, s18, v62
	v_mov_b64_e32 v[12:13], s[8:9]
	v_mad_i64_i32 v[12:13], s[8:9], v14, s66, v[12:13]
	v_and_b32_e32 v164, 3, v178
	s_mov_b64 s[8:9], 0x1a00
	v_lshl_add_u64 v[16:17], v[12:13], 0, s[8:9]
	v_lshlrev_b32_e32 v160, 8, v164
	v_mov_b32_e32 v161, v3
	v_lshl_add_u64 v[18:19], v[16:17], 0, v[160:161]
	s_waitcnt lgkmcnt(0)
	s_barrier
	global_load_dwordx4 v[56:59], v[18:19], off
	global_load_dwordx4 v[64:67], v[18:19], off offset:16
	global_load_dwordx4 v[180:183], v[18:19], off offset:32
	global_load_dwordx4 v[184:187], v[18:19], off offset:48
	global_load_dwordx4 v[52:55], v[18:19], off offset:112
	global_load_dwordx4 v[188:191], v[18:19], off offset:96
	global_load_dwordx4 v[192:195], v[18:19], off offset:80
	global_load_dwordx4 v[196:199], v[18:19], off offset:64
	global_load_dwordx4 v[36:39], v[18:19], off offset:176
	global_load_dwordx4 v[40:43], v[18:19], off offset:160
	global_load_dwordx4 v[44:47], v[18:19], off offset:144
	global_load_dwordx4 v[48:51], v[18:19], off offset:128
	global_load_dwordx4 v[12:15], v[18:19], off offset:240
	global_load_dwordx4 v[20:23], v[18:19], off offset:224
	global_load_dwordx4 v[24:27], v[18:19], off offset:208
	global_load_dwordx4 v[32:35], v[18:19], off offset:192
	s_lshl_b32 s38, s6, 9
	v_lshlrev_b32_e32 v28, 7, v164
	v_mov_b32_e32 v29, v3
	v_lshl_add_u64 v[16:17], v[16:17], 0, s[38:39]
	v_lshl_add_u64 v[60:61], v[16:17], 0, v[28:29]
	global_load_dwordx4 v[16:19], v[60:61], off offset:16
	global_load_dwordx4 v[28:31], v[60:61], off
	s_load_dwordx4 s[8:11], s[56:57], 0xb0
	s_load_dwordx2 s[58:59], s[56:57], 0xc8
	s_lshl_b32 s6, s6, 10
	v_mul_u32_u24_e32 v164, 0x4400, v164
	s_waitcnt lgkmcnt(0)
	s_add_u32 s8, s8, s6
	s_addc_u32 s9, s9, 0
	s_add_u32 s10, s10, s6
	s_addc_u32 s11, s11, 0
	s_mov_b32 s6, 0x3b000000
	s_waitcnt vmcnt(17)
; template <int CTRL> __device__ __forceinline__ float dpp_f(float x) { return __int_as_float(__builtin_amdgcn_update_dpp(0, __float_as_int(x), CTRL, 0xF, 0xF, true)); }
; __device__ __forceinline__ void cvt8(const u32x4 r, float (&f)[8]) { f[0] = bflo(r.x); f[1] = bfhi(r.x); f[2] = bflo(r.y); f[3] = bfhi(r.y); f[4] = bflo(r.z); f[5] = bfhi(r.z); f[6] = bflo(r.w); f[7] = bfhi(r.w); }
; __device__ __forceinline__ void gmlp_unit(Ctx& C, int l, int uidx) {
;     ...
;         float s = 0.f, q = 0.f;
; #pragma unroll
;         for (int c8 = 0; c8 < 16; ++c8) { float f[8]; cvt8(r1[c8], f);
; #pragma unroll
;             for (int j = 0; j < 8; ++j) { s += f[j]; q += f[j] * f[j]; } }
;         s += dpp_f<DPP_XOR1>(s); s += dpp_f<DPP_XOR2>(s); q += dpp_f<DPP_XOR1>(q); q += dpp_f<DPP_XOR2>(q);
	v_lshlrev_b32_e32 v63, 16, v56
	v_and_b32_e32 v56, 0xffff0000, v56
	v_add_f32_e32 v200, 0, v63
	v_lshlrev_b32_e32 v157, 16, v57
	v_add_f32_e32 v200, v200, v56
	v_mul_f32_e32 v56, v56, v56
	v_and_b32_e32 v57, 0xffff0000, v57
	v_fmac_f32_e32 v56, v63, v63
	v_add_f32_e32 v63, v200, v157
	v_lshlrev_b32_e32 v161, 16, v58
	v_fmac_f32_e32 v56, v157, v157
	v_add_f32_e32 v63, v63, v57
	v_and_b32_e32 v58, 0xffff0000, v58
	v_fmac_f32_e32 v56, v57, v57
	v_add_f32_e32 v57, v63, v161
	v_lshlrev_b32_e32 v179, 16, v59
	v_fmac_f32_e32 v56, v161, v161
	v_add_f32_e32 v57, v57, v58
	v_and_b32_e32 v59, 0xffff0000, v59
	v_fmac_f32_e32 v56, v58, v58
	v_add_f32_e32 v57, v57, v179
	v_fmac_f32_e32 v56, v179, v179
	v_add_f32_e32 v57, v57, v59
	s_waitcnt vmcnt(16)
	v_lshlrev_b32_e32 v58, 16, v64
	v_fmac_f32_e32 v56, v59, v59
	v_and_b32_e32 v59, 0xffff0000, v64
	v_add_f32_e32 v57, v57, v58
	v_lshlrev_b32_e32 v63, 16, v65
	v_fmac_f32_e32 v56, v58, v58
	v_add_f32_e32 v57, v57, v59
	v_and_b32_e32 v64, 0xffff0000, v65
	v_fmac_f32_e32 v56, v59, v59
	v_add_f32_e32 v57, v57, v63
	v_lshlrev_b32_e32 v65, 16, v66
	v_fmac_f32_e32 v56, v63, v63
	v_add_f32_e32 v57, v57, v64
	v_and_b32_e32 v66, 0xffff0000, v66
	v_fmac_f32_e32 v56, v64, v64
	v_add_f32_e32 v57, v57, v65
	v_lshlrev_b32_e32 v157, 16, v67
	v_fmac_f32_e32 v56, v65, v65
	v_add_f32_e32 v57, v57, v66
	v_and_b32_e32 v67, 0xffff0000, v67
	v_fmac_f32_e32 v56, v66, v66
	v_add_f32_e32 v57, v57, v157
	v_fmac_f32_e32 v56, v157, v157
	v_add_f32_e32 v57, v57, v67
	s_waitcnt vmcnt(15)
	v_lshlrev_b32_e32 v58, 16, v180
	v_fmac_f32_e32 v56, v67, v67
	v_and_b32_e32 v59, 0xffff0000, v180
	v_add_f32_e32 v57, v57, v58
	v_lshlrev_b32_e32 v63, 16, v181
	v_fmac_f32_e32 v56, v58, v58
	v_add_f32_e32 v57, v57, v59
	v_and_b32_e32 v64, 0xffff0000, v181
	v_fmac_f32_e32 v56, v59, v59
	v_add_f32_e32 v57, v57, v63
	v_lshlrev_b32_e32 v65, 16, v182
	v_fmac_f32_e32 v56, v63, v63
	v_add_f32_e32 v57, v57, v64
	v_and_b32_e32 v66, 0xffff0000, v182
	v_fmac_f32_e32 v56, v64, v64
	v_add_f32_e32 v57, v57, v65
	v_lshlrev_b32_e32 v67, 16, v183
	v_fmac_f32_e32 v56, v65, v65
	v_add_f32_e32 v57, v57, v66
	v_and_b32_e32 v157, 0xffff0000, v183
	v_fmac_f32_e32 v56, v66, v66
	v_add_f32_e32 v57, v57, v67
	v_fmac_f32_e32 v56, v67, v67
	v_add_f32_e32 v57, v57, v157
	s_waitcnt vmcnt(14)
	v_lshlrev_b32_e32 v58, 16, v184
	v_fmac_f32_e32 v56, v157, v157
	v_and_b32_e32 v59, 0xffff0000, v184
	v_add_f32_e32 v57, v57, v58
	v_lshlrev_b32_e32 v63, 16, v185
	v_fmac_f32_e32 v56, v58, v58
	v_add_f32_e32 v57, v57, v59
	v_and_b32_e32 v64, 0xffff0000, v185
	v_fmac_f32_e32 v56, v59, v59
	v_add_f32_e32 v57, v57, v63
	v_lshlrev_b32_e32 v65, 16, v186
	v_fmac_f32_e32 v56, v63, v63
	v_add_f32_e32 v57, v57, v64
	v_and_b32_e32 v66, 0xffff0000, v186
	v_fmac_f32_e32 v56, v64, v64
	v_add_f32_e32 v57, v57, v65
	v_lshlrev_b32_e32 v67, 16, v187
	v_fmac_f32_e32 v56, v65, v65
	v_add_f32_e32 v57, v57, v66
	v_and_b32_e32 v157, 0xffff0000, v187
	v_fmac_f32_e32 v56, v66, v66
	v_add_f32_e32 v57, v57, v67
	v_fmac_f32_e32 v56, v67, v67
	v_add_f32_e32 v57, v57, v157
	s_waitcnt vmcnt(10)
	v_lshlrev_b32_e32 v58, 16, v196
	v_fmac_f32_e32 v56, v157, v157
	v_and_b32_e32 v59, 0xffff0000, v196
	v_add_f32_e32 v57, v57, v58
	v_lshlrev_b32_e32 v63, 16, v197
	v_fmac_f32_e32 v56, v58, v58
	v_add_f32_e32 v57, v57, v59
	v_and_b32_e32 v64, 0xffff0000, v197
	v_fmac_f32_e32 v56, v59, v59
	v_add_f32_e32 v57, v57, v63
	v_lshlrev_b32_e32 v65, 16, v198
	v_fmac_f32_e32 v56, v63, v63
	v_add_f32_e32 v57, v57, v64
	v_and_b32_e32 v66, 0xffff0000, v198
	v_fmac_f32_e32 v56, v64, v64
	v_add_f32_e32 v57, v57, v65
	v_lshlrev_b32_e32 v67, 16, v199
	v_fmac_f32_e32 v56, v65, v65
	v_add_f32_e32 v57, v57, v66
	v_and_b32_e32 v157, 0xffff0000, v199
	v_fmac_f32_e32 v56, v66, v66
	v_add_f32_e32 v57, v57, v67
	v_fmac_f32_e32 v56, v67, v67
	v_add_f32_e32 v57, v57, v157
	v_lshlrev_b32_e32 v58, 16, v192
	v_fmac_f32_e32 v56, v157, v157
	v_and_b32_e32 v59, 0xffff0000, v192
	v_add_f32_e32 v57, v57, v58
	v_lshlrev_b32_e32 v63, 16, v193
	v_fmac_f32_e32 v56, v58, v58
	v_add_f32_e32 v57, v57, v59
	v_and_b32_e32 v64, 0xffff0000, v193
	v_fmac_f32_e32 v56, v59, v59
	v_add_f32_e32 v57, v57, v63
	v_lshlrev_b32_e32 v65, 16, v194
	v_fmac_f32_e32 v56, v63, v63
	v_add_f32_e32 v57, v57, v64
	v_and_b32_e32 v66, 0xffff0000, v194
	v_fmac_f32_e32 v56, v64, v64
	v_add_f32_e32 v57, v57, v65
	v_lshlrev_b32_e32 v67, 16, v195
	v_fmac_f32_e32 v56, v65, v65
	v_add_f32_e32 v57, v57, v66
	v_and_b32_e32 v157, 0xffff0000, v195
	v_fmac_f32_e32 v56, v66, v66
	v_add_f32_e32 v57, v57, v67
	v_fmac_f32_e32 v56, v67, v67
	v_add_f32_e32 v57, v57, v157
	v_lshlrev_b32_e32 v58, 16, v188
	v_fmac_f32_e32 v56, v157, v157
	v_and_b32_e32 v59, 0xffff0000, v188
	v_add_f32_e32 v57, v57, v58
	v_lshlrev_b32_e32 v63, 16, v189
	v_fmac_f32_e32 v56, v58, v58
	v_add_f32_e32 v57, v57, v59
	v_and_b32_e32 v64, 0xffff0000, v189
	v_fmac_f32_e32 v56, v59, v59
	v_add_f32_e32 v57, v57, v63
	v_lshlrev_b32_e32 v65, 16, v190
	v_fmac_f32_e32 v56, v63, v63
	v_add_f32_e32 v57, v57, v64
	v_and_b32_e32 v66, 0xffff0000, v190
	v_fmac_f32_e32 v56, v64, v64
	v_add_f32_e32 v57, v57, v65
	v_lshlrev_b32_e32 v67, 16, v191
	v_fmac_f32_e32 v56, v65, v65
	v_add_f32_e32 v57, v57, v66
	v_and_b32_e32 v157, 0xffff0000, v191
	v_fmac_f32_e32 v56, v66, v66
	v_add_f32_e32 v57, v57, v67
	v_fmac_f32_e32 v56, v67, v67
	v_add_f32_e32 v57, v57, v157
	v_lshlrev_b32_e32 v58, 16, v52
	v_fmac_f32_e32 v56, v157, v157
	v_and_b32_e32 v52, 0xffff0000, v52
	v_add_f32_e32 v57, v57, v58
	v_lshlrev_b32_e32 v59, 16, v53
	v_fmac_f32_e32 v56, v58, v58
	v_add_f32_e32 v57, v57, v52
	v_and_b32_e32 v53, 0xffff0000, v53
	v_fmac_f32_e32 v56, v52, v52
	v_add_f32_e32 v52, v57, v59
	v_lshlrev_b32_e32 v63, 16, v54
	v_fmac_f32_e32 v56, v59, v59
	v_add_f32_e32 v52, v52, v53
	v_and_b32_e32 v54, 0xffff0000, v54
	v_fmac_f32_e32 v56, v53, v53
	v_add_f32_e32 v52, v52, v63
	v_lshlrev_b32_e32 v64, 16, v55
	v_fmac_f32_e32 v56, v63, v63
	v_add_f32_e32 v52, v52, v54
	v_and_b32_e32 v55, 0xffff0000, v55
	v_fmac_f32_e32 v56, v54, v54
	v_add_f32_e32 v52, v52, v64
	v_fmac_f32_e32 v56, v64, v64
	v_add_f32_e32 v52, v52, v55
	s_waitcnt vmcnt(6)
; template <int CTRL> __device__ __forceinline__ float dpp_f(float x) { return __int_as_float(__builtin_amdgcn_update_dpp(0, __float_as_int(x), CTRL, 0xF, 0xF, true)); }
; __device__ __forceinline__ void cvt8(const u32x4 r, float (&f)[8]) { f[0] = bflo(r.x); f[1] = bfhi(r.x); f[2] = bflo(r.y); f[3] = bfhi(r.y); f[4] = bflo(r.z); f[5] = bfhi(r.z); f[6] = bflo(r.w); f[7] = bfhi(r.w); }
; __device__ __forceinline__ void gmlp_unit(Ctx& C, int l, int uidx) {
;     ...
;         for (int c8 = 0; c8 < 16; ++c8) { float f[8]; cvt8(r1[c8], f);
; #pragma unroll
;             for (int j = 0; j < 8; ++j) { s += f[j]; q += f[j] * f[j]; } }
;         s += dpp_f<DPP_XOR1>(s); s += dpp_f<DPP_XOR2>(s); q += dpp_f<DPP_XOR1>(q); q += dpp_f<DPP_XOR2>(q);
;         const float mean = s * (1.0f / 512.0f); const float var = fmaxf(q * (1.0f / 512.0f) - mean * mean, 0.f); const float rstd = 1.0f / sqrtf(var + LN_EPS);
;         const float* lg = INP(I_GLG) + l * 512 + 256 * hf + 64 * part; const float* lb = INP(I_GLB) + l * 512 + 256 * hf + 64 * part;
; #pragma unroll
;         for (int c8 = 0; c8 < 8; ++c8) { float f[8]; cvt8(r2[c8], f);
;             const f32x4 g0 = *(const f32x4*)(lg + 8 * c8), g1 = *(const f32x4*)(lg + 8 * c8 + 4), b0 = *(const f32x4*)(lb + 8 * c8), b1 = *(const f32x4*)(lb + 8 * c8 + 4);
	v_lshlrev_b32_e32 v53, 16, v48
	v_fmac_f32_e32 v56, v55, v55
	v_and_b32_e32 v48, 0xffff0000, v48
	v_add_f32_e32 v52, v52, v53
	v_lshlrev_b32_e32 v54, 16, v49
	v_fmac_f32_e32 v56, v53, v53
	v_add_f32_e32 v52, v52, v48
	v_and_b32_e32 v49, 0xffff0000, v49
	v_fmac_f32_e32 v56, v48, v48
	v_add_f32_e32 v48, v52, v54
	v_lshlrev_b32_e32 v55, 16, v50
	v_fmac_f32_e32 v56, v54, v54
	v_add_f32_e32 v48, v48, v49
	v_and_b32_e32 v50, 0xffff0000, v50
	v_fmac_f32_e32 v56, v49, v49
	v_add_f32_e32 v48, v48, v55
	v_lshlrev_b32_e32 v57, 16, v51
	v_fmac_f32_e32 v56, v55, v55
	v_add_f32_e32 v48, v48, v50
	v_and_b32_e32 v51, 0xffff0000, v51
	v_fmac_f32_e32 v56, v50, v50
	v_add_f32_e32 v48, v48, v57
	v_fmac_f32_e32 v56, v57, v57
	v_add_f32_e32 v48, v48, v51
	v_lshlrev_b32_e32 v49, 16, v44
	v_fmac_f32_e32 v56, v51, v51
	v_and_b32_e32 v44, 0xffff0000, v44
	v_add_f32_e32 v48, v48, v49
	v_lshlrev_b32_e32 v50, 16, v45
	v_fmac_f32_e32 v56, v49, v49
	v_add_f32_e32 v48, v48, v44
	v_and_b32_e32 v45, 0xffff0000, v45
	v_fmac_f32_e32 v56, v44, v44
	v_add_f32_e32 v44, v48, v50
	v_lshlrev_b32_e32 v51, 16, v46
	v_fmac_f32_e32 v56, v50, v50
	v_add_f32_e32 v44, v44, v45
	v_and_b32_e32 v46, 0xffff0000, v46
	v_fmac_f32_e32 v56, v45, v45
	v_add_f32_e32 v44, v44, v51
	v_lshlrev_b32_e32 v52, 16, v47
	v_fmac_f32_e32 v56, v51, v51
	v_add_f32_e32 v44, v44, v46
	v_and_b32_e32 v47, 0xffff0000, v47
	v_fmac_f32_e32 v56, v46, v46
	v_add_f32_e32 v44, v44, v52
	v_fmac_f32_e32 v56, v52, v52
	v_add_f32_e32 v44, v44, v47
	v_lshlrev_b32_e32 v45, 16, v40
	v_fmac_f32_e32 v56, v47, v47
	v_and_b32_e32 v40, 0xffff0000, v40
	v_add_f32_e32 v44, v44, v45
	v_lshlrev_b32_e32 v46, 16, v41
	v_fmac_f32_e32 v56, v45, v45
	v_add_f32_e32 v44, v44, v40
	v_and_b32_e32 v41, 0xffff0000, v41
	v_fmac_f32_e32 v56, v40, v40
	v_add_f32_e32 v40, v44, v46
	v_lshlrev_b32_e32 v47, 16, v42
	v_fmac_f32_e32 v56, v46, v46
	v_add_f32_e32 v40, v40, v41
	v_and_b32_e32 v42, 0xffff0000, v42
	v_fmac_f32_e32 v56, v41, v41
	v_add_f32_e32 v40, v40, v47
	v_lshlrev_b32_e32 v48, 16, v43
	v_fmac_f32_e32 v56, v47, v47
	v_add_f32_e32 v40, v40, v42
	v_and_b32_e32 v43, 0xffff0000, v43
	v_fmac_f32_e32 v56, v42, v42
	v_add_f32_e32 v40, v40, v48
	v_fmac_f32_e32 v56, v48, v48
	v_add_f32_e32 v40, v40, v43
	v_lshlrev_b32_e32 v41, 16, v36
	v_fmac_f32_e32 v56, v43, v43
	v_and_b32_e32 v36, 0xffff0000, v36
	v_add_f32_e32 v40, v40, v41
	v_lshlrev_b32_e32 v42, 16, v37
	v_fmac_f32_e32 v56, v41, v41
	v_add_f32_e32 v40, v40, v36
	v_and_b32_e32 v37, 0xffff0000, v37
	v_fmac_f32_e32 v56, v36, v36
	v_add_f32_e32 v36, v40, v42
	v_lshlrev_b32_e32 v43, 16, v38
	v_fmac_f32_e32 v56, v42, v42
	v_add_f32_e32 v36, v36, v37
	v_and_b32_e32 v38, 0xffff0000, v38
	v_fmac_f32_e32 v56, v37, v37
	v_add_f32_e32 v36, v36, v43
	v_lshlrev_b32_e32 v44, 16, v39
	v_fmac_f32_e32 v56, v43, v43
	v_add_f32_e32 v36, v36, v38
	v_and_b32_e32 v39, 0xffff0000, v39
	v_fmac_f32_e32 v56, v38, v38
	v_add_f32_e32 v36, v36, v44
	v_fmac_f32_e32 v56, v44, v44
	v_add_f32_e32 v36, v36, v39
	s_waitcnt vmcnt(2)
	v_lshlrev_b32_e32 v37, 16, v32
	v_fmac_f32_e32 v56, v39, v39
	v_and_b32_e32 v32, 0xffff0000, v32
	v_add_f32_e32 v36, v36, v37
	v_lshlrev_b32_e32 v38, 16, v33
	v_fmac_f32_e32 v56, v37, v37
	v_add_f32_e32 v36, v36, v32
	v_and_b32_e32 v33, 0xffff0000, v33
	v_fmac_f32_e32 v56, v32, v32
	v_add_f32_e32 v32, v36, v38
	v_lshlrev_b32_e32 v39, 16, v34
	v_fmac_f32_e32 v56, v38, v38
	v_add_f32_e32 v32, v32, v33
	v_and_b32_e32 v34, 0xffff0000, v34
	v_fmac_f32_e32 v56, v33, v33
	v_add_f32_e32 v32, v32, v39
	v_lshlrev_b32_e32 v40, 16, v35
	v_fmac_f32_e32 v56, v39, v39
	v_add_f32_e32 v32, v32, v34
	v_and_b32_e32 v35, 0xffff0000, v35
	v_fmac_f32_e32 v56, v34, v34
	v_add_f32_e32 v32, v32, v40
	v_fmac_f32_e32 v56, v40, v40
	v_add_f32_e32 v32, v32, v35
	v_lshlrev_b32_e32 v33, 16, v24
	v_fmac_f32_e32 v56, v35, v35
	v_and_b32_e32 v24, 0xffff0000, v24
	v_add_f32_e32 v32, v32, v33
	v_lshlrev_b32_e32 v34, 16, v25
	v_fmac_f32_e32 v56, v33, v33
	v_add_f32_e32 v32, v32, v24
	v_and_b32_e32 v25, 0xffff0000, v25
	v_fmac_f32_e32 v56, v24, v24
	v_add_f32_e32 v24, v32, v34
	v_lshlrev_b32_e32 v35, 16, v26
	v_fmac_f32_e32 v56, v34, v34
	v_add_f32_e32 v24, v24, v25
	v_and_b32_e32 v26, 0xffff0000, v26
	v_fmac_f32_e32 v56, v25, v25
	v_add_f32_e32 v24, v24, v35
	v_lshlrev_b32_e32 v36, 16, v27
	v_fmac_f32_e32 v56, v35, v35
	v_add_f32_e32 v24, v24, v26
	v_and_b32_e32 v27, 0xffff0000, v27
	v_fmac_f32_e32 v56, v26, v26
	v_add_f32_e32 v24, v24, v36
	v_fmac_f32_e32 v56, v36, v36
	v_add_f32_e32 v24, v24, v27
	v_lshlrev_b32_e32 v25, 16, v20
	v_fmac_f32_e32 v56, v27, v27
	v_and_b32_e32 v20, 0xffff0000, v20
	v_add_f32_e32 v24, v24, v25
	v_lshlrev_b32_e32 v26, 16, v21
	v_fmac_f32_e32 v56, v25, v25
	v_add_f32_e32 v24, v24, v20
	v_and_b32_e32 v21, 0xffff0000, v21
	v_fmac_f32_e32 v56, v20, v20
	v_add_f32_e32 v20, v24, v26
	v_lshlrev_b32_e32 v27, 16, v22
	v_fmac_f32_e32 v56, v26, v26
	v_add_f32_e32 v20, v20, v21
	v_and_b32_e32 v22, 0xffff0000, v22
	v_fmac_f32_e32 v56, v21, v21
	v_add_f32_e32 v20, v20, v27
	v_lshlrev_b32_e32 v32, 16, v23
	v_fmac_f32_e32 v56, v27, v27
	v_add_f32_e32 v20, v20, v22
	v_and_b32_e32 v23, 0xffff0000, v23
	v_fmac_f32_e32 v56, v22, v22
	v_add_f32_e32 v20, v20, v32
	v_fmac_f32_e32 v56, v32, v32
	v_add_f32_e32 v20, v20, v23
	v_lshlrev_b32_e32 v21, 16, v12
	v_fmac_f32_e32 v56, v23, v23
	v_and_b32_e32 v12, 0xffff0000, v12
	v_add_f32_e32 v20, v20, v21
	v_lshlrev_b32_e32 v22, 16, v13
	v_fmac_f32_e32 v56, v21, v21
	v_add_f32_e32 v20, v20, v12
	v_and_b32_e32 v13, 0xffff0000, v13
	v_fmac_f32_e32 v56, v12, v12
	v_add_f32_e32 v12, v20, v22
	v_lshlrev_b32_e32 v23, 16, v14
	v_add_f32_e32 v12, v12, v13
	v_and_b32_e32 v14, 0xffff0000, v14
	v_fmac_f32_e32 v56, v22, v22
	v_add_f32_e32 v12, v12, v23
	v_lshlrev_b32_e32 v24, 16, v15
	v_fmac_f32_e32 v56, v13, v13
	v_add_f32_e32 v12, v12, v14
	v_and_b32_e32 v15, 0xffff0000, v15
	v_fmac_f32_e32 v56, v23, v23
	v_add_f32_e32 v12, v12, v24
	v_fmac_f32_e32 v56, v14, v14
	v_add_f32_e32 v12, v12, v15
	global_load_dwordx4 v[180:183], v160, s[8:9]
	global_load_dwordx4 v[184:187], v160, s[10:11]
	v_fmac_f32_e32 v56, v24, v24
	v_add_f32_dpp v12, v12, v12 quad_perm:[1,0,3,2] row_mask:0xf bank_mask:0xf bound_ctrl:1
	v_fmac_f32_e32 v56, v15, v15
	global_load_dwordx4 v[44:47], v160, s[8:9] offset:16
	global_load_dwordx4 v[48:51], v160, s[10:11] offset:16
	v_add_f32_dpp v157, v12, v12 quad_perm:[2,3,0,1] row_mask:0xf bank_mask:0xf bound_ctrl:1
	v_add_f32_dpp v12, v56, v56 quad_perm:[1,0,3,2] row_mask:0xf bank_mask:0xf bound_ctrl:1
	v_mul_f32_e32 v13, 0x3b000000, v157
	v_mul_f32_e32 v13, v13, v13
	v_add_f32_dpp v12, v12, v12 quad_perm:[2,3,0,1] row_mask:0xf bank_mask:0xf bound_ctrl:1
	v_fma_f32 v12, v12, s6, -v13
	v_max_f32_e32 v12, 0, v12
	v_add_f32_e32 v12, 0x358637bd, v12
	s_mov_b32 s6, 0xf800000
	v_mul_f32_e32 v13, 0x4f800000, v12
	v_cmp_gt_f32_e32 vcc, s6, v12
	v_lshlrev_b32_e32 v179, 1, v62
	s_waitcnt vmcnt(4)
; #define LAS __attribute__((address_space(3)))
; __device__ __forceinline__ unsigned pk2(float lo, float hi) { f32x2 v = {lo, hi}; bf16x2_t b = __builtin_convertvector(v, bf16x2_t); return __builtin_bit_cast(unsigned, b); }
; __device__ __forceinline__ void cvt8(const u32x4 r, float (&f)[8]) { f[0] = bflo(r.x); f[1] = bfhi(r.x); f[2] = bflo(r.y); f[3] = bfhi(r.y); f[4] = bflo(r.z); f[5] = bfhi(r.z); f[6] = bflo(r.w); f[7] = bfhi(r.w); }
; __device__ __forceinline__ void gmlp_unit(Ctx& C, int l, int uidx) {
;     ...
;         const float mean = s * (1.0f / 512.0f); const float var = fmaxf(q * (1.0f / 512.0f) - mean * mean, 0.f); const float rstd = 1.0f / sqrtf(var + LN_EPS);
;         const float* lg = INP(I_GLG) + l * 512 + 256 * hf + 64 * part; const float* lb = INP(I_GLB) + l * 512 + 256 * hf + 64 * part;
; #pragma unroll
;         for (int c8 = 0; c8 < 8; ++c8) { float f[8]; cvt8(r2[c8], f);
;             const f32x4 g0 = *(const f32x4*)(lg + 8 * c8), g1 = *(const f32x4*)(lg + 8 * c8 + 4), b0 = *(const f32x4*)(lb + 8 * c8), b1 = *(const f32x4*)(lb + 8 * c8 + 4);
;             const float gg[8] = {g0[0], g0[1], g0[2], g0[3], g1[0], g1[1], g1[2], g1[3]}, bb[8] = {b0[0], b0[1], b0[2], b0[3], b1[0], b1[1], b1[2], b1[3]};
; #pragma unroll
;             for (int j = 0; j < 8; ++j) { const float vn = (f[j] - mean) * rstd * gg[j] + bb[j];
;                 *(LAS bf16*)(C.lds + (64 * part + 8 * c8 + j) * VS + tok * 2) = (bf16)(pk2(vn, 0.f) & 0xffffu); } }
	v_lshlrev_b32_e32 v188, 16, v28
	v_cndmask_b32_e32 v24, v12, v13, vcc
	v_sqrt_f32_e32 v25, v24
	global_load_dwordx4 v[36:39], v[60:61], off offset:48
	global_load_dwordx4 v[40:43], v[60:61], off offset:32
	global_load_dwordx4 v[12:15], v[60:61], off offset:112
	global_load_dwordx4 v[20:23], v[60:61], off offset:96
	v_and_b32_e32 v28, 0xffff0000, v28
	v_fmac_f32_e32 v28, 0xbb000000, v157
	v_add_u32_e32 v26, -1, v25
	v_fma_f32 v27, -v26, v25, v24
	v_cmp_ge_f32_e64 s[6:7], 0, v27
	v_add_u32_e32 v27, 1, v25
	v_lshlrev_b32_e32 v189, 16, v29
	v_cndmask_b32_e64 v26, v25, v26, s[6:7]
	v_fma_f32 v25, -v27, v25, v24
	v_cmp_lt_f32_e64 s[6:7], 0, v25
	v_add3_u32 v164, 0, v179, v164
	v_fmac_f32_e32 v189, 0xbb000000, v157
	v_cndmask_b32_e64 v25, v26, v27, s[6:7]
	v_mul_f32_e32 v26, 0x37800000, v25
	v_cndmask_b32_e32 v25, v25, v26, vcc
	v_cmp_class_f32_e32 vcc, v24, v163
	v_and_b32_e32 v29, 0xffff0000, v29
	v_fmac_f32_e32 v29, 0xbb000000, v157
	v_cndmask_b32_e32 v63, v25, v24, vcc
	v_div_scale_f32 v64, s[6:7], v63, v63, 1.0
	v_rcp_f32_e32 v65, v64
	global_load_dwordx4 v[52:55], v160, s[8:9] offset:32
	global_load_dwordx4 v[56:59], v160, s[10:11] offset:32
	global_load_dwordx4 v[24:27], v[60:61], off offset:80
	global_load_dwordx4 v[32:35], v[60:61], off offset:64
	v_lshlrev_b32_e32 v190, 16, v30
	v_fmac_f32_e32 v188, 0xbb000000, v157
	v_fma_f32 v60, -v64, v65, 1.0
	v_fmac_f32_e32 v65, v60, v65
	v_div_scale_f32 v60, vcc, 1.0, v63, 1.0
	v_mul_f32_e32 v61, v60, v65
	v_fma_f32 v66, -v64, v61, v60
	v_fmac_f32_e32 v61, v66, v65
	v_fma_f32 v60, -v64, v61, v60
	v_div_fmas_f32 v60, v60, v65, v61
	v_div_fixup_f32 v161, v60, v63, 1.0
	global_load_dwordx4 v[60:63], v160, s[8:9] offset:48
	global_load_dwordx4 v[64:67], v160, s[10:11] offset:48
	v_mul_f32_e32 v28, v28, v161
	v_fmac_f32_e32 v190, 0xbb000000, v157
	v_mul_f32_e32 v188, v188, v161
	v_and_b32_e32 v30, 0xffff0000, v30
	v_fmac_f32_e32 v30, 0xbb000000, v157
	v_lshlrev_b32_e32 v191, 16, v31
	v_fmac_f32_e32 v191, 0xbb000000, v157
	v_and_b32_e32 v31, 0xffff0000, v31
	v_fmac_f32_e32 v31, 0xbb000000, v157
	s_movk_i32 s6, 0x110
	s_waitcnt vmcnt(12)
	v_fma_f32 v28, v181, v28, v185
	v_cvt_pk_bf16_f32 v28, v28, s0
	ds_write_b16 v164, v28 offset:272
	v_mul_f32_e32 v28, v189, v161
	v_fma_f32 v28, v182, v28, v186
	v_cvt_pk_bf16_f32 v28, v28, s0
	ds_write_b16 v164, v28 offset:544
	v_mul_f32_e32 v28, v29, v161
	v_fmac_f32_e32 v187, v183, v28
	v_cvt_pk_bf16_f32 v28, v187, s0
	ds_write_b16 v164, v28 offset:816
	v_mul_f32_e32 v28, v190, v161
	v_fma_f32 v180, v180, v188, v184
	s_waitcnt vmcnt(10)
	v_fma_f32 v28, v44, v28, v48
	v_cvt_pk_bf16_f32 v180, v180, s0
	v_cvt_pk_bf16_f32 v28, v28, s0
	ds_write_b16 v164, v180
	ds_write_b16 v164, v28 offset:1088
	v_mul_f32_e32 v28, v30, v161
	global_load_dwordx4 v[180:183], v160, s[8:9] offset:64
	global_load_dwordx4 v[184:187], v160, s[10:11] offset:64
	v_fma_f32 v28, v45, v28, v49
	v_cvt_pk_bf16_f32 v28, v28, s0
	ds_write_b16 v164, v28 offset:1360
	v_mul_f32_e32 v28, v191, v161
	v_fma_f32 v28, v46, v28, v50
	v_cvt_pk_bf16_f32 v28, v28, s0
	ds_write_b16 v164, v28 offset:1632
	v_mul_f32_e32 v28, v31, v161
	v_fmac_f32_e32 v51, v47, v28
	v_cvt_pk_bf16_f32 v28, v51, s0
	ds_write_b16 v164, v28 offset:1904
	global_load_dwordx4 v[28:31], v160, s[8:9] offset:80
	global_load_dwordx4 v[48:51], v160, s[10:11] offset:80
	v_lshlrev_b32_e32 v44, 16, v16
	v_and_b32_e32 v16, 0xffff0000, v16
	v_fmac_f32_e32 v16, 0xbb000000, v157
	v_mul_f32_e32 v16, v16, v161
	v_lshlrev_b32_e32 v45, 16, v17
	v_fmac_f32_e32 v45, 0xbb000000, v157
	v_and_b32_e32 v17, 0xffff0000, v17
	v_fmac_f32_e32 v17, 0xbb000000, v157
	v_lshlrev_b32_e32 v46, 16, v18
	s_waitcnt vmcnt(8)
	v_fma_f32 v16, v53, v16, v57
	v_cvt_pk_bf16_f32 v16, v16, s0
	ds_write_b16 v164, v16 offset:2448
	v_mul_f32_e32 v16, v45, v161
	v_fma_f32 v16, v54, v16, v58
	v_cvt_pk_bf16_f32 v16, v16, s0
	ds_write_b16 v164, v16 offset:2720
	v_mul_f32_e32 v16, v17, v161
	v_fmac_f32_e32 v59, v55, v16
	v_fmac_f32_e32 v44, 0xbb000000, v157
	v_cvt_pk_bf16_f32 v16, v59, s0
	v_fmac_f32_e32 v46, 0xbb000000, v157
	v_mul_f32_e32 v44, v44, v161
	ds_write_b16 v164, v16 offset:2992
	v_mul_f32_e32 v16, v46, v161
	v_and_b32_e32 v18, 0xffff0000, v18
	v_fma_f32 v44, v52, v44, v56
	s_waitcnt vmcnt(4)
	v_fma_f32 v16, v60, v16, v64
	v_cvt_pk_bf16_f32 v44, v44, s0
	v_cvt_pk_bf16_f32 v16, v16, s0
	v_fmac_f32_e32 v18, 0xbb000000, v157
	ds_write_b16 v164, v44 offset:2176
	ds_write_b16 v164, v16 offset:3264
	v_mul_f32_e32 v16, v18, v161
	v_lshlrev_b32_e32 v47, 16, v19
	global_load_dwordx4 v[52:55], v160, s[8:9] offset:96
	global_load_dwordx4 v[56:59], v160, s[10:11] offset:96
	v_fma_f32 v16, v61, v16, v65
	v_cvt_pk_bf16_f32 v16, v16, s0
	v_fmac_f32_e32 v47, 0xbb000000, v157
	ds_write_b16 v164, v16 offset:3536
	v_mul_f32_e32 v16, v47, v161
	v_and_b32_e32 v19, 0xffff0000, v19
	v_fma_f32 v16, v62, v16, v66
	v_cvt_pk_bf16_f32 v16, v16, s0
	v_fmac_f32_e32 v19, 0xbb000000, v157
	ds_write_b16 v164, v16 offset:3808
	v_mul_f32_e32 v16, v19, v161
	v_fmac_f32_e32 v67, v63, v16
	v_cvt_pk_bf16_f32 v16, v67, s0
	ds_write_b16 v164, v16 offset:4080
	global_load_dwordx4 v[16:19], v160, s[8:9] offset:112
	global_load_dwordx4 v[44:47], v160, s[10:11] offset:112
	v_lshlrev_b32_e32 v60, 16, v40
	v_and_b32_e32 v40, 0xffff0000, v40
	v_fmac_f32_e32 v40, 0xbb000000, v157
	v_mul_f32_e32 v40, v40, v161
	v_lshlrev_b32_e32 v61, 16, v41
	v_fmac_f32_e32 v61, 0xbb000000, v157
	v_and_b32_e32 v41, 0xffff0000, v41
	v_fmac_f32_e32 v41, 0xbb000000, v157
	v_lshlrev_b32_e32 v62, 16, v42
	v_fmac_f32_e32 v60, 0xbb000000, v157
	v_fmac_f32_e32 v62, 0xbb000000, v157
	v_mul_f32_e32 v60, v60, v161
	v_and_b32_e32 v42, 0xffff0000, v42
	v_fmac_f32_e32 v42, 0xbb000000, v157
	v_lshlrev_b32_e32 v179, 16, v43
	v_fmac_f32_e32 v179, 0xbb000000, v157
	v_and_b32_e32 v43, 0xffff0000, v43
	s_waitcnt vmcnt(6)
; #define LAS __attribute__((address_space(3)))
; __device__ __forceinline__ unsigned pk2(float lo, float hi) { f32x2 v = {lo, hi}; bf16x2_t b = __builtin_convertvector(v, bf16x2_t); return __builtin_bit_cast(unsigned, b); }
; __device__ __forceinline__ void cvt8(const u32x4 r, float (&f)[8]) { f[0] = bflo(r.x); f[1] = bfhi(r.x); f[2] = bflo(r.y); f[3] = bfhi(r.y); f[4] = bflo(r.z); f[5] = bfhi(r.z); f[6] = bflo(r.w); f[7] = bfhi(r.w); }
; __device__ __forceinline__ void gmlp_unit(Ctx& C, int l, int uidx) {
;     ...
;         for (int c8 = 0; c8 < 8; ++c8) { float f[8]; cvt8(r2[c8], f);
;             const f32x4 g0 = *(const f32x4*)(lg + 8 * c8), g1 = *(const f32x4*)(lg + 8 * c8 + 4), b0 = *(const f32x4*)(lb + 8 * c8), b1 = *(const f32x4*)(lb + 8 * c8 + 4);
;             const float gg[8] = {g0[0], g0[1], g0[2], g0[3], g1[0], g1[1], g1[2], g1[3]}, bb[8] = {b0[0], b0[1], b0[2], b0[3], b1[0], b1[1], b1[2], b1[3]};
; #pragma unroll
;             for (int j = 0; j < 8; ++j) { const float vn = (f[j] - mean) * rstd * gg[j] + bb[j];
;                 *(LAS bf16*)(C.lds + (64 * part + 8 * c8 + j) * VS + tok * 2) = (bf16)(pk2(vn, 0.f) & 0xffffu); } }
	v_fma_f32 v40, v181, v40, v185
	v_cvt_pk_bf16_f32 v40, v40, s0
	ds_write_b16 v164, v40 offset:4624
	v_mul_f32_e32 v40, v61, v161
	v_fma_f32 v40, v182, v40, v186
	v_cvt_pk_bf16_f32 v40, v40, s0
	ds_write_b16 v164, v40 offset:4896
	v_mul_f32_e32 v40, v41, v161
	v_fmac_f32_e32 v187, v183, v40
	v_cvt_pk_bf16_f32 v40, v187, s0
	ds_write_b16 v164, v40 offset:5168
	v_mul_f32_e32 v40, v62, v161
	v_fma_f32 v60, v180, v60, v184
	s_waitcnt vmcnt(4)
	v_fma_f32 v28, v28, v40, v48
	v_cvt_pk_bf16_f32 v60, v60, s0
	v_cvt_pk_bf16_f32 v28, v28, s0
	ds_write_b16 v164, v60 offset:4352
	ds_write_b16 v164, v28 offset:5440
	v_mul_f32_e32 v28, v42, v161
	global_load_dwordx4 v[60:63], v160, s[8:9] offset:128
	global_load_dwordx4 v[64:67], v160, s[10:11] offset:128
	v_fma_f32 v28, v29, v28, v49
	v_cvt_pk_bf16_f32 v28, v28, s0
	ds_write_b16 v164, v28 offset:5712
	v_mul_f32_e32 v28, v179, v161
	v_fma_f32 v28, v30, v28, v50
	v_cvt_pk_bf16_f32 v28, v28, s0
	v_fmac_f32_e32 v43, 0xbb000000, v157
	ds_write_b16 v164, v28 offset:5984
	v_mul_f32_e32 v28, v43, v161
	v_fmac_f32_e32 v51, v31, v28
	v_cvt_pk_bf16_f32 v28, v51, s0
	ds_write_b16 v164, v28 offset:6256
	global_load_dwordx4 v[28:31], v160, s[8:9] offset:144
	global_load_dwordx4 v[40:43], v160, s[10:11] offset:144
	v_lshlrev_b32_e32 v48, 16, v36
	v_and_b32_e32 v36, 0xffff0000, v36
	v_fmac_f32_e32 v36, 0xbb000000, v157
	v_mul_f32_e32 v36, v36, v161
	v_lshlrev_b32_e32 v49, 16, v37
	v_fmac_f32_e32 v49, 0xbb000000, v157
	v_and_b32_e32 v37, 0xffff0000, v37
	v_fmac_f32_e32 v37, 0xbb000000, v157
	v_lshlrev_b32_e32 v50, 16, v38
	v_fmac_f32_e32 v50, 0xbb000000, v157
	v_fmac_f32_e32 v48, 0xbb000000, v157
	v_and_b32_e32 v179, 0xffff0000, v38
	v_mul_f32_e32 v38, v48, v161
	v_fmac_f32_e32 v179, 0xbb000000, v157
	s_waitcnt vmcnt(6)
	v_fma_f32 v36, v53, v36, v57
	v_cvt_pk_bf16_f32 v36, v36, s0
	ds_write_b16 v164, v36 offset:6800
	v_mul_f32_e32 v36, v49, v161
	v_fma_f32 v36, v54, v36, v58
	v_cvt_pk_bf16_f32 v36, v36, s0
	ds_write_b16 v164, v36 offset:7072
	v_mul_f32_e32 v36, v37, v161
	v_fmac_f32_e32 v59, v55, v36
	v_cvt_pk_bf16_f32 v36, v59, s0
	ds_write_b16 v164, v36 offset:7344
	v_mul_f32_e32 v36, v50, v161
	v_fma_f32 v38, v52, v38, v56
	v_cvt_pk_bf16_f32 v38, v38, s0
	v_lshlrev_b32_e32 v180, 16, v39
	s_waitcnt vmcnt(4)
	v_fma_f32 v16, v16, v36, v44
	v_cvt_pk_bf16_f32 v16, v16, s0
	ds_write_b16 v164, v16 offset:7616
	v_mul_f32_e32 v16, v179, v161
	ds_write_b16 v164, v38 offset:6528
	v_fma_f32 v16, v17, v16, v45
	v_and_b32_e32 v181, 0xffff0000, v39
	global_load_dwordx4 v[36:39], v160, s[8:9] offset:160
	global_load_dwordx4 v[48:51], v160, s[10:11] offset:160
	v_cvt_pk_bf16_f32 v16, v16, s0
	v_fmac_f32_e32 v180, 0xbb000000, v157
	ds_write_b16 v164, v16 offset:7888
	v_mul_f32_e32 v16, v180, v161
	v_fma_f32 v16, v18, v16, v46
	v_cvt_pk_bf16_f32 v16, v16, s0
	v_fmac_f32_e32 v181, 0xbb000000, v157
	ds_write_b16 v164, v16 offset:8160
	v_mul_f32_e32 v16, v181, v161
	v_fmac_f32_e32 v47, v19, v16
	v_cvt_pk_bf16_f32 v16, v47, s0
	ds_write_b16 v164, v16 offset:8432
	global_load_dwordx4 v[16:19], v160, s[8:9] offset:176
	global_load_dwordx4 v[44:47], v160, s[10:11] offset:176
	v_lshlrev_b32_e32 v52, 16, v32
	v_and_b32_e32 v32, 0xffff0000, v32
	v_fmac_f32_e32 v32, 0xbb000000, v157
	v_mul_f32_e32 v32, v32, v161
	v_lshlrev_b32_e32 v53, 16, v33
	v_fmac_f32_e32 v53, 0xbb000000, v157
	v_and_b32_e32 v33, 0xffff0000, v33
	v_fmac_f32_e32 v33, 0xbb000000, v157
	v_lshlrev_b32_e32 v54, 16, v34
	v_fmac_f32_e32 v52, 0xbb000000, v157
	v_fmac_f32_e32 v54, 0xbb000000, v157
	v_and_b32_e32 v56, 0xffff0000, v34
	v_mul_f32_e32 v34, v52, v161
	v_fmac_f32_e32 v56, 0xbb000000, v157
	v_lshlrev_b32_e32 v57, 16, v35
	v_and_b32_e32 v58, 0xffff0000, v35
	s_waitcnt vmcnt(6)
	v_fma_f32 v32, v61, v32, v65
	v_cvt_pk_bf16_f32 v32, v32, s0
	ds_write_b16 v164, v32 offset:8976
	v_mul_f32_e32 v32, v53, v161
	v_fma_f32 v32, v62, v32, v66
	v_cvt_pk_bf16_f32 v32, v32, s0
	ds_write_b16 v164, v32 offset:9248
	v_mul_f32_e32 v32, v33, v161
	v_fmac_f32_e32 v67, v63, v32
	v_cvt_pk_bf16_f32 v32, v67, s0
	ds_write_b16 v164, v32 offset:9520
	v_mul_f32_e32 v32, v54, v161
	v_fma_f32 v34, v60, v34, v64
	s_waitcnt vmcnt(4)
	v_fma_f32 v28, v28, v32, v40
	v_cvt_pk_bf16_f32 v34, v34, s0
	v_cvt_pk_bf16_f32 v28, v28, s0
	ds_write_b16 v164, v34 offset:8704
	ds_write_b16 v164, v28 offset:9792
	v_mul_f32_e32 v28, v56, v161
	global_load_dwordx4 v[32:35], v160, s[8:9] offset:192
	global_load_dwordx4 v[52:55], v160, s[10:11] offset:192
	v_fma_f32 v28, v29, v28, v41
	v_cvt_pk_bf16_f32 v28, v28, s0
	v_fmac_f32_e32 v57, 0xbb000000, v157
	ds_write_b16 v164, v28 offset:10064
	v_mul_f32_e32 v28, v57, v161
	v_fma_f32 v28, v30, v28, v42
	v_cvt_pk_bf16_f32 v28, v28, s0
	v_fmac_f32_e32 v58, 0xbb000000, v157
	ds_write_b16 v164, v28 offset:10336
	v_mul_f32_e32 v28, v58, v161
	v_fmac_f32_e32 v43, v31, v28
	v_cvt_pk_bf16_f32 v28, v43, s0
	ds_write_b16 v164, v28 offset:10608
	global_load_dwordx4 v[28:31], v160, s[8:9] offset:208
	global_load_dwordx4 v[40:43], v160, s[10:11] offset:208
	v_lshlrev_b32_e32 v56, 16, v24
	v_and_b32_e32 v24, 0xffff0000, v24
	v_fmac_f32_e32 v24, 0xbb000000, v157
	v_mul_f32_e32 v24, v24, v161
	v_lshlrev_b32_e32 v57, 16, v25
	v_fmac_f32_e32 v57, 0xbb000000, v157
	v_and_b32_e32 v25, 0xffff0000, v25
	v_fmac_f32_e32 v56, 0xbb000000, v157
	v_fmac_f32_e32 v25, 0xbb000000, v157
	v_lshlrev_b32_e32 v58, 16, v26
	v_and_b32_e32 v59, 0xffff0000, v26
	v_mul_f32_e32 v26, v56, v161
	v_fmac_f32_e32 v58, 0xbb000000, v157
	v_lshlrev_b32_e32 v60, 16, v27
	v_and_b32_e32 v61, 0xffff0000, v27
	v_fmac_f32_e32 v59, 0xbb000000, v157
	s_waitcnt vmcnt(6)
; #define LAS __attribute__((address_space(3)))
; __device__ __forceinline__ unsigned pk2(float lo, float hi) { f32x2 v = {lo, hi}; bf16x2_t b = __builtin_convertvector(v, bf16x2_t); return __builtin_bit_cast(unsigned, b); }
; __device__ __forceinline__ void cvt8(const u32x4 r, float (&f)[8]) { f[0] = bflo(r.x); f[1] = bfhi(r.x); f[2] = bflo(r.y); f[3] = bfhi(r.y); f[4] = bflo(r.z); f[5] = bfhi(r.z); f[6] = bflo(r.w); f[7] = bfhi(r.w); }
; __device__ __forceinline__ void gmlp_unit(Ctx& C, int l, int uidx) {
;     ...
;         for (int c8 = 0; c8 < 8; ++c8) { float f[8]; cvt8(r2[c8], f);
;             const f32x4 g0 = *(const f32x4*)(lg + 8 * c8), g1 = *(const f32x4*)(lg + 8 * c8 + 4), b0 = *(const f32x4*)(lb + 8 * c8), b1 = *(const f32x4*)(lb + 8 * c8 + 4);
;             const float gg[8] = {g0[0], g0[1], g0[2], g0[3], g1[0], g1[1], g1[2], g1[3]}, bb[8] = {b0[0], b0[1], b0[2], b0[3], b1[0], b1[1], b1[2], b1[3]};
; #pragma unroll
;             for (int j = 0; j < 8; ++j) { const float vn = (f[j] - mean) * rstd * gg[j] + bb[j];
;                 *(LAS bf16*)(C.lds + (64 * part + 8 * c8 + j) * VS + tok * 2) = (bf16)(pk2(vn, 0.f) & 0xffffu); } }
;     }
;     __syncthreads();
	v_fma_f32 v24, v37, v24, v49
	v_cvt_pk_bf16_f32 v24, v24, s0
	ds_write_b16 v164, v24 offset:11152
	v_mul_f32_e32 v24, v57, v161
	v_fma_f32 v24, v38, v24, v50
	v_cvt_pk_bf16_f32 v24, v24, s0
	ds_write_b16 v164, v24 offset:11424
	v_mul_f32_e32 v24, v25, v161
	v_fma_f32 v26, v36, v26, v48
	v_fmac_f32_e32 v51, v39, v24
	v_cvt_pk_bf16_f32 v26, v26, s0
	v_cvt_pk_bf16_f32 v24, v51, s0
	v_mul_f32_e32 v48, v58, v161
	ds_write_b16 v164, v26 offset:10880
	ds_write_b16 v164, v24 offset:11696
	s_waitcnt vmcnt(4)
	v_fma_f32 v16, v16, v48, v44
	global_load_dwordx4 v[24:27], v160, s[8:9] offset:224
	global_load_dwordx4 v[36:39], v160, s[10:11] offset:224
	v_cvt_pk_bf16_f32 v16, v16, s0
	ds_write_b16 v164, v16 offset:11968
	v_mul_f32_e32 v16, v59, v161
	v_fma_f32 v16, v17, v16, v45
	v_cvt_pk_bf16_f32 v16, v16, s0
	v_fmac_f32_e32 v60, 0xbb000000, v157
	ds_write_b16 v164, v16 offset:12240
	v_mul_f32_e32 v16, v60, v161
	v_fma_f32 v16, v18, v16, v46
	v_cvt_pk_bf16_f32 v16, v16, s0
	v_fmac_f32_e32 v61, 0xbb000000, v157
	ds_write_b16 v164, v16 offset:12512
	v_mul_f32_e32 v16, v61, v161
	v_fmac_f32_e32 v47, v19, v16
	v_cvt_pk_bf16_f32 v48, v47, s0
	global_load_dwordx4 v[16:19], v160, s[8:9] offset:240
	global_load_dwordx4 v[44:47], v160, s[10:11] offset:240
	ds_write_b16 v164, v48 offset:12784
	v_lshlrev_b32_e32 v48, 16, v20
	v_and_b32_e32 v20, 0xffff0000, v20
	v_fmac_f32_e32 v20, 0xbb000000, v157
	v_mul_f32_e32 v20, v20, v161
	v_lshlrev_b32_e32 v49, 16, v21
	v_fmac_f32_e32 v49, 0xbb000000, v157
	v_and_b32_e32 v21, 0xffff0000, v21
	v_fmac_f32_e32 v21, 0xbb000000, v157
	v_lshlrev_b32_e32 v50, 16, v22
	v_fmac_f32_e32 v50, 0xbb000000, v157
	v_and_b32_e32 v22, 0xffff0000, v22
	v_fmac_f32_e32 v22, 0xbb000000, v157
	v_lshlrev_b32_e32 v51, 16, v23
	v_fmac_f32_e32 v51, 0xbb000000, v157
	v_and_b32_e32 v23, 0xffff0000, v23
	s_waitcnt vmcnt(6)
	v_fma_f32 v20, v33, v20, v53
	v_cvt_pk_bf16_f32 v20, v20, s0
	ds_write_b16 v164, v20 offset:13328
	v_mul_f32_e32 v20, v49, v161
	v_fma_f32 v20, v34, v20, v54
	v_cvt_pk_bf16_f32 v20, v20, s0
	ds_write_b16 v164, v20 offset:13600
	v_mul_f32_e32 v20, v21, v161
	v_fmac_f32_e32 v55, v35, v20
	v_cvt_pk_bf16_f32 v20, v55, s0
	ds_write_b16 v164, v20 offset:13872
	v_mul_f32_e32 v20, v50, v161
	v_fmac_f32_e32 v23, 0xbb000000, v157
	v_lshlrev_b32_e32 v21, 16, v13
	s_waitcnt vmcnt(4)
	v_fma_f32 v20, v28, v20, v40
	v_cvt_pk_bf16_f32 v20, v20, s0
	ds_write_b16 v164, v20 offset:14144
	v_mul_f32_e32 v20, v22, v161
	v_fma_f32 v20, v29, v20, v41
	v_cvt_pk_bf16_f32 v20, v20, s0
	ds_write_b16 v164, v20 offset:14416
	v_mul_f32_e32 v20, v51, v161
	v_fma_f32 v20, v30, v20, v42
	v_cvt_pk_bf16_f32 v20, v20, s0
	ds_write_b16 v164, v20 offset:14688
	v_mul_f32_e32 v20, v23, v161
	v_fmac_f32_e32 v43, v31, v20
	v_cvt_pk_bf16_f32 v20, v43, s0
	ds_write_b16 v164, v20 offset:14960
	v_lshlrev_b32_e32 v20, 16, v12
	v_and_b32_e32 v12, 0xffff0000, v12
	v_fmac_f32_e32 v12, 0xbb000000, v157
	v_mul_f32_e32 v12, v12, v161
	v_fmac_f32_e32 v21, 0xbb000000, v157
	v_and_b32_e32 v13, 0xffff0000, v13
	v_fmac_f32_e32 v13, 0xbb000000, v157
	v_lshlrev_b32_e32 v22, 16, v14
	v_fmac_f32_e32 v22, 0xbb000000, v157
	v_and_b32_e32 v14, 0xffff0000, v14
	v_fmac_f32_e32 v14, 0xbb000000, v157
	v_lshlrev_b32_e32 v23, 16, v15
	v_fmac_f32_e32 v23, 0xbb000000, v157
	v_and_b32_e32 v15, 0xffff0000, v15
	v_fmac_f32_e32 v15, 0xbb000000, v157
	v_fmac_f32_e32 v48, 0xbb000000, v157
	v_fmac_f32_e32 v20, 0xbb000000, v157
	v_mul_f32_e32 v48, v48, v161
	s_waitcnt vmcnt(2)
	v_fma_f32 v12, v25, v12, v37
	v_cvt_pk_bf16_f32 v12, v12, s0
	ds_write_b16 v164, v12 offset:15504
	v_mul_f32_e32 v12, v21, v161
	v_fma_f32 v12, v26, v12, v38
	v_cvt_pk_bf16_f32 v12, v12, s0
	ds_write_b16 v164, v12 offset:15776
	v_mul_f32_e32 v12, v13, v161
	v_fmac_f32_e32 v39, v27, v12
	v_cvt_pk_bf16_f32 v12, v39, s0
	ds_write_b16 v164, v12 offset:16048
	v_mul_f32_e32 v12, v22, v161
	v_mul_f32_e32 v20, v20, v161
	v_fma_f32 v32, v32, v48, v52
	v_fma_f32 v20, v24, v20, v36
	v_cvt_pk_bf16_f32 v32, v32, s0
	s_waitcnt vmcnt(0)
	v_fma_f32 v12, v16, v12, v44
	v_cvt_pk_bf16_f32 v12, v12, s0
	ds_write_b16 v164, v12 offset:16320
	v_mul_f32_e32 v12, v14, v161
	v_fma_f32 v12, v17, v12, v45
	v_cvt_pk_bf16_f32 v12, v12, s0
	ds_write_b16 v164, v12 offset:16592
	v_mul_f32_e32 v12, v23, v161
	v_fma_f32 v12, v18, v12, v46
	v_cvt_pk_bf16_f32 v12, v12, s0
	ds_write_b16 v164, v12 offset:16864
	v_mul_f32_e32 v12, v15, v161
	v_fmac_f32_e32 v47, v19, v12
	v_cvt_pk_bf16_f32 v12, v47, s0
	ds_write_b16 v164, v12 offset:17136
	v_lshl_or_b32 v12, s19, 6, v159
	v_mul_lo_u32 v12, v12, s6
	v_cvt_pk_bf16_f32 v20, v20, s0
	v_add3_u32 v156, 0, v156, v12
	ds_write_b16 v164, v32 offset:13056
	ds_write_b16 v164, v20 offset:15232
	s_waitcnt lgkmcnt(0)
	s_barrier
; #define LAS __attribute__((address_space(3)))
; __device__ __forceinline__ unsigned pk2(float lo, float hi) { f32x2 v = {lo, hi}; bf16x2_t b = __builtin_convertvector(v, bf16x2_t); return __builtin_bit_cast(unsigned, b); }
; __device__ __forceinline__ float bflo(unsigned w) { return __uint_as_float(w << 16); }
; __device__ __forceinline__ float bfhi(unsigned w) { return __uint_as_float(w & 0xffff0000u); }
; #define MFMA32(a, b, c) __builtin_amdgcn_mfma_f32_32x32x16_bf16((a), (b), (c), 0, 0, 0)
; __device__ __forceinline__ void gmlp_unit(Ctx& C, int l, int uidx) {
;     ...
; #pragma unroll
;     for (int s = 0; s < 8; ++s) {
;         bf16x8 Vf[2];
; #pragma unroll
;         for (int cb = 0; cb < 2; ++cb) Vf[cb] = *(const LAS bf16x8*)(C.lds + (64 * gl + 32 * cb + r32) * VS + (16 * s + 8 * h) * 2);
; #pragma unroll
;         for (int cb = 0; cb < 2; ++cb)
; #pragma unroll
;             for (int pb = 0; pb < 2; ++pb) acc[cb][pb] = MFMA32(Vf[cb], Wf[pb][s], acc[cb][pb]);
;     }
;     bf16* Y = WSP(bf16, WS_YCAT);
; #pragma unroll
;     for (int pb = 0; pb < 2; ++pb) { const int p = 64 * ph + 32 * pb + r32; const float bs = INP(I_GBS)[(l * 8 + g) * 128 + p];
;         bf16* yp = Y + (size_t)(row0 + p) * DM + 1536 + 64 * g + 4 * h;
; #pragma unroll
;         for (int cb = 0; cb < 2; ++cb)
; #pragma unroll
;             for (int rg = 0; rg < 4; ++rg) { const u32x2 uv = upre[pb][cb][rg];
;                 u32x2 w; w.x = pk2(bflo(uv.x) * (acc[cb][pb][4 * rg] + bs), bfhi(uv.x) * (acc[cb][pb][4 * rg + 1] + bs)); w.y = pk2(bflo(uv.y) * (acc[cb][pb][4 * rg + 2] + bs), bfhi(uv.y) * (acc[cb][pb][4 * rg + 3] + bs));
;                 *(u32x2*)(yp + 32 * cb + 8 * rg) = w; } }
	ds_read_b128 v[12:15], v156
	ds_read_b128 v[180:183], v156 offset:32
	s_waitcnt lgkmcnt(1)
	v_mfma_f32_32x32x16_bf16 v[52:67], v[12:15], v[4:7], 0
	s_lshl_b32 s6, s14, 7
	s_mov_b64 s[8:9], 0x3e000c00
	v_mfma_f32_32x32x16_bf16 v[20:35], v[12:15], v[8:11], 0
	ds_read_b128 v[12:15], v156 offset:8704
	ds_read_b128 v[184:187], v156 offset:8736
	s_waitcnt lgkmcnt(1)
	v_mfma_f32_32x32x16_bf16 v[36:51], v[12:15], v[4:7], 0
	v_mfma_f32_32x32x16_bf16 v[4:19], v[12:15], v[8:11], 0
	v_mfma_f32_32x32x16_bf16 v[52:67], v[180:183], v[116:119], v[52:67]
	v_mfma_f32_32x32x16_bf16 v[20:35], v[180:183], v[120:123], v[20:35]
	s_waitcnt lgkmcnt(0)
	v_mfma_f32_32x32x16_bf16 v[36:51], v[184:187], v[116:119], v[36:51]
	v_mfma_f32_32x32x16_bf16 v[4:19], v[184:187], v[120:123], v[4:19]
	ds_read_b128 v[116:119], v156 offset:64
	ds_read_b128 v[120:123], v156 offset:96
	s_waitcnt lgkmcnt(1)
	v_mfma_f32_32x32x16_bf16 v[52:67], v[116:119], v[104:107], v[52:67]
	v_mfma_f32_32x32x16_bf16 v[20:35], v[116:119], v[112:115], v[20:35]
	ds_read_b128 v[116:119], v156 offset:8768
	ds_read_b128 v[180:183], v156 offset:8800
	s_waitcnt lgkmcnt(1)
	v_mfma_f32_32x32x16_bf16 v[36:51], v[116:119], v[104:107], v[36:51]
	v_mfma_f32_32x32x16_bf16 v[4:19], v[116:119], v[112:115], v[4:19]
	v_mfma_f32_32x32x16_bf16 v[52:67], v[120:123], v[100:103], v[52:67]
	v_mfma_f32_32x32x16_bf16 v[20:35], v[120:123], v[108:111], v[20:35]
	s_waitcnt lgkmcnt(0)
	v_mfma_f32_32x32x16_bf16 v[36:51], v[180:183], v[100:103], v[36:51]
	ds_read_b128 v[100:103], v156 offset:128
	ds_read_b128 v[104:107], v156 offset:160
	v_mfma_f32_32x32x16_bf16 v[4:19], v[180:183], v[108:111], v[4:19]
	s_waitcnt lgkmcnt(1)
	v_mfma_f32_32x32x16_bf16 v[52:67], v[100:103], v[88:91], v[52:67]
	v_mfma_f32_32x32x16_bf16 v[20:35], v[100:103], v[96:99], v[20:35]
	ds_read_b128 v[100:103], v156 offset:8832
	ds_read_b128 v[108:111], v156 offset:8864
	s_waitcnt lgkmcnt(1)
	v_mfma_f32_32x32x16_bf16 v[36:51], v[100:103], v[88:91], v[36:51]
	v_mfma_f32_32x32x16_bf16 v[4:19], v[100:103], v[96:99], v[4:19]
	v_mfma_f32_32x32x16_bf16 v[52:67], v[104:107], v[84:87], v[52:67]
	v_mfma_f32_32x32x16_bf16 v[20:35], v[104:107], v[92:95], v[20:35]
	s_waitcnt lgkmcnt(0)
	v_mfma_f32_32x32x16_bf16 v[36:51], v[108:111], v[84:87], v[36:51]
	ds_read_b128 v[84:87], v156 offset:192
	ds_read_b128 v[88:91], v156 offset:224
	v_mfma_f32_32x32x16_bf16 v[4:19], v[108:111], v[92:95], v[4:19]
	s_waitcnt lgkmcnt(1)
	v_mfma_f32_32x32x16_bf16 v[52:67], v[84:87], v[76:79], v[52:67]
	v_mfma_f32_32x32x16_bf16 v[20:35], v[84:87], v[80:83], v[20:35]
	ds_read_b128 v[84:87], v156 offset:8896
	ds_read_b128 v[92:95], v156 offset:8928
	s_waitcnt lgkmcnt(1)
	v_mfma_f32_32x32x16_bf16 v[4:19], v[84:87], v[80:83], v[4:19]
	v_or_b32_e32 v80, s15, v159
	v_lshlrev_b32_e32 v82, 16, v154
	v_and_b32_e32 v83, 0xffff0000, v154
	v_mfma_f32_32x32x16_bf16 v[36:51], v[84:87], v[76:79], v[36:51]
	v_or_b32_e32 v76, s6, v80
	v_ashrrev_i32_e32 v77, 31, v76
	v_lshl_add_u64 v[78:79], v[76:77], 2, s[58:59]
	global_load_dword v78, v[78:79], off
	s_ashr_i32 s6, s6, 31
	v_mov_b32_e32 v77, s6
	v_mfma_f32_32x32x16_bf16 v[52:67], v[88:91], v[72:75], v[52:67]
	s_waitcnt lgkmcnt(0)
	v_mfma_f32_32x32x16_bf16 v[36:51], v[92:95], v[72:75], v[36:51]
	v_or_b32_e32 v72, s18, v80
	v_lshlrev_b32_e32 v72, 12, v72
	v_mov_b32_e32 v73, v3
	v_lshl_add_u64 v[74:75], s[54:55], 0, v[72:73]
	v_lshl_add_u64 v[74:75], v[74:75], 0, s[12:13]
	v_lshl_add_u64 v[74:75], v[74:75], 0, v[2:3]
	v_lshl_add_u64 v[80:81], v[74:75], 0, s[8:9]
	v_mfma_f32_32x32x16_bf16 v[20:35], v[88:91], v[68:71], v[20:35]
	s_waitcnt vmcnt(0)
	s_nop 0
	v_add_f32_e64 v52, v52, v78
	v_add_f32_e64 v53, v53, v78
	v_mul_f32_e64 v52, v52, v82
	v_mul_f32_e64 v53, v53, v83
	v_lshlrev_b32_e32 v82, 16, v155
	v_and_b32_e32 v83, 0xffff0000, v155
	v_pk_add_f32 v[54:55], v[54:55], v[78:79] op_sel_hi:[1,0]
	v_cvt_pk_bf16_f32 v52, v52, v53
	v_pk_mul_f32 v[54:55], v[54:55], v[82:83]
	v_pk_add_f32 v[36:37], v[36:37], v[78:79] op_sel_hi:[1,0]
	v_cvt_pk_bf16_f32 v53, v54, v55
	v_add_co_u32_e32 v54, vcc, s73, v74
	v_pk_add_f32 v[38:39], v[38:39], v[78:79] op_sel_hi:[1,0]
	s_nop 0
	v_addc_co_u32_e32 v55, vcc, 0, v75, vcc
	global_store_dwordx2 v[54:55], v[52:53], off offset:3072
	v_lshlrev_b32_e32 v52, 16, v152
	v_and_b32_e32 v53, 0xffff0000, v152
	v_pk_add_f32 v[54:55], v[56:57], v[78:79] op_sel_hi:[1,0]
	v_pk_add_f32 v[56:57], v[58:59], v[78:79] op_sel_hi:[1,0]
	v_pk_mul_f32 v[52:53], v[54:55], v[52:53]
	v_lshlrev_b32_e32 v54, 16, v153
	v_and_b32_e32 v55, 0xffff0000, v153
	v_pk_mul_f32 v[54:55], v[56:57], v[54:55]
	v_cvt_pk_bf16_f32 v52, v52, v53
	v_cvt_pk_bf16_f32 v53, v54, v55
	global_store_dwordx2 v[80:81], v[52:53], off offset:16
	v_lshlrev_b32_e32 v52, 16, v150
	v_and_b32_e32 v53, 0xffff0000, v150
	v_pk_add_f32 v[54:55], v[60:61], v[78:79] op_sel_hi:[1,0]
	v_pk_add_f32 v[56:57], v[62:63], v[78:79] op_sel_hi:[1,0]
	v_pk_mul_f32 v[52:53], v[54:55], v[52:53]
	v_lshlrev_b32_e32 v54, 16, v151
	v_and_b32_e32 v55, 0xffff0000, v151
	v_pk_mul_f32 v[54:55], v[56:57], v[54:55]
	v_cvt_pk_bf16_f32 v52, v52, v53
	v_cvt_pk_bf16_f32 v53, v54, v55
	global_store_dwordx2 v[80:81], v[52:53], off offset:32
	v_lshlrev_b32_e32 v52, 16, v148
	v_and_b32_e32 v53, 0xffff0000, v148
	v_pk_add_f32 v[54:55], v[64:65], v[78:79] op_sel_hi:[1,0]
	v_pk_add_f32 v[56:57], v[66:67], v[78:79] op_sel_hi:[1,0]
	v_pk_mul_f32 v[52:53], v[54:55], v[52:53]
	v_lshlrev_b32_e32 v54, 16, v149
	v_and_b32_e32 v55, 0xffff0000, v149
	v_pk_mul_f32 v[54:55], v[56:57], v[54:55]
	v_cvt_pk_bf16_f32 v52, v52, v53
	v_cvt_pk_bf16_f32 v53, v54, v55
	global_store_dwordx2 v[80:81], v[52:53], off offset:48
	v_lshlrev_b32_e32 v52, 16, v146
; __device__ __forceinline__ unsigned pk2(float lo, float hi) { f32x2 v = {lo, hi}; bf16x2_t b = __builtin_convertvector(v, bf16x2_t); return __builtin_bit_cast(unsigned, b); }
; __device__ __forceinline__ float bflo(unsigned w) { return __uint_as_float(w << 16); }
; __device__ __forceinline__ float bfhi(unsigned w) { return __uint_as_float(w & 0xffff0000u); }
; __device__ __forceinline__ void gmlp_unit(Ctx& C, int l, int uidx) {
;     ...
;     for (int pb = 0; pb < 2; ++pb) { const int p = 64 * ph + 32 * pb + r32; const float bs = INP(I_GBS)[(l * 8 + g) * 128 + p];
;         bf16* yp = Y + (size_t)(row0 + p) * DM + 1536 + 64 * g + 4 * h;
; #pragma unroll
;         for (int cb = 0; cb < 2; ++cb)
; #pragma unroll
;             for (int rg = 0; rg < 4; ++rg) { const u32x2 uv = upre[pb][cb][rg];
;                 u32x2 w; w.x = pk2(bflo(uv.x) * (acc[cb][pb][4 * rg] + bs), bfhi(uv.x) * (acc[cb][pb][4 * rg + 1] + bs)); w.y = pk2(bflo(uv.y) * (acc[cb][pb][4 * rg + 2] + bs), bfhi(uv.y) * (acc[cb][pb][4 * rg + 3] + bs));
;                 *(u32x2*)(yp + 32 * cb + 8 * rg) = w; } }
	v_and_b32_e32 v53, 0xffff0000, v146
	v_pk_mul_f32 v[36:37], v[36:37], v[52:53]
	v_lshlrev_b32_e32 v52, 16, v147
	v_and_b32_e32 v53, 0xffff0000, v147
	v_pk_mul_f32 v[38:39], v[38:39], v[52:53]
	v_cvt_pk_bf16_f32 v36, v36, v37
	v_cvt_pk_bf16_f32 v37, v38, v39
	global_store_dwordx2 v[80:81], v[36:37], off offset:64
	v_lshlrev_b32_e32 v36, 16, v144
	v_and_b32_e32 v37, 0xffff0000, v144
	v_pk_add_f32 v[38:39], v[40:41], v[78:79] op_sel_hi:[1,0]
	v_pk_add_f32 v[40:41], v[42:43], v[78:79] op_sel_hi:[1,0]
	v_pk_mul_f32 v[36:37], v[38:39], v[36:37]
	v_lshlrev_b32_e32 v38, 16, v145
	v_and_b32_e32 v39, 0xffff0000, v145
	v_pk_mul_f32 v[38:39], v[40:41], v[38:39]
	v_cvt_pk_bf16_f32 v36, v36, v37
	v_cvt_pk_bf16_f32 v37, v38, v39
	global_store_dwordx2 v[80:81], v[36:37], off offset:80
	v_lshlrev_b32_e32 v36, 16, v142
	v_and_b32_e32 v37, 0xffff0000, v142
	v_pk_add_f32 v[38:39], v[44:45], v[78:79] op_sel_hi:[1,0]
	v_pk_add_f32 v[40:41], v[46:47], v[78:79] op_sel_hi:[1,0]
	v_pk_mul_f32 v[36:37], v[38:39], v[36:37]
	v_lshlrev_b32_e32 v38, 16, v143
	v_and_b32_e32 v39, 0xffff0000, v143
	v_pk_mul_f32 v[38:39], v[40:41], v[38:39]
	v_cvt_pk_bf16_f32 v36, v36, v37
	v_cvt_pk_bf16_f32 v37, v38, v39
	global_store_dwordx2 v[80:81], v[36:37], off offset:96
	v_lshlrev_b32_e32 v36, 16, v140
	v_and_b32_e32 v37, 0xffff0000, v140
	v_pk_add_f32 v[38:39], v[48:49], v[78:79] op_sel_hi:[1,0]
	v_pk_add_f32 v[40:41], v[50:51], v[78:79] op_sel_hi:[1,0]
	v_pk_mul_f32 v[36:37], v[38:39], v[36:37]
	v_lshlrev_b32_e32 v38, 16, v141
	v_and_b32_e32 v39, 0xffff0000, v141
	v_pk_mul_f32 v[38:39], v[40:41], v[38:39]
	v_cvt_pk_bf16_f32 v36, v36, v37
	v_cvt_pk_bf16_f32 v37, v38, v39
	global_store_dwordx2 v[80:81], v[36:37], off offset:112
	v_lshl_add_u64 v[36:37], v[76:77], 2, s[58:59]
	global_load_dword v36, v[36:37], off offset:128
	v_or_b32_e32 v38, 0x20000, v72
	v_mov_b32_e32 v39, v3
	v_lshl_add_u64 v[38:39], s[54:55], 0, v[38:39]
	v_lshlrev_b32_e32 v42, 16, v138
	v_and_b32_e32 v43, 0xffff0000, v138
	v_lshl_add_u64 v[38:39], v[38:39], 0, s[12:13]
	v_lshl_add_u64 v[38:39], v[38:39], 0, v[2:3]
	v_lshl_add_u64 v[40:41], v[38:39], 0, s[8:9]
	v_mfma_f32_32x32x16_bf16 v[4:19], v[92:95], v[68:71], v[4:19]
	s_waitcnt vmcnt(0)
	v_add_f32_e64 v20, v20, v36
	v_add_f32_e64 v21, v21, v36
	v_mul_f32_e64 v20, v20, v42
	v_mul_f32_e64 v21, v21, v43
	v_lshlrev_b32_e32 v42, 16, v139
	v_and_b32_e32 v43, 0xffff0000, v139
	v_pk_add_f32 v[22:23], v[22:23], v[36:37] op_sel_hi:[1,0]
	v_cvt_pk_bf16_f32 v20, v20, v21
	v_pk_mul_f32 v[22:23], v[22:23], v[42:43]
	s_nop 1
	v_pk_add_f32 v[4:5], v[4:5], v[36:37] op_sel_hi:[1,0]
	v_cvt_pk_bf16_f32 v21, v22, v23
	v_add_co_u32_e32 v22, vcc, s73, v38
	v_pk_add_f32 v[6:7], v[6:7], v[36:37] op_sel_hi:[1,0]
	s_nop 0
	v_addc_co_u32_e32 v23, vcc, 0, v39, vcc
	global_store_dwordx2 v[22:23], v[20:21], off offset:3072
	v_lshlrev_b32_e32 v20, 16, v136
	v_and_b32_e32 v21, 0xffff0000, v136
	v_pk_add_f32 v[22:23], v[24:25], v[36:37] op_sel_hi:[1,0]
	v_pk_add_f32 v[24:25], v[26:27], v[36:37] op_sel_hi:[1,0]
	v_pk_mul_f32 v[20:21], v[22:23], v[20:21]
	v_lshlrev_b32_e32 v22, 16, v137
	v_and_b32_e32 v23, 0xffff0000, v137
	v_pk_mul_f32 v[22:23], v[24:25], v[22:23]
	v_cvt_pk_bf16_f32 v20, v20, v21
	v_cvt_pk_bf16_f32 v21, v22, v23
	global_store_dwordx2 v[40:41], v[20:21], off offset:16
	v_lshlrev_b32_e32 v20, 16, v134
	v_and_b32_e32 v21, 0xffff0000, v134
	v_pk_add_f32 v[22:23], v[28:29], v[36:37] op_sel_hi:[1,0]
	v_pk_add_f32 v[24:25], v[30:31], v[36:37] op_sel_hi:[1,0]
	v_pk_mul_f32 v[20:21], v[22:23], v[20:21]
	v_lshlrev_b32_e32 v22, 16, v135
	v_and_b32_e32 v23, 0xffff0000, v135
	v_pk_mul_f32 v[22:23], v[24:25], v[22:23]
	v_cvt_pk_bf16_f32 v20, v20, v21
	v_cvt_pk_bf16_f32 v21, v22, v23
	global_store_dwordx2 v[40:41], v[20:21], off offset:32
	v_lshlrev_b32_e32 v20, 16, v132
	v_and_b32_e32 v21, 0xffff0000, v132
	v_pk_add_f32 v[22:23], v[32:33], v[36:37] op_sel_hi:[1,0]
	v_pk_add_f32 v[24:25], v[34:35], v[36:37] op_sel_hi:[1,0]
	v_pk_mul_f32 v[20:21], v[22:23], v[20:21]
	v_lshlrev_b32_e32 v22, 16, v133
	v_and_b32_e32 v23, 0xffff0000, v133
	v_pk_mul_f32 v[22:23], v[24:25], v[22:23]
	v_cvt_pk_bf16_f32 v20, v20, v21
	v_cvt_pk_bf16_f32 v21, v22, v23
	global_store_dwordx2 v[40:41], v[20:21], off offset:48
	v_lshlrev_b32_e32 v20, 16, v130
	v_and_b32_e32 v21, 0xffff0000, v130
	v_pk_mul_f32 v[4:5], v[4:5], v[20:21]
	v_lshlrev_b32_e32 v20, 16, v131
	v_and_b32_e32 v21, 0xffff0000, v131
	v_pk_mul_f32 v[6:7], v[6:7], v[20:21]
	v_cvt_pk_bf16_f32 v4, v4, v5
	v_cvt_pk_bf16_f32 v5, v6, v7
	global_store_dwordx2 v[40:41], v[4:5], off offset:64
	v_lshlrev_b32_e32 v4, 16, v128
	v_and_b32_e32 v5, 0xffff0000, v128
	v_pk_add_f32 v[6:7], v[8:9], v[36:37] op_sel_hi:[1,0]
	v_pk_add_f32 v[8:9], v[10:11], v[36:37] op_sel_hi:[1,0]
	v_pk_mul_f32 v[4:5], v[6:7], v[4:5]
	v_lshlrev_b32_e32 v6, 16, v129
	v_and_b32_e32 v7, 0xffff0000, v129
	v_pk_mul_f32 v[6:7], v[8:9], v[6:7]
	v_cvt_pk_bf16_f32 v4, v4, v5
	v_cvt_pk_bf16_f32 v5, v6, v7
	global_store_dwordx2 v[40:41], v[4:5], off offset:80
	v_lshlrev_b32_e32 v4, 16, v126
	v_and_b32_e32 v5, 0xffff0000, v126
	v_pk_add_f32 v[6:7], v[12:13], v[36:37] op_sel_hi:[1,0]
	v_pk_add_f32 v[8:9], v[14:15], v[36:37] op_sel_hi:[1,0]
	v_pk_mul_f32 v[4:5], v[6:7], v[4:5]
	v_lshlrev_b32_e32 v6, 16, v127
	v_and_b32_e32 v7, 0xffff0000, v127
	v_pk_mul_f32 v[6:7], v[8:9], v[6:7]
	v_cvt_pk_bf16_f32 v4, v4, v5
	v_cvt_pk_bf16_f32 v5, v6, v7
	global_store_dwordx2 v[40:41], v[4:5], off offset:96
	v_lshlrev_b32_e32 v4, 16, v124
	v_and_b32_e32 v5, 0xffff0000, v124
	v_pk_add_f32 v[6:7], v[16:17], v[36:37] op_sel_hi:[1,0]
	v_pk_add_f32 v[8:9], v[18:19], v[36:37] op_sel_hi:[1,0]
	v_pk_mul_f32 v[4:5], v[6:7], v[4:5]
	v_lshlrev_b32_e32 v6, 16, v125
	v_and_b32_e32 v7, 0xffff0000, v125
	v_pk_mul_f32 v[6:7], v[8:9], v[6:7]
	v_cvt_pk_bf16_f32 v4, v4, v5
	v_cvt_pk_bf16_f32 v5, v6, v7
	global_store_dwordx2 v[40:41], v[4:5], off offset:112

.LBB0_814:
	s_waitcnt vmcnt(0) lgkmcnt(0)
	s_barrier
	s_and_saveexec_b64 s[6:7], s[4:5]
	s_cbranch_execz .LBB0_453
	v_add_u32_e32 v2, s3, v243
	v_cmp_eq_u32_e32 vcc, -1, v176
	s_nop 1
	v_cndmask_b32_e32 v176, v176, v2, vcc
	v_mov_b32_e32 v2, s70
	ds_write_b32 v2, v176
	v_mov_b32_e32 v2, s48
	ds_write_b32 v2, v177
	s_branch .LBB0_453

.LBB0_971:
	s_and_b64 vcc, exec, s[8:9]
	s_cbranch_vccz .LBB0_981
	v_mov_b32_e32 v130, 0x7f8
	s_and_saveexec_b64 s[6:7], s[4:5]
	s_cbranch_execz .LBB0_976
	s_mov_b64 s[10:11], exec
	v_mbcnt_lo_u32_b32 v2, s10, 0
	v_mbcnt_hi_u32_b32 v2, s11, v2
	v_cmp_eq_u32_e32 vcc, 0, v2
	s_and_saveexec_b64 s[8:9], vcc
	s_cbranch_execz .LBB0_975
	s_bcnt1_i32_b64 s10, s[10:11]
	v_mov_b32_e32 v3, s10
	global_atomic_add v243, v163, v3, s[26:27] sc0
.LBB0_975:
	s_or_b64 exec, exec, s[8:9]
	v_mov_b32_e32 v130, -1

; #define GAS __attribute__((address_space(1)))
; __device__ __forceinline__ void tr_load(const TrBlk& t, int wave, int lane, f32x4 (&v)[16]) {
; #pragma unroll
;     for (int i = 0; i < 16; ++i) v[i] = __builtin_nontemporal_load((const f32x4 GAS*)((const char GAS*)t.src + (size_t)(16 * wave + i) * t.N * 4 + 16u * lane));
; }
.LBB0_997:
	s_ashr_i32 s24, s74, 6
	s_add_u32 s10, s10, s58
	s_addc_u32 s11, s11, s59
	s_and_b64 s[58:59], s[6:7], exec
	s_cselect_b32 s19, s82, 0x1b200000
	s_and_b64 s[54:55], s[54:55], exec
	s_cselect_b32 s19, 0x2200000, s19
	s_and_b64 s[54:55], s[56:57], exec
	s_cselect_b32 s19, 0x400000, s19
	s_add_u32 s58, s50, s19
	s_addc_u32 s59, s51, 0
	s_cmp_eq_u32 s18, 2
	s_cselect_b64 s[54:55], -1, 0
	s_and_b64 s[54:55], s[12:13], s[54:55]
	s_and_b64 s[54:55], s[54:55], exec
	s_cselect_b32 s19, s81, 0x800
	s_and_b64 s[54:55], s[12:13], exec
	s_cselect_b32 s54, s97, 0
	s_mul_i32 s60, s19, s54
	s_mul_hi_i32 s61, s19, s54
	s_and_b64 s[54:55], s[6:7], exec
	s_cselect_b32 s62, 0x600, s78
	s_and_b64 s[54:55], s[56:57], exec
	s_cselect_b32 s54, 0xf00, s62
	s_mul_i32 s55, s61, s54
	s_mul_hi_u32 s56, s60, s54
	s_add_i32 s56, s56, s55
	s_mul_i32 s54, s60, s54
	s_add_u32 s54, s58, s54
	s_mul_i32 s96, s96, 48
	s_addc_u32 s55, s59, s56
	s_sub_i32 s56, s95, s96
	s_and_b64 s[12:13], s[12:13], exec
	s_cselect_b32 s56, s56, s94
	s_abs_i32 s57, s93
	v_cvt_f32_u32_e32 v2, s57
	s_sub_i32 s58, 0, s57
	s_abs_i32 s13, s56
	s_xor_b32 s12, s56, s93
	v_rcp_iflag_f32_e32 v2, v2
	s_ashr_i32 s12, s12, 31
	s_load_dwordx2 s[10:11], s[10:11], 0x0
	s_mul_i32 s61, s61, s35
	v_mul_f32_e32 v2, 0x4f7ffffe, v2
	v_cvt_u32_f32_e32 v2, v2
	s_mul_i32 s91, s91, 48
	v_and_b32_e32 v133, 63, v131
	v_lshlrev_b32_e32 v132, 4, v133
	v_readfirstlane_b32 s59, v2
	s_mul_i32 s58, s58, s59
	s_mul_hi_u32 s58, s59, s58
	s_add_i32 s59, s59, s58
	s_mul_hi_u32 s58, s13, s59
	s_mul_i32 s59, s58, s57
	s_sub_i32 s13, s13, s59
	s_add_i32 s59, s58, 1
	s_sub_i32 s62, s13, s57
	s_cmp_ge_u32 s13, s57
	s_cselect_b32 s58, s59, s58
	s_cselect_b32 s13, s62, s13
	s_add_i32 s59, s58, 1
	s_cmp_ge_u32 s13, s57
	s_cselect_b32 s13, s59, s58
	s_xor_b32 s13, s13, s12
	s_sub_i32 s57, s13, s12
	s_lshl_b32 s58, s57, 7
	s_ashr_i32 s13, s58, 31
	s_add_u32 s12, s54, s58
	s_mul_hi_u32 s54, s60, s35
	s_addc_u32 s13, s55, s13
	s_add_i32 s55, s54, s61
	s_mul_i32 s54, s60, s35
	s_lshl_b64 s[54:55], s[54:55], 2
	s_waitcnt lgkmcnt(0)
	s_add_u32 s54, s10, s54
	s_addc_u32 s55, s11, s55
	s_mul_hi_i32 s11, s58, s35
	s_mul_i32 s10, s58, s35
	s_lshl_b64 s[10:11], s[10:11], 2
	s_add_u32 s58, s54, s10
	s_mul_i32 s57, s57, s93
	s_addc_u32 s59, s55, s11
	s_sub_i32 s10, s56, s57
	s_lshl_b32 s10, s10, 8
	s_ashr_i32 s11, s10, 31
	s_lshl_b64 s[54:55], s[10:11], 2
	s_add_u32 s54, s58, s54
	s_addc_u32 s55, s59, s55
	s_and_b64 s[56:57], s[8:9], exec
	s_cselect_b32 s11, s82, 0x1b200000
	s_and_b64 s[46:47], s[46:47], exec
	s_cselect_b32 s11, 0x2200000, s11
	s_and_b64 s[46:47], s[48:49], exec
	s_cselect_b32 s11, 0x400000, s11
	s_add_u32 s50, s50, s11
	s_addc_u32 s51, s51, 0
	s_cmp_eq_u32 s34, 2
	s_cselect_b64 s[46:47], -1, 0
	s_and_b64 s[46:47], s[44:45], s[46:47]
	s_and_b64 s[46:47], s[46:47], exec
	s_cselect_b32 s11, s81, 0x800
	s_and_b64 s[46:47], s[44:45], exec
	s_cselect_b32 s46, s92, 0
	s_mul_i32 s56, s11, s46
	s_mul_hi_i32 s57, s11, s46
	s_and_b64 s[46:47], s[8:9], exec
	s_cselect_b32 s58, 0x600, s78
	s_and_b64 s[46:47], s[48:49], exec
	s_cselect_b32 s46, 0xf00, s58
	s_mul_i32 s47, s57, s46
	s_mul_hi_u32 s48, s56, s46
	s_add_i32 s48, s48, s47
	s_mul_i32 s46, s56, s46
	s_add_u32 s46, s50, s46
	s_addc_u32 s47, s51, s48
	s_sub_i32 s48, s90, s91
	s_and_b64 s[44:45], s[44:45], exec
	s_cselect_b32 s48, s48, s89
	s_abs_i32 s49, s88
	v_cvt_f32_u32_e32 v2, s49
	s_sub_i32 s50, 0, s49
	s_abs_i32 s45, s48
	s_xor_b32 s44, s48, s88
	v_rcp_iflag_f32_e32 v2, v2
	s_ashr_i32 s44, s44, 31
	s_mul_i32 s57, s57, s43
	v_mov_b32_e32 v134, 0
	v_mul_f32_e32 v2, 0x4f7ffffe, v2
	v_cvt_u32_f32_e32 v2, v2
	v_mov_b32_e32 v135, 0
	v_mov_b32_e32 v136, 0
	v_mov_b32_e32 v137, 0
	v_readfirstlane_b32 s51, v2
	s_mul_i32 s50, s50, s51
	s_mul_hi_u32 s50, s51, s50
	s_add_i32 s51, s51, s50
	s_mul_hi_u32 s50, s45, s51
	s_mul_i32 s51, s50, s49
	s_sub_i32 s45, s45, s51
	s_add_i32 s51, s50, 1
	s_sub_i32 s58, s45, s49
	s_cmp_ge_u32 s45, s49
	s_cselect_b32 s50, s51, s50
	s_cselect_b32 s45, s58, s45
	s_add_i32 s51, s50, 1
	s_cmp_ge_u32 s45, s49
	s_cselect_b32 s45, s51, s50
	s_xor_b32 s45, s45, s44
	s_sub_i32 s49, s45, s44
	s_lshl_b32 s50, s49, 7
	s_ashr_i32 s44, s50, 31
	s_add_u32 s46, s46, s50
	s_addc_u32 s47, s47, s44
	s_mul_hi_u32 s44, s56, s43
	s_add_i32 s45, s44, s57
	s_mul_i32 s44, s56, s43
	s_lshl_b64 s[44:45], s[44:45], 2
	s_add_u32 s51, s52, s44
	s_addc_u32 s52, s53, s45
	s_mul_hi_i32 s45, s50, s43
	s_mul_i32 s44, s50, s43
	s_lshl_b64 s[44:45], s[44:45], 2
	s_add_u32 s50, s51, s44
	s_mul_i32 s49, s49, s88
	s_addc_u32 s51, s52, s45
	s_sub_i32 s44, s48, s49
	s_lshl_b32 s44, s44, 8
	s_ashr_i32 s45, s44, 31
	s_lshl_b64 s[48:49], s[44:45], 2
	s_add_u32 s50, s50, s48
	s_addc_u32 s51, s51, s49
	s_and_b32 s52, s74, 0xffffffc0
	s_lshl_b32 s45, s24, 4
	s_mul_i32 s48, s52, s43
	s_mul_hi_i32 s49, s52, s43
	s_add_u32 s48, s50, s48
	s_addc_u32 s49, s51, s49
	s_or_b32 s53, s52, 4
	global_load_dwordx4 v[66:69], v132, s[48:49] nt
	s_mul_i32 s48, s53, s43
	s_mul_hi_i32 s49, s53, s43
	s_add_u32 s48, s50, s48
	s_addc_u32 s49, s51, s49
	s_or_b32 s56, s52, 8
	global_load_dwordx4 v[70:73], v132, s[48:49] nt
	s_mul_i32 s48, s56, s43
	s_mul_hi_i32 s49, s56, s43
	s_add_u32 s48, s50, s48
	s_addc_u32 s49, s51, s49
	s_or_b32 s57, s52, 12
	global_load_dwordx4 v[74:77], v132, s[48:49] nt
	s_mul_i32 s48, s57, s43
	s_mul_hi_i32 s49, s57, s43
	s_add_u32 s48, s50, s48
	s_addc_u32 s49, s51, s49
	s_or_b32 s58, s52, 16
	global_load_dwordx4 v[82:85], v132, s[48:49] nt
	s_mul_i32 s48, s58, s43
	s_mul_hi_i32 s49, s58, s43
	s_add_u32 s48, s50, s48
	s_addc_u32 s49, s51, s49
	s_or_b32 s59, s52, 20
	global_load_dwordx4 v[78:81], v132, s[48:49] nt
; #define LAS __attribute__((address_space(3)))
; #define GAS __attribute__((address_space(1)))
; __device__ __forceinline__ unsigned pk4_fp8(float a, float b, float c, float d) { int p = 0; p = __builtin_amdgcn_cvt_pk_fp8_f32(a, b, p, false); p = __builtin_amdgcn_cvt_pk_fp8_f32(c, d, p, true); return (unsigned)p; }
; #define WG_BAR() do { LDS_WAIT(); __builtin_amdgcn_s_barrier(); asm volatile("" ::: "memory"); } while (0)
; __device__ __forceinline__ void tr_load(const TrBlk& t, int wave, int lane, f32x4 (&v)[16]) {
; #pragma unroll
;     for (int i = 0; i < 16; ++i) v[i] = __builtin_nontemporal_load((const f32x4 GAS*)((const char GAS*)t.src + (size_t)(16 * wave + i) * t.N * 4 + 16u * lane));
; }
; __device__ __forceinline__ void tr_pack(LAS unsigned char* buf, int wave, int lane, const f32x4 (&v)[16]) {
; #pragma unroll
;     for (int j = 0; j < 4; ++j) { u32x4 o;
; #pragma unroll
;         for (int w = 0; w < 4; ++w) o[w] = pk4_fp8(64.f * v[4 * w][j], 64.f * v[4 * w + 1][j], 64.f * v[4 * w + 2][j], 64.f * v[4 * w + 3][j]);
;         *(LAS u32x4*)(buf + (4 * lane + j) * TRP + 16 * wave) = o; }
; }
; template <int NBK> __device__ __forceinline__ void tr_blocks(Ctx& C, int L, int b0) {
;     ...
;     const TrBlk t0 = tr_decode(C, L, b0), t1 = tr_decode(C, L, b0 + (NBK > 1 ? 1 : 0)), t2 = tr_decode(C, L, b0 + (NBK > 2 ? 2 : 0)), t3 = tr_decode(C, L, b0 + (NBK > 3 ? 3 : 0));
;     tr_load(t0, C.wave, C.lane, r0); if (NBK > 1) tr_load(t1, C.wave, C.lane, r1); if (NBK > 2) tr_load(t2, C.wave, C.lane, r2);
;     WG_BAR();
;     tr_pack(buf0, C.wave, C.lane, r0);
;     if (NBK > 3) tr_load(t3, C.wave, C.lane, r0);
;     WG_BAR(); tr_flush(t0, buf0, C.wave, C.lane);
	s_mul_i32 s48, s59, s43
	s_mul_hi_i32 s49, s59, s43
	s_add_u32 s48, s50, s48
	s_addc_u32 s49, s51, s49
	s_or_b32 s60, s52, 24
	global_load_dwordx4 v[86:89], v132, s[48:49] nt
	s_mul_i32 s48, s60, s43
	s_mul_hi_i32 s49, s60, s43
	s_add_u32 s48, s50, s48
	s_addc_u32 s49, s51, s49
	s_or_b32 s61, s52, 28
	global_load_dwordx4 v[94:97], v132, s[48:49] nt
	s_mul_i32 s48, s61, s43
	s_mul_hi_i32 s49, s61, s43
	s_add_u32 s48, s50, s48
	s_addc_u32 s49, s51, s49
	s_or_b32 s62, s52, 32
	global_load_dwordx4 v[102:105], v132, s[48:49] nt
	s_mul_i32 s48, s62, s43
	s_mul_hi_i32 s49, s62, s43
	s_add_u32 s48, s50, s48
	s_addc_u32 s49, s51, s49
	s_or_b32 s63, s52, 36
	global_load_dwordx4 v[90:93], v132, s[48:49] nt
	s_mul_i32 s48, s63, s43
	s_mul_hi_i32 s49, s63, s43
	s_add_u32 s48, s50, s48
	s_addc_u32 s49, s51, s49
	s_or_b32 s74, s52, 40
	global_load_dwordx4 v[98:101], v132, s[48:49] nt
	s_mul_i32 s48, s74, s43
	s_mul_hi_i32 s49, s74, s43
	s_add_u32 s48, s50, s48
	s_addc_u32 s49, s51, s49
	s_or_b32 s88, s52, 44
	global_load_dwordx4 v[106:109], v132, s[48:49] nt
	s_mul_i32 s48, s88, s43
	s_mul_hi_i32 s49, s88, s43
	s_add_u32 s48, s50, s48
	s_addc_u32 s49, s51, s49
	s_or_b32 s89, s52, 48
	global_load_dwordx4 v[114:117], v132, s[48:49] nt
	s_mul_i32 s48, s89, s43
	s_mul_hi_i32 s49, s89, s43
	s_add_u32 s48, s50, s48
	s_addc_u32 s49, s51, s49
	s_or_b32 s90, s52, 52
	global_load_dwordx4 v[110:113], v132, s[48:49] nt
	s_mul_i32 s48, s90, s43
	s_mul_hi_i32 s49, s90, s43
	s_add_u32 s48, s50, s48
	s_addc_u32 s49, s51, s49
	s_or_b32 s91, s52, 56
	global_load_dwordx4 v[118:121], v132, s[48:49] nt
	s_mul_i32 s48, s91, s43
	s_mul_hi_i32 s49, s91, s43
	s_add_u32 s48, s50, s48
	s_addc_u32 s49, s51, s49
	s_or_b32 s92, s52, 60
	global_load_dwordx4 v[122:125], v132, s[48:49] nt
	s_mul_hi_i32 s49, s92, s43
	s_mul_i32 s43, s92, s43
	s_add_u32 s48, s50, s43
	s_addc_u32 s49, s51, s49
	global_load_dwordx4 v[126:129], v132, s[48:49] nt
	s_mul_hi_i32 s43, s52, s35
	s_mul_i32 s52, s52, s35
	s_add_u32 s48, s54, s52
	s_addc_u32 s49, s55, s43
	s_mul_hi_i32 s43, s53, s35
	s_mul_i32 s53, s53, s35
	global_load_dwordx4 v[2:5], v132, s[48:49] nt
	s_add_u32 s48, s54, s53
	s_addc_u32 s49, s55, s43
	s_mul_hi_i32 s43, s56, s35
	s_mul_i32 s56, s56, s35
	global_load_dwordx4 v[6:9], v132, s[48:49] nt
	s_add_u32 s48, s54, s56
	s_addc_u32 s49, s55, s43
	s_mul_hi_i32 s43, s57, s35
	s_mul_i32 s57, s57, s35
	global_load_dwordx4 v[10:13], v132, s[48:49] nt
	s_add_u32 s48, s54, s57
	s_addc_u32 s49, s55, s43
	s_mul_hi_i32 s43, s58, s35
	s_mul_i32 s58, s58, s35
	global_load_dwordx4 v[18:21], v132, s[48:49] nt
	s_add_u32 s48, s54, s58
	s_addc_u32 s49, s55, s43
	s_mul_hi_i32 s43, s59, s35
	s_mul_i32 s59, s59, s35
	global_load_dwordx4 v[14:17], v132, s[48:49] nt
	s_add_u32 s48, s54, s59
	s_addc_u32 s49, s55, s43
	s_mul_hi_i32 s43, s60, s35
	s_mul_i32 s60, s60, s35
	global_load_dwordx4 v[26:29], v132, s[48:49] nt
	s_add_u32 s48, s54, s60
	s_addc_u32 s49, s55, s43
	s_mul_hi_i32 s43, s61, s35
	s_mul_i32 s61, s61, s35
	global_load_dwordx4 v[30:33], v132, s[48:49] nt
	s_add_u32 s48, s54, s61
	s_addc_u32 s49, s55, s43
	s_mul_hi_i32 s43, s62, s35
	s_mul_i32 s62, s62, s35
	global_load_dwordx4 v[42:45], v132, s[48:49] nt
	s_add_u32 s48, s54, s62
	s_addc_u32 s49, s55, s43
	s_mul_hi_i32 s43, s63, s35
	s_mul_i32 s63, s63, s35
	global_load_dwordx4 v[22:25], v132, s[48:49] nt
	s_add_u32 s48, s54, s63
	s_addc_u32 s49, s55, s43
	s_mul_hi_i32 s43, s74, s35
	s_mul_i32 s74, s74, s35
	global_load_dwordx4 v[34:37], v132, s[48:49] nt
	s_add_u32 s48, s54, s74
	s_addc_u32 s49, s55, s43
	s_mul_hi_i32 s43, s88, s35
	s_mul_i32 s88, s88, s35
	global_load_dwordx4 v[38:41], v132, s[48:49] nt
	s_add_u32 s48, s54, s88
	s_addc_u32 s49, s55, s43
	s_mul_hi_i32 s43, s89, s35
	s_mul_i32 s89, s89, s35
	global_load_dwordx4 v[50:53], v132, s[48:49] nt
	s_add_u32 s48, s54, s89
	s_waitcnt vmcnt(0)
	v_mul_f32_e32 v66, 0x42800000, v66
	v_mul_f32_e32 v70, 0x42800000, v70
	s_addc_u32 s49, s55, s43
	s_mul_hi_i32 s43, s90, s35
	s_mul_i32 s90, s90, s35
	v_cvt_pk_fp8_f32 v134, v66, v70
	v_mul_f32_e32 v66, 0x42800000, v78
	v_mul_f32_e32 v70, 0x42800000, v86
	global_load_dwordx4 v[46:49], v132, s[48:49] nt
	s_add_u32 s48, s54, s90
	v_cvt_pk_fp8_f32 v135, v66, v70
	v_mul_f32_e32 v66, 0x42800000, v90
	v_mul_f32_e32 v70, 0x42800000, v98
	s_addc_u32 s49, s55, s43
	s_mul_hi_i32 s43, s91, s35
	s_mul_i32 s91, s91, s35
	v_cvt_pk_fp8_f32 v136, v66, v70
	v_mul_f32_e32 v66, 0x42800000, v110
	v_mul_f32_e32 v70, 0x42800000, v118
	global_load_dwordx4 v[54:57], v132, s[48:49] nt
	s_add_u32 s48, s54, s91
	v_mul_f32_e32 v74, 0x42800000, v74
	v_mul_f32_e32 v82, 0x42800000, v82
	v_cvt_pk_fp8_f32 v137, v66, v70
	s_addc_u32 s49, s55, s43
	s_mul_hi_i32 s43, s92, s35
	s_mul_i32 s92, s92, s35
	v_cvt_pk_fp8_f32 v134, v74, v82 op_sel:[0,0,1]
	v_mul_f32_e32 v74, 0x42800000, v94
	v_mul_f32_e32 v78, 0x42800000, v102
	global_load_dwordx4 v[58:61], v132, s[48:49] nt
	s_add_u32 s48, s54, s92
	v_cvt_pk_fp8_f32 v135, v74, v78 op_sel:[0,0,1]
	v_mul_f32_e32 v74, 0x42800000, v106
	v_mul_f32_e32 v78, 0x42800000, v114
	s_addc_u32 s49, s55, s43
	v_cvt_pk_fp8_f32 v136, v74, v78 op_sel:[0,0,1]
	v_mul_f32_e32 v74, 0x42800000, v122
	v_mul_f32_e32 v78, 0x42800000, v126
	global_load_dwordx4 v[62:65], v132, s[48:49] nt
	v_cvt_pk_fp8_f32 v137, v74, v78 op_sel:[0,0,1]
	s_add_i32 s35, s45, 0
	v_mov_b32_e32 v66, s35
	s_movk_i32 s35, 0x240
	v_mad_u32_u24 v66, v133, s35, v66
	s_waitcnt lgkmcnt(0)
	s_barrier
; #define LAS __attribute__((address_space(3)))
; #define GAS __attribute__((address_space(1)))
; __device__ __forceinline__ unsigned pk4_fp8(float a, float b, float c, float d) { int p = 0; p = __builtin_amdgcn_cvt_pk_fp8_f32(a, b, p, false); p = __builtin_amdgcn_cvt_pk_fp8_f32(c, d, p, true); return (unsigned)p; }
; __device__ __forceinline__ void tr_pack(LAS unsigned char* buf, int wave, int lane, const f32x4 (&v)[16]) {
; #pragma unroll
;     for (int j = 0; j < 4; ++j) { u32x4 o;
; #pragma unroll
;         for (int w = 0; w < 4; ++w) o[w] = pk4_fp8(64.f * v[4 * w][j], 64.f * v[4 * w + 1][j], 64.f * v[4 * w + 2][j], 64.f * v[4 * w + 3][j]);
;         *(LAS u32x4*)(buf + (4 * lane + j) * TRP + 16 * wave) = o; }
; }
; __device__ __forceinline__ void tr_flush(const TrBlk& t, const LAS unsigned char* buf, int wave, int lane) {
; #pragma unroll
;     for (int tt = 0; tt < 4; ++tt) { const int nl = 32 * wave + 8 * tt + (lane >> 3), n = 256 * t.nb + nl;
;         const u32x4 o = *(const LAS u32x4*)(buf + nl * TRP + 16 * (lane & 7));
;         const int drow = t.gu ? ((n >> 7) * 256 + (n & 127) + 128 * t.which) : n;
;         __builtin_nontemporal_store(o, (u32x4 GAS*)(t.dst + (size_t)drow * t.K + 16 * (lane & 7))); }
; }
	ds_write_b128 v66, v[134:137]
	v_mul_f32_e32 v67, 0x42800000, v67
	v_mul_f32_e32 v70, 0x42800000, v71
	v_mov_b32_e32 v134, 0
	v_cvt_pk_fp8_f32 v134, v67, v70
	v_mul_f32_e32 v67, 0x42800000, v79
	v_mul_f32_e32 v70, 0x42800000, v87
	v_mov_b32_e32 v135, 0
	v_cvt_pk_fp8_f32 v135, v67, v70
	v_mul_f32_e32 v67, 0x42800000, v91
	v_mul_f32_e32 v70, 0x42800000, v99
	v_mov_b32_e32 v136, 0
	v_cvt_pk_fp8_f32 v136, v67, v70
	v_mul_f32_e32 v67, 0x42800000, v111
	v_mul_f32_e32 v70, 0x42800000, v119
	v_mov_b32_e32 v137, 0
	v_mul_f32_e32 v71, 0x42800000, v75
	v_mul_f32_e32 v74, 0x42800000, v83
	v_cvt_pk_fp8_f32 v137, v67, v70
	v_cvt_pk_fp8_f32 v134, v71, v74 op_sel:[0,0,1]
	v_mul_f32_e32 v71, 0x42800000, v95
	v_mul_f32_e32 v74, 0x42800000, v103
	v_cvt_pk_fp8_f32 v135, v71, v74 op_sel:[0,0,1]
	v_mul_f32_e32 v71, 0x42800000, v107
	v_mul_f32_e32 v74, 0x42800000, v115
	v_cvt_pk_fp8_f32 v136, v71, v74 op_sel:[0,0,1]
	v_mul_f32_e32 v71, 0x42800000, v123
	v_mul_f32_e32 v74, 0x42800000, v127
	v_cvt_pk_fp8_f32 v137, v71, v74 op_sel:[0,0,1]
	v_mul_f32_e32 v67, 0x42800000, v68
	v_mul_f32_e32 v68, 0x42800000, v72
	v_mul_f32_e32 v70, 0x42800000, v76
	ds_write_b128 v66, v[134:137] offset:144
	v_mov_b32_e32 v134, 0
	v_cvt_pk_fp8_f32 v134, v67, v68
	v_mul_f32_e32 v67, 0x42800000, v80
	v_mul_f32_e32 v68, 0x42800000, v88
	v_mov_b32_e32 v135, 0
	v_cvt_pk_fp8_f32 v135, v67, v68
	v_mul_f32_e32 v67, 0x42800000, v92
	v_mul_f32_e32 v68, 0x42800000, v100
	v_mov_b32_e32 v136, 0
	v_cvt_pk_fp8_f32 v136, v67, v68
	v_mul_f32_e32 v67, 0x42800000, v112
	v_mul_f32_e32 v68, 0x42800000, v120
	v_mov_b32_e32 v137, 0
	v_mul_f32_e32 v71, 0x42800000, v84
	v_cvt_pk_fp8_f32 v137, v67, v68
	v_mul_f32_e32 v67, 0x42800000, v69
	v_mul_f32_e32 v69, 0x42800000, v73
	v_mov_b32_e32 v68, 0
	v_cvt_pk_fp8_f32 v134, v70, v71 op_sel:[0,0,1]
	v_mul_f32_e32 v70, 0x42800000, v96
	v_mul_f32_e32 v71, 0x42800000, v104
	v_cvt_pk_fp8_f32 v68, v67, v69
	v_cvt_pk_fp8_f32 v135, v70, v71 op_sel:[0,0,1]
	v_mul_f32_e32 v70, 0x42800000, v108
	v_mul_f32_e32 v71, 0x42800000, v116
	v_cvt_pk_fp8_f32 v136, v70, v71 op_sel:[0,0,1]
	v_mul_f32_e32 v70, 0x42800000, v124
	v_mul_f32_e32 v71, 0x42800000, v128
	v_cvt_pk_fp8_f32 v137, v70, v71 op_sel:[0,0,1]
	v_mul_f32_e32 v70, 0x42800000, v77
	v_mul_f32_e32 v71, 0x42800000, v85
	v_cvt_pk_fp8_f32 v68, v70, v71 op_sel:[0,0,1]
	v_mul_f32_e32 v67, 0x42800000, v81
	v_mul_f32_e32 v70, 0x42800000, v89
	v_mov_b32_e32 v69, 0
	v_cvt_pk_fp8_f32 v69, v67, v70
	v_mul_f32_e32 v71, 0x42800000, v97
	v_mul_f32_e32 v72, 0x42800000, v105
	v_mul_f32_e32 v67, 0x42800000, v93
	v_cvt_pk_fp8_f32 v69, v71, v72 op_sel:[0,0,1]
	v_mul_f32_e32 v71, 0x42800000, v101
	v_mov_b32_e32 v70, 0
	v_cvt_pk_fp8_f32 v70, v67, v71
	v_mul_f32_e32 v72, 0x42800000, v109
	v_mul_f32_e32 v73, 0x42800000, v117
	v_mul_f32_e32 v67, 0x42800000, v113
	v_cvt_pk_fp8_f32 v70, v72, v73 op_sel:[0,0,1]
	v_mul_f32_e32 v72, 0x42800000, v121
	v_mov_b32_e32 v71, 0
	v_cvt_pk_fp8_f32 v71, v67, v72
	v_mul_f32_e32 v73, 0x42800000, v125
	v_mul_f32_e32 v74, 0x42800000, v129
	s_lshl_b32 s24, s24, 5
	v_cvt_pk_fp8_f32 v71, v73, v74 op_sel:[0,0,1]
	v_bfe_u32 v67, v131, 3, 3
	v_or_b32_e32 v76, s24, v67
	s_movk_i32 s35, 0x90
	ds_write_b128 v66, v[134:137] offset:288
	ds_write_b128 v66, v[68:71] offset:432
	v_and_b32_e32 v162, 0x70, v132
	v_add_u32_e32 v72, s44, v76
	v_mul_lo_u32 v68, v76, s35
	s_waitcnt lgkmcnt(0)
	s_barrier
	v_add3_u32 v77, 0, v162, v68
	v_lshlrev_b32_e32 v73, 1, v72
	v_bitop3_b32 v67, s24, v211, v67 bitop3:0xc8
	s_lshl_b32 s24, s34, 7
	ds_read_b128 v[68:71], v77
	v_and_b32_e32 v73, 0xffffff00, v73
	v_or_b32_e32 v74, s24, v67
	v_add_u32_e32 v73, v74, v73
	v_cndmask_b32_e64 v74, v72, v73, s[8:9]
	v_mov_b64_e32 v[72:73], s[46:47]
	v_mad_i64_i32 v[74:75], s[34:35], s11, v74, v[72:73]
	v_lshl_add_u64 v[74:75], v[74:75], 0, v[162:163]
	v_or_b32_e32 v78, 8, v76
	s_waitcnt lgkmcnt(0)
	global_store_dwordx4 v[74:75], v[68:71], off nt
	v_add_u32_e32 v74, s44, v78
	v_lshlrev_b32_e32 v75, 1, v74
	v_bitop3_b32 v79, v76, s83, 8 bitop3:0xc8
	ds_read_b128 v[68:71], v77 offset:1152
	v_and_b32_e32 v75, 0xffffff00, v75
	v_or_b32_e32 v80, s24, v79
	v_add_u32_e32 v75, v80, v75
	v_cndmask_b32_e64 v74, v74, v75, s[8:9]
	v_mad_i64_i32 v[74:75], s[34:35], s11, v74, v[72:73]
	v_lshl_add_u64 v[74:75], v[74:75], 0, v[162:163]
	v_or_b32_e32 v80, 16, v76
	s_waitcnt lgkmcnt(0)
	global_store_dwordx4 v[74:75], v[68:71], off nt
	v_add_u32_e32 v74, s44, v80
	v_lshlrev_b32_e32 v75, 1, v74
	v_bitop3_b32 v81, v76, s84, 16 bitop3:0xc8
	ds_read_b128 v[68:71], v77 offset:2304
	v_and_b32_e32 v75, 0xffffff00, v75
	v_or_b32_e32 v82, s24, v81
	v_add_u32_e32 v75, v82, v75
	v_cndmask_b32_e64 v74, v74, v75, s[8:9]
	v_mad_i64_i32 v[74:75], s[34:35], s11, v74, v[72:73]
	v_lshl_add_u64 v[74:75], v[74:75], 0, v[162:163]
	s_waitcnt lgkmcnt(0)
	global_store_dwordx4 v[74:75], v[68:71], off nt
	v_or_b32_e32 v74, 24, v76
	v_add_u32_e32 v75, s44, v74
	s_movk_i32 s34, 0x7f
	v_lshlrev_b32_e32 v82, 1, v75
	v_bitop3_b32 v83, v76, s34, 24 bitop3:0xc8
	ds_read_b128 v[68:71], v77 offset:3456
	v_and_b32_e32 v82, 0xffffff00, v82
	v_or_b32_e32 v84, s24, v83
	v_add_u32_e32 v82, v84, v82
	v_cndmask_b32_e64 v75, v75, v82, s[8:9]
	v_mad_i64_i32 v[72:73], s[8:9], s11, v75, v[72:73]
	v_lshl_add_u64 v[72:73], v[72:73], 0, v[162:163]
	s_waitcnt lgkmcnt(0)
	global_store_dwordx4 v[72:73], v[68:71], off nt
	v_mul_f32_e32 v2, 0x42800000, v2
	v_mul_f32_e32 v6, 0x42800000, v6
	v_mov_b32_e32 v68, v163
	v_cvt_pk_fp8_f32 v68, v2, v6
	v_mul_f32_e32 v2, 0x42800000, v14
	v_mul_f32_e32 v6, 0x42800000, v26
	v_mov_b32_e32 v69, v163
	v_cvt_pk_fp8_f32 v69, v2, v6
	v_mul_f32_e32 v2, 0x42800000, v22
	v_mul_f32_e32 v6, 0x42800000, v34
	v_mov_b32_e32 v70, v163
	v_cvt_pk_fp8_f32 v70, v2, v6
	s_waitcnt vmcnt(7)
; #define LAS __attribute__((address_space(3)))
; #define GAS __attribute__((address_space(1)))
; __device__ __forceinline__ unsigned pk4_fp8(float a, float b, float c, float d) { int p = 0; p = __builtin_amdgcn_cvt_pk_fp8_f32(a, b, p, false); p = __builtin_amdgcn_cvt_pk_fp8_f32(c, d, p, true); return (unsigned)p; }
; __device__ __forceinline__ void tr_pack(LAS unsigned char* buf, int wave, int lane, const f32x4 (&v)[16]) {
; #pragma unroll
;     for (int j = 0; j < 4; ++j) { u32x4 o;
; #pragma unroll
;         for (int w = 0; w < 4; ++w) o[w] = pk4_fp8(64.f * v[4 * w][j], 64.f * v[4 * w + 1][j], 64.f * v[4 * w + 2][j], 64.f * v[4 * w + 3][j]);
;         *(LAS u32x4*)(buf + (4 * lane + j) * TRP + 16 * wave) = o; }
; }
; __device__ __forceinline__ void tr_flush(const TrBlk& t, const LAS unsigned char* buf, int wave, int lane) {
; #pragma unroll
;     for (int tt = 0; tt < 4; ++tt) { const int nl = 32 * wave + 8 * tt + (lane >> 3), n = 256 * t.nb + nl;
;         const u32x4 o = *(const LAS u32x4*)(buf + nl * TRP + 16 * (lane & 7));
;         const int drow = t.gu ? ((n >> 7) * 256 + (n & 127) + 128 * t.which) : n;
;         __builtin_nontemporal_store(o, (u32x4 GAS*)(t.dst + (size_t)drow * t.K + 16 * (lane & 7))); }
; }
	v_mul_f32_e32 v2, 0x42800000, v46
	s_waitcnt vmcnt(6)
	v_mul_f32_e32 v6, 0x42800000, v54
	v_mov_b32_e32 v71, v163
	v_mul_f32_e32 v10, 0x42800000, v10
	v_mul_f32_e32 v18, 0x42800000, v18
	v_cvt_pk_fp8_f32 v71, v2, v6
	v_cvt_pk_fp8_f32 v68, v10, v18 op_sel:[0,0,1]
	v_mul_f32_e32 v10, 0x42800000, v30
	v_mul_f32_e32 v14, 0x42800000, v42
	v_cvt_pk_fp8_f32 v69, v10, v14 op_sel:[0,0,1]
	v_mul_f32_e32 v10, 0x42800000, v38
	v_mul_f32_e32 v14, 0x42800000, v50
	v_cvt_pk_fp8_f32 v70, v10, v14 op_sel:[0,0,1]
	s_waitcnt vmcnt(5)
	v_mul_f32_e32 v10, 0x42800000, v58
	s_waitcnt vmcnt(4)
	v_mul_f32_e32 v14, 0x42800000, v62
	v_cvt_pk_fp8_f32 v71, v10, v14 op_sel:[0,0,1]
	v_mul_f32_e32 v2, 0x42800000, v3
	v_mul_f32_e32 v3, 0x42800000, v7
	v_mul_f32_e32 v6, 0x42800000, v11
	ds_write_b128 v66, v[68:71] offset:36864
	v_mov_b32_e32 v68, v163
	v_cvt_pk_fp8_f32 v68, v2, v3
	v_mul_f32_e32 v2, 0x42800000, v15
	v_mul_f32_e32 v3, 0x42800000, v27
	v_mov_b32_e32 v69, v163
	v_cvt_pk_fp8_f32 v69, v2, v3
	v_mul_f32_e32 v2, 0x42800000, v23
	v_mul_f32_e32 v3, 0x42800000, v35
	v_mov_b32_e32 v70, v163
	v_cvt_pk_fp8_f32 v70, v2, v3
	v_mul_f32_e32 v2, 0x42800000, v47
	v_mul_f32_e32 v3, 0x42800000, v55
	v_mov_b32_e32 v71, v163
	v_mul_f32_e32 v7, 0x42800000, v19
	v_cvt_pk_fp8_f32 v71, v2, v3
	v_cvt_pk_fp8_f32 v68, v6, v7 op_sel:[0,0,1]
	v_mul_f32_e32 v6, 0x42800000, v31
	v_mul_f32_e32 v7, 0x42800000, v43
	v_cvt_pk_fp8_f32 v69, v6, v7 op_sel:[0,0,1]
	v_mul_f32_e32 v6, 0x42800000, v39
	v_mul_f32_e32 v7, 0x42800000, v51
	v_cvt_pk_fp8_f32 v70, v6, v7 op_sel:[0,0,1]
	v_mul_f32_e32 v6, 0x42800000, v59
	v_mul_f32_e32 v7, 0x42800000, v63
	v_cvt_pk_fp8_f32 v71, v6, v7 op_sel:[0,0,1]
	v_mul_f32_e32 v2, 0x42800000, v4
	v_mul_f32_e32 v3, 0x42800000, v8
	v_mul_f32_e32 v4, 0x42800000, v12
	ds_write_b128 v66, v[68:71] offset:37008
	v_mov_b32_e32 v68, v163
	v_cvt_pk_fp8_f32 v68, v2, v3
	v_mul_f32_e32 v2, 0x42800000, v16
	v_mul_f32_e32 v3, 0x42800000, v28
	v_mov_b32_e32 v69, v163
	v_cvt_pk_fp8_f32 v69, v2, v3
	v_mul_f32_e32 v2, 0x42800000, v24
	v_mul_f32_e32 v3, 0x42800000, v36
	v_mov_b32_e32 v70, v163
	v_cvt_pk_fp8_f32 v70, v2, v3
	v_mul_f32_e32 v2, 0x42800000, v48
	v_mul_f32_e32 v3, 0x42800000, v56
	v_mov_b32_e32 v71, v163
	v_mul_f32_e32 v6, 0x42800000, v20
	v_cvt_pk_fp8_f32 v71, v2, v3
	v_cvt_pk_fp8_f32 v68, v4, v6 op_sel:[0,0,1]
	v_mul_f32_e32 v4, 0x42800000, v32
	v_mul_f32_e32 v6, 0x42800000, v44
	v_cvt_pk_fp8_f32 v69, v4, v6 op_sel:[0,0,1]
	v_mul_f32_e32 v4, 0x42800000, v40
	v_mul_f32_e32 v6, 0x42800000, v52
	v_cvt_pk_fp8_f32 v70, v4, v6 op_sel:[0,0,1]
	v_mul_f32_e32 v4, 0x42800000, v60
	v_mul_f32_e32 v6, 0x42800000, v64
	v_cvt_pk_fp8_f32 v71, v4, v6 op_sel:[0,0,1]
	v_mul_f32_e32 v3, 0x42800000, v5
	v_mul_f32_e32 v4, 0x42800000, v9
	v_mov_b32_e32 v2, v163
	v_cvt_pk_fp8_f32 v2, v3, v4
	v_mul_f32_e32 v5, 0x42800000, v13
	v_mul_f32_e32 v6, 0x42800000, v21
	v_mul_f32_e32 v4, 0x42800000, v17
	v_cvt_pk_fp8_f32 v2, v5, v6 op_sel:[0,0,1]
	v_mul_f32_e32 v5, 0x42800000, v29
	v_mov_b32_e32 v3, v163
	v_cvt_pk_fp8_f32 v3, v4, v5
	v_mul_f32_e32 v6, 0x42800000, v33
	v_mul_f32_e32 v7, 0x42800000, v45
	v_mul_f32_e32 v5, 0x42800000, v25
	v_cvt_pk_fp8_f32 v3, v6, v7 op_sel:[0,0,1]
	v_mul_f32_e32 v6, 0x42800000, v37
	v_mov_b32_e32 v4, v163
	v_cvt_pk_fp8_f32 v4, v5, v6
	v_mul_f32_e32 v7, 0x42800000, v41
	v_mul_f32_e32 v8, 0x42800000, v53
	v_mul_f32_e32 v6, 0x42800000, v49
	v_cvt_pk_fp8_f32 v4, v7, v8 op_sel:[0,0,1]
	v_mul_f32_e32 v7, 0x42800000, v57
	v_mov_b32_e32 v5, v163
	v_cvt_pk_fp8_f32 v5, v6, v7
	v_mul_f32_e32 v8, 0x42800000, v61
	v_mul_f32_e32 v9, 0x42800000, v65
	ds_write_b128 v66, v[68:71] offset:37152
	v_cvt_pk_fp8_f32 v5, v8, v9 op_sel:[0,0,1]
	v_add_u32_e32 v6, s10, v76
	v_lshlrev_b32_e32 v7, 1, v6
	s_lshl_b32 s11, s18, 7
	ds_write_b128 v66, v[2:5] offset:37296
	s_waitcnt lgkmcnt(0)
	s_barrier
	ds_read_b128 v[2:5], v77 offset:36864
	v_and_b32_e32 v7, 0xffffff00, v7
	v_or_b32_e32 v8, s11, v67
	v_add_u32_e32 v7, v8, v7
	v_cndmask_b32_e64 v8, v6, v7, s[6:7]
	v_mov_b64_e32 v[6:7], s[12:13]
	v_mad_i64_i32 v[8:9], s[8:9], s19, v8, v[6:7]
	v_lshl_add_u64 v[8:9], v[8:9], 0, v[162:163]
	s_waitcnt lgkmcnt(0)
	global_store_dwordx4 v[8:9], v[2:5], off nt
	v_add_u32_e32 v8, s10, v78
	v_lshlrev_b32_e32 v9, 1, v8
	ds_read_b128 v[2:5], v77 offset:38016
	v_and_b32_e32 v9, 0xffffff00, v9
	v_or_b32_e32 v10, s11, v79
	v_add_u32_e32 v9, v10, v9
	v_cndmask_b32_e64 v8, v8, v9, s[6:7]
	v_mad_i64_i32 v[8:9], s[8:9], s19, v8, v[6:7]
	v_lshl_add_u64 v[8:9], v[8:9], 0, v[162:163]
	s_waitcnt lgkmcnt(0)
	global_store_dwordx4 v[8:9], v[2:5], off nt
	v_add_u32_e32 v8, s10, v80
	v_lshlrev_b32_e32 v9, 1, v8
	ds_read_b128 v[2:5], v77 offset:39168
	v_and_b32_e32 v9, 0xffffff00, v9
	v_or_b32_e32 v10, s11, v81
	v_add_u32_e32 v9, v10, v9
	v_cndmask_b32_e64 v8, v8, v9, s[6:7]
	v_mad_i64_i32 v[8:9], s[8:9], s19, v8, v[6:7]
	v_lshl_add_u64 v[8:9], v[8:9], 0, v[162:163]
	s_waitcnt lgkmcnt(0)
	global_store_dwordx4 v[8:9], v[2:5], off nt
	v_add_u32_e32 v8, s10, v74
	v_lshlrev_b32_e32 v9, 1, v8
	ds_read_b128 v[2:5], v77 offset:40320
	v_and_b32_e32 v9, 0xffffff00, v9
	v_or_b32_e32 v10, s11, v83
	v_add_u32_e32 v9, v10, v9
	v_cndmask_b32_e64 v8, v8, v9, s[6:7]
	v_mad_i64_i32 v[6:7], s[6:7], s19, v8, v[6:7]
	v_lshl_add_u64 v[6:7], v[6:7], 0, v[162:163]
	s_waitcnt lgkmcnt(0)
	global_store_dwordx4 v[6:7], v[2:5], off nt
	s_barrier
	s_and_saveexec_b64 s[6:7], s[4:5]
	s_cbranch_execz .LBB0_873
	s_waitcnt vmcnt(8)
	v_add_u32_e32 v2, s64, v243
	v_cmp_eq_u32_e32 vcc, -1, v130
	s_nop 1
	v_cndmask_b32_e32 v130, v130, v2, vcc
	v_mov_b32_e32 v2, s85
	ds_write_b32 v2, v130
	s_branch .LBB0_873

.LBB0_1707:
	v_cndmask_b32_e64 v2, 0, 1, s[6:7]
	v_mov_b32_e32 v170, 0xa00
	v_cmp_ne_u32_e64 s[6:7], 1, v2
	v_mov_b32_e32 v171, 0x9b8
	s_and_saveexec_b64 s[8:9], s[4:5]
	s_cbranch_execz .LBB0_1716
	s_and_b64 vcc, exec, s[6:7]
	v_mov_b32_e32 v170, 0xa00
	s_cbranch_vccnz .LBB0_1712
	s_mov_b64 s[46:47], exec
	v_mbcnt_lo_u32_b32 v2, s46, 0
	v_mbcnt_hi_u32_b32 v2, s47, v2
	v_cmp_eq_u32_e32 vcc, 0, v2
	s_and_saveexec_b64 s[10:11], vcc
	s_cbranch_execz .LBB0_1711
	s_bcnt1_i32_b64 s18, s[46:47]
	v_mov_b32_e32 v4, s18
	global_atomic_add v243, v3, v4, s[22:23] sc0
.LBB0_1711:
	s_or_b64 exec, exec, s[10:11]
	v_mov_b32_e32 v170, -1

; #define LAS __attribute__((address_space(3)))
; __device__ __forceinline__ void hyprep_unit(Ctx& C, int l, int uidx) {
;     constexpr int RS = 528;
;     int seq, tb, cb, L, rowbase; bf16* T;
;     if (uidx < 1536) { seq = uidx / 384; const int rem = uidx % 384; tb = rem / 6; cb = rem % 6; L = SL; rowbase = seq * SL; T = WSP(bf16, WS_TL); }
;     else { const int v = uidx - 1536; seq = v / 24; const int rem = v % 24; tb = rem / 6; cb = rem % 6; L = CL; rowbase = NLAT + seq * CL; T = WSP(bf16, WS_TC); }
;     const int t0 = 64 * tb; const bf16* Z = WSP(bf16, WS_Z);
;     __syncthreads();
;     { u32x4 v[5];
; #pragma unroll
;         for (int i = 0; i < 5; ++i) { const int idx0 = C.tid + 512 * i, idx = idx0 < 66 * 32 ? idx0 : 66 * 32 - 1, r = idx >> 5, ch = idx & 31, t = t0 - 1 + r; const bool ok = t >= 0 && t < L;
;             const int tc = t < 0 ? 0 : (t < L ? t : L - 1);
;             v[i] = *(const u32x4*)(Z + (size_t)(rowbase + tc) * INW + 1280 + 256 * cb + 8 * ch); if (!ok) v[i] = (u32x4){0u, 0u, 0u, 0u}; }
; #pragma unroll
;         for (int i = 0; i < 5; ++i) { const int idx0 = C.tid + 512 * i, idx = idx0 < 66 * 32 ? idx0 : 66 * 32 - 1, r = idx >> 5, ch = idx & 31;
;             if (i < 4 || idx0 < 66 * 32) *(LAS u32x4*)(C.lds + r * RS + ch * 16) = v[i]; } }
.LBB0_1716:
	s_or_b64 exec, exec, s[8:9]
	s_and_b64 vcc, exec, s[6:7]
	s_cbranch_vccnz .LBB0_1951
	v_mov_b32_e32 v172, v1
	s_mov_b64 s[6:7], s[20:21]
	s_mov_b32 s8, s3
	s_mov_b64 s[46:47], s[14:15]
	s_mov_b32 s9, s39
	s_mov_b64 s[48:49], s[16:17]
	s_cmpk_gt_i32 s56, 0xff
	v_and_b32_e32 v160, 63, v172
	v_readfirstlane_b32 s57, v172
	s_mov_b64 s[6:7], -1
	s_cbranch_scc0 .LBB0_1735
	s_cmpk_gt_u32 s56, 0x1ff
	s_cbranch_scc0 .LBB0_1732
	s_cmpk_gt_u32 s56, 0x3ff
	s_cbranch_scc0 .LBB0_1723
	s_add_i32 s6, s56, 0xfc00
	s_and_b32 s7, s6, 0xffff
	s_mul_i32 s7, s7, 0xaaab
	s_lshr_b32 s7, s7, 24
	s_mul_i32 s8, s7, 0x180
	s_sub_i32 s6, s6, s8
	s_lshl_b32 s18, s7, 12
	s_and_b32 s7, s6, 0xffff
	s_mul_i32 s7, s7, 0xaaab
	s_lshr_b32 s7, s7, 18
	s_mul_i32 s8, s7, 6
	s_lshl_b32 s19, s7, 6
	v_min_i32_e32 v2, 0x63f, v172
	s_sub_i32 s9, s6, s8
	s_and_b32 s8, s19, 0xffc0
	v_add_u32_e32 v4, 0x200, v2
	s_add_i32 s8, s8, -1
	v_ashrrev_i32_e32 v26, 5, v4
	v_min_i32_e32 v8, 0x43f, v172
	v_add_u32_e32 v27, s8, v26
	v_add_u32_e32 v6, 0x400, v8
	v_med3_i32 v4, v27, 0, v166
	v_ashrrev_i32_e32 v28, 5, v6
	v_or_b32_e32 v4, s18, v4
	v_mov_b64_e32 v[16:17], s[46:47]
	v_add_u32_e32 v29, s8, v28
	v_mad_u64_u32 v[4:5], s[6:7], v4, s63, v[16:17]
	v_med3_i32 v6, v29, 0, v166
	s_lshl_b32 s6, s9, 9
	v_or_b32_e32 v6, s18, v6
	s_and_b32 s26, s6, 0x1fe00
	v_mad_u64_u32 v[6:7], s[6:7], v6, s63, v[16:17]
	v_lshlrev_b32_e32 v8, 4, v8
	v_min_i32_e32 v14, 0x23f, v172
	v_lshl_add_u64 v[6:7], v[6:7], 0, s[26:27]
	v_and_b32_e32 v20, 0x1f0, v8
	v_mov_b32_e32 v21, v3
	v_add_u32_e32 v12, 0x600, v14
	v_lshl_add_u64 v[6:7], v[6:7], 0, v[20:21]
	v_ashrrev_i32_e32 v21, 5, v12
	v_add_u32_e32 v30, s8, v21
	v_med3_i32 v12, v30, 0, v166
	v_or_b32_e32 v12, s18, v12
	v_lshlrev_b32_e32 v2, 4, v2
	v_mad_u64_u32 v[12:13], s[6:7], v12, s63, v[16:17]
	v_lshlrev_b32_e32 v14, 4, v14
	v_lshl_add_u64 v[4:5], v[4:5], 0, s[26:27]
	v_and_b32_e32 v2, 0x1f0, v2
	v_lshl_add_u64 v[12:13], v[12:13], 0, s[26:27]
	v_and_b32_e32 v22, 0x1f0, v14
	v_mov_b32_e32 v23, v3
	v_min_i32_e32 v18, 0x83f, v172
	v_lshl_add_u64 v[4:5], v[4:5], 0, v[2:3]
	v_lshl_add_u64 v[12:13], v[12:13], 0, v[22:23]
	v_ashrrev_i32_e32 v23, 5, v18
	v_add_co_u32_e32 v4, vcc, s64, v4
	v_add_u32_e32 v31, s8, v23
	s_nop 0
	v_addc_co_u32_e32 v5, vcc, 0, v5, vcc
	v_med3_i32 v19, v31, 0, v166
	v_add_co_u32_e32 v8, vcc, s64, v6
	v_or_b32_e32 v19, s18, v19
	s_nop 0
	v_addc_co_u32_e32 v9, vcc, 0, v7, vcc
	v_mad_u64_u32 v[16:17], s[6:7], v19, s63, v[16:17]
	v_lshlrev_b32_e32 v18, 4, v18
	v_add_co_u32_e32 v12, vcc, s64, v12
	v_lshl_add_u64 v[16:17], v[16:17], 0, s[26:27]
	v_and_b32_e32 v24, 0x1f0, v18
	v_mov_b32_e32 v25, v3
	v_addc_co_u32_e32 v13, vcc, 0, v13, vcc
	v_lshl_add_u64 v[16:17], v[16:17], 0, v[24:25]
	s_waitcnt lgkmcnt(0)
	s_barrier
	global_load_dwordx4 v[4:7], v[4:5], off offset:2560
	s_nop 0
	global_load_dwordx4 v[8:11], v[8:9], off offset:2560
	v_add_co_u32_e32 v16, vcc, s64, v16
	global_load_dwordx4 v[12:15], v[12:13], off offset:2560
	s_nop 0
	v_addc_co_u32_e32 v17, vcc, 0, v17, vcc
	global_load_dwordx4 v[16:19], v[16:17], off offset:2560
	v_cmp_gt_u32_e32 vcc, s62, v27
	v_mul_lo_u32 v23, v23, s66
	v_add3_u32 v23, 0, v23, v24
	s_lshl_b32 s34, s9, 8
	s_waitcnt vmcnt(3)
	v_cndmask_b32_e32 v7, 0, v7, vcc
	v_cndmask_b32_e32 v6, 0, v6, vcc
	v_cndmask_b32_e32 v5, 0, v5, vcc
	v_cndmask_b32_e32 v4, 0, v4, vcc
	v_cmp_gt_u32_e32 vcc, s62, v29
	s_waitcnt vmcnt(2)
	s_nop 0
	v_cndmask_b32_e32 v11, 0, v11, vcc
	v_cndmask_b32_e32 v10, 0, v10, vcc
	v_cndmask_b32_e32 v9, 0, v9, vcc
	v_cndmask_b32_e32 v8, 0, v8, vcc
	v_cmp_gt_u32_e32 vcc, s62, v30
	s_waitcnt vmcnt(1)
	s_nop 0
	v_cndmask_b32_e32 v15, 0, v15, vcc
	v_cndmask_b32_e32 v14, 0, v14, vcc
	v_cndmask_b32_e32 v13, 0, v13, vcc
	v_cndmask_b32_e32 v12, 0, v12, vcc
	v_cmp_gt_u32_e32 vcc, s62, v31
	s_waitcnt vmcnt(0)
	s_nop 0
	v_cndmask_b32_e32 v19, 0, v19, vcc
	v_cndmask_b32_e32 v18, 0, v18, vcc
	v_cndmask_b32_e32 v17, 0, v17, vcc
	v_cndmask_b32_e32 v16, 0, v16, vcc
	ds_write_b128 v23, v[16:19]
	v_mul_lo_u32 v16, v26, s66
	v_add3_u32 v2, 0, v16, v2
	ds_write_b128 v2, v[4:7]
	v_mul_lo_u32 v2, v28, s66
	v_add3_u32 v2, 0, v2, v20
	ds_write_b128 v2, v[8:11]
	v_mul_lo_u32 v2, v21, s66
	v_add3_u32 v2, 0, v2, v22
	v_cmp_gt_i32_e32 vcc, 64, v172
	ds_write_b128 v2, v[12:15]
	s_and_saveexec_b64 s[6:7], vcc
	s_cbranch_execz .LBB0_1722
	v_min_i32_e32 v2, 63, v172
	v_add_u32_e32 v4, 0x800, v2
	v_ashrrev_i32_e32 v4, 5, v4
	v_add_u32_e32 v8, s8, v4
	v_med3_i32 v4, v8, 0, v166
	s_and_b32 s10, s34, 0xff00
	v_or_b32_e32 v6, s18, v4
	v_mov_b64_e32 v[4:5], s[46:47]
	v_mad_u64_u32 v[4:5], s[8:9], v6, s63, v[4:5]
	s_lshl_b32 s26, s10, 1
	v_lshlrev_b32_e32 v2, 4, v2
	v_lshl_add_u64 v[4:5], v[4:5], 0, s[26:27]
	v_and_b32_e32 v2, 0x1f0, v2
	v_lshl_add_u64 v[4:5], v[4:5], 0, v[2:3]
	v_add_co_u32_e32 v4, vcc, s64, v4
	v_add_u32_e32 v2, 0x800, v172
	s_nop 0
	v_addc_co_u32_e32 v5, vcc, 0, v5, vcc
	global_load_dwordx4 v[4:7], v[4:5], off offset:2560
	v_lshlrev_b32_e32 v9, 4, v172
	v_ashrrev_i32_e32 v2, 5, v2
	v_and_b32_e32 v9, 0x1f0, v9
	v_mul_lo_u32 v2, v2, s66
	v_cmp_gt_u32_e32 vcc, s62, v8
	v_add3_u32 v2, 0, v2, v9
	s_waitcnt vmcnt(0)
	v_cndmask_b32_e32 v7, 0, v7, vcc
	v_cndmask_b32_e32 v6, 0, v6, vcc
	v_cndmask_b32_e32 v5, 0, v5, vcc
	v_cndmask_b32_e32 v4, 0, v4, vcc
	ds_write_b128 v2, v[4:7]

; #define LAS __attribute__((address_space(3)))
; __device__ __forceinline__ void pool_unit(Ctx& C, int l, int blk) {
;     ...
;     const int row0 = 32 * blk;
;     const int s0 = row0 < NLAT ? (row0 / SL) * SL : NLAT + ((row0 - NLAT) / CL) * CL, L = row0 < NLAT ? SL : CL, t0 = row0 - s0;
;     const bf16* Z = WSP(bf16, WS_Z);
;     __syncthreads();
;     { u32x4 v[6];
; #pragma unroll
;         for (int i = 0; i < 6; ++i) { const int idx = C.tid + 512 * i, r = idx >> 6, ch = idx & 63, t = t0 - 8 + r; const bool ok = t >= 0 && t < L; const int tc = t < 0 ? 0 : (t < L ? t : L - 1);
;             v[i] = *(const u32x4*)(Z + (size_t)(s0 + tc) * INW + 8 * ch); if (!ok) v[i] = (u32x4){0u, 0u, 0u, 0u}; }
; #pragma unroll
;         for (int i = 0; i < 6; ++i) { const int idx = C.tid + 512 * i, r = idx >> 6, ch = idx & 63; *(LAS u32x4*)(C.lds + r * RS + ch * 16) = v[i]; } }
;     __syncthreads();
;     {
;         const int c8 = C.tid & 63, tg = C.tid >> 6, hw = 1 << (c8 >> 4);
.LBB0_1723:
	s_and_b64 vcc, exec, s[6:7]
	s_cbranch_vccz .LBB0_1731
	s_lshl_b32 s6, s56, 5
	s_add_i32 s10, s6, 0xffffc000
	s_and_b32 s11, s10, 0xffffcfe0
	v_lshlrev_b32_e32 v2, 4, v172
	v_add_u32_e32 v6, 0x200, v172
	s_add_i32 s9, s11, -8
	v_and_b32_e32 v2, 0x3f0, v2
	v_ashrrev_i32_e32 v28, 6, v172
	v_ashrrev_i32_e32 v30, 6, v6
	s_and_b32 s8, s6, 0x3000
	v_lshl_add_u64 v[4:5], s[46:47], 0, v[2:3]
	s_mov_b64 s[6:7], 0x36000000
	v_add_u32_e32 v29, s9, v28
	v_add_u32_e32 v31, s9, v30
	v_lshl_add_u64 v[24:25], v[4:5], 0, s[6:7]
	v_med3_i32 v4, v29, 0, v166
	v_med3_i32 v6, v31, 0, v166
	v_or_b32_e32 v4, s8, v4
	v_or_b32_e32 v6, s8, v6
	v_add_u32_e32 v12, 0x400, v172
	v_add_u32_e32 v14, 0x600, v172
	v_mul_u32_u24_e32 v4, 0x1e00, v4
	v_mov_b32_e32 v5, v3
	v_mul_u32_u24_e32 v6, 0x1e00, v6
	v_mov_b32_e32 v7, v3
	v_ashrrev_i32_e32 v32, 6, v12
	v_ashrrev_i32_e32 v34, 6, v14
	v_lshl_add_u64 v[4:5], v[24:25], 0, v[4:5]
	v_lshl_add_u64 v[8:9], v[24:25], 0, v[6:7]
	v_add_u32_e32 v33, s9, v32
	v_add_u32_e32 v35, s9, v34
	s_waitcnt lgkmcnt(0)
	s_barrier
	global_load_dwordx4 v[4:7], v[4:5], off
	s_nop 0
	global_load_dwordx4 v[8:11], v[8:9], off
	v_med3_i32 v12, v33, 0, v166
	v_med3_i32 v14, v35, 0, v166
	v_add_u32_e32 v20, 0x800, v172
	v_or_b32_e32 v12, s8, v12
	v_or_b32_e32 v14, s8, v14
	v_ashrrev_i32_e32 v36, 6, v20
	v_mul_u32_u24_e32 v12, 0x1e00, v12
	v_mov_b32_e32 v13, v3
	v_mul_u32_u24_e32 v14, 0x1e00, v14
	v_mov_b32_e32 v15, v3
	v_add_u32_e32 v37, s9, v36
	v_add_u32_e32 v26, 0xa00, v172
	v_lshl_add_u64 v[12:13], v[24:25], 0, v[12:13]
	v_lshl_add_u64 v[16:17], v[24:25], 0, v[14:15]
	v_med3_i32 v20, v37, 0, v166
	v_ashrrev_i32_e32 v38, 6, v26
	global_load_dwordx4 v[12:15], v[12:13], off
	s_nop 0
	global_load_dwordx4 v[16:19], v[16:17], off
	v_or_b32_e32 v20, s8, v20
	v_add_u32_e32 v39, s9, v38
	v_mul_u32_u24_e32 v20, 0x1e00, v20
	v_mov_b32_e32 v21, v3
	v_med3_i32 v26, v39, 0, v166
	v_lshl_add_u64 v[20:21], v[24:25], 0, v[20:21]
	v_or_b32_e32 v26, s8, v26
	global_load_dwordx4 v[20:23], v[20:21], off
	v_mul_u32_u24_e32 v26, 0x1e00, v26
	v_mov_b32_e32 v27, v3
	v_lshl_add_u64 v[24:25], v[24:25], 0, v[26:27]
	global_load_dwordx4 v[24:27], v[24:25], off
	v_cmp_gt_u32_e32 vcc, s62, v29
	v_mul_lo_u32 v28, v28, s67
	v_add3_u32 v28, 0, v28, v2
	s_mul_i32 s6, s11, 0x410
	s_mov_b32 s18, 0
	s_waitcnt vmcnt(5)
	v_cndmask_b32_e32 v7, 0, v7, vcc
	v_cndmask_b32_e32 v6, 0, v6, vcc
	v_cndmask_b32_e32 v5, 0, v5, vcc
	v_cndmask_b32_e32 v4, 0, v4, vcc
	v_cmp_gt_u32_e32 vcc, s62, v31
	ds_write_b128 v28, v[4:7]
	v_mul_lo_u32 v4, v30, s67
	s_waitcnt vmcnt(4)
	v_cndmask_b32_e32 v11, 0, v11, vcc
	v_cndmask_b32_e32 v10, 0, v10, vcc
	v_cndmask_b32_e32 v9, 0, v9, vcc
	v_cndmask_b32_e32 v8, 0, v8, vcc
	v_add3_u32 v4, 0, v4, v2
	v_cmp_gt_u32_e32 vcc, s62, v33
	ds_write_b128 v4, v[8:11]
	v_mul_lo_u32 v4, v32, s67
	v_add3_u32 v4, 0, v4, v2
	s_waitcnt vmcnt(3)
	v_cndmask_b32_e32 v15, 0, v15, vcc
	v_cndmask_b32_e32 v14, 0, v14, vcc
	v_cndmask_b32_e32 v13, 0, v13, vcc
	v_cndmask_b32_e32 v12, 0, v12, vcc
	v_cmp_gt_u32_e32 vcc, s62, v35
	ds_write_b128 v4, v[12:15]
	v_mul_lo_u32 v4, v34, s67
	s_waitcnt vmcnt(2)
	v_cndmask_b32_e32 v19, 0, v19, vcc
	v_cndmask_b32_e32 v18, 0, v18, vcc
	v_cndmask_b32_e32 v17, 0, v17, vcc
	v_cndmask_b32_e32 v16, 0, v16, vcc
	v_add3_u32 v4, 0, v4, v2
	v_cmp_gt_u32_e32 vcc, s62, v37
	ds_write_b128 v4, v[16:19]
	v_mul_lo_u32 v4, v36, s67
	s_waitcnt vmcnt(1)
	v_cndmask_b32_e32 v23, 0, v23, vcc
	v_cndmask_b32_e32 v22, 0, v22, vcc
	v_cndmask_b32_e32 v21, 0, v21, vcc
	v_cndmask_b32_e32 v20, 0, v20, vcc
	v_add3_u32 v4, 0, v4, v2
	v_cmp_gt_u32_e32 vcc, s62, v39
	ds_write_b128 v4, v[20:23]
	v_mul_lo_u32 v4, v38, s67
	s_waitcnt vmcnt(0)
	v_cndmask_b32_e32 v27, 0, v27, vcc
	v_cndmask_b32_e32 v26, 0, v26, vcc
	v_cndmask_b32_e32 v25, 0, v25, vcc
	v_cndmask_b32_e32 v24, 0, v24, vcc
	v_add3_u32 v2, 0, v4, v2
	ds_write_b128 v2, v[24:27]
	v_lshrrev_b32_e32 v2, 4, v160
	v_lshlrev_b32_e64 v5, v2, 1
	v_ashrrev_i32_e32 v2, 4, v172
	v_and_b32_e32 v16, -4, v2
	v_lshlrev_b32_e32 v4, 4, v160
	v_add_u32_e32 v2, 0, v4
	v_subrev_u32_e32 v4, s6, v4
	v_add_u32_e32 v6, s11, v16
	v_add_u32_e32 v4, s68, v4
	v_sub_u32_e32 v17, v6, v5
	s_waitcnt lgkmcnt(0)
	s_barrier
	s_branch .LBB0_1726

; __device__ __forceinline__ void gmlp_unit(Ctx& C, int l, int uidx) {
;     ...
;     const int gl = C.wave >> 1, ph = C.wave & 1, g = 4 * hf + gl, r32 = C.lane & 31, h = C.lane >> 5;
;     bf16x8 Wf[2][8]; u32x2 upre[2][2][4];
;     { const bf16* wsb = WSP(bf16, WS_GWSB) + ((size_t)(l * 8 + g) * 128 + 64 * ph + r32) * 128 + 8 * h;
; #pragma unroll
;       for (int pb = 0; pb < 2; ++pb)
; #pragma unroll
;           for (int s = 0; s < 8; ++s) Wf[pb][s] = *(const bf16x8*)(wsb + (size_t)(32 * pb) * 128 + 16 * s);
; #pragma unroll
;       for (int pb = 0; pb < 2; ++pb) { const bf16* up = Z + (size_t)(row0 + 64 * ph + 32 * pb + r32) * INW + 2816 + 64 * g + 4 * h;
; #pragma unroll
;           for (int cb = 0; cb < 2; ++cb)
; #pragma unroll
;               for (int rg = 0; rg < 4; ++rg) upre[pb][cb][rg] = *(const u32x2*)(up + 32 * cb + 8 * rg); } }
;     __syncthreads();
;     {
;         const int tok = C.tid >> 2, part = C.tid & 3;
;         const bf16* zp = Z + (size_t)(row0 + tok) * INW + 3328 + 128 * part;
;         const bf16* zq = Z + (size_t)(row0 + tok) * INW + 3328 + 256 * hf + 64 * part;
;         u32x4 r1[16], r2[8];
; #pragma unroll
;         for (int c8 = 0; c8 < 16; ++c8) r1[c8] = *(const u32x4*)(zp + 8 * c8);
; #pragma unroll
;         for (int c8 = 0; c8 < 8; ++c8) r2[c8] = *(const u32x4*)(zq + 8 * c8);
.LBB0_1732:
	s_andn2_b64 vcc, exec, s[6:7]
	s_cbranch_vccnz .LBB0_1734
	s_and_b32 s6, s56, 1
	s_ashr_i32 s34, s57, 7
	s_lshl_b32 s8, s6, 2
	s_add_i32 s10, s34, s8
	s_add_i32 s52, s10, 8
	s_ashr_i32 s53, s52, 31
	s_lshl_b64 s[8:9], s[52:53], 7
	s_and_b32 s18, s57, 64
	v_and_b32_e32 v161, 31, v172
	s_or_b32 s8, s8, s18
	v_or_b32_e32 v4, s8, v161
	v_mov_b32_e32 v5, s9
	v_lshrrev_b32_e32 v6, 5, v160
	v_lshlrev_b64 v[4:5], 8, v[4:5]
	v_lshl_add_u64 v[4:5], s[46:47], 0, v[4:5]
	v_lshlrev_b32_e32 v156, 4, v6
	v_mov_b32_e32 v157, v3
	v_lshl_add_u64 v[8:9], v[4:5], 0, v[156:157]
	s_mov_b64 s[8:9], 0x380000
	s_lshl_b32 s7, s56, 6
	v_lshl_add_u64 v[10:11], v[8:9], 0, s[8:9]
	s_mov_b32 s8, 0x380000
	v_add_co_u32_e32 v4, vcc, s8, v8
	s_and_b32 s7, s7, 0x7f80
	s_nop 0
	v_addc_co_u32_e32 v5, vcc, 0, v9, vcc
	s_mov_b32 s8, 0x382000
	s_xor_b32 s19, s7, 0x4000
	v_add_co_u32_e32 v12, vcc, s8, v8
	s_add_u32 s8, s46, 0x36000000
	s_nop 0
	v_addc_co_u32_e32 v13, vcc, 0, v9, vcc
	s_addc_u32 s9, s47, 0
	s_or_b32 s7, s19, s18
	v_lshlrev_b32_e32 v2, 3, v6
	global_load_dwordx4 v[116:119], v[10:11], off offset:32
	global_load_dwordx4 v[104:107], v[10:11], off offset:64
	global_load_dwordx4 v[100:103], v[10:11], off offset:96
	global_load_dwordx4 v[88:91], v[10:11], off offset:128
	global_load_dwordx4 v[84:87], v[10:11], off offset:160
	global_load_dwordx4 v[76:79], v[10:11], off offset:192
	s_nop 0
	global_load_dwordx4 v[4:7], v[4:5], off
	s_nop 0
	global_load_dwordx4 v[72:75], v[10:11], off offset:224
	s_nop 0
	global_load_dwordx4 v[8:11], v[12:13], off
	global_load_dwordx4 v[120:123], v[12:13], off offset:32
	global_load_dwordx4 v[112:115], v[12:13], off offset:64
	global_load_dwordx4 v[108:111], v[12:13], off offset:96
	global_load_dwordx4 v[96:99], v[12:13], off offset:128
	global_load_dwordx4 v[92:95], v[12:13], off offset:160
	global_load_dwordx4 v[80:83], v[12:13], off offset:192
	global_load_dwordx4 v[68:71], v[12:13], off offset:224
	v_or_b32_e32 v12, s7, v161
	s_lshl_b32 s10, s10, 6
	v_mul_u32_u24_e32 v12, 0xf00, v12
	s_ashr_i32 s11, s10, 31
	v_lshlrev_b32_e32 v12, 1, v12
	v_mov_b32_e32 v13, v3
	v_lshl_add_u64 v[12:13], s[8:9], 0, v[12:13]
	s_lshl_b64 s[50:51], s[10:11], 1
	v_lshl_add_u64 v[12:13], v[12:13], 0, s[50:51]
	v_lshl_add_u64 v[12:13], v[12:13], 0, v[2:3]
	s_mov_b64 s[10:11], 0x1600
	v_add_co_u32_e32 v16, vcc, s62, v12
	v_lshl_add_u64 v[14:15], v[12:13], 0, s[10:11]
	s_nop 0
	v_addc_co_u32_e32 v17, vcc, 0, v13, vcc
	s_mov_b64 s[10:11], 0x3d600
	s_mov_b32 s7, 0x3d000
	global_load_dwordx2 v[152:153], v[14:15], off offset:16
	global_load_dwordx2 v[150:151], v[14:15], off offset:32
	global_load_dwordx2 v[148:149], v[14:15], off offset:48
	global_load_dwordx2 v[146:147], v[14:15], off offset:64
	global_load_dwordx2 v[154:155], v[16:17], off offset:1536
	global_load_dwordx2 v[144:145], v[14:15], off offset:80
	global_load_dwordx2 v[142:143], v[14:15], off offset:96
	global_load_dwordx2 v[140:141], v[14:15], off offset:112
	v_lshl_add_u64 v[14:15], v[12:13], 0, s[10:11]
	v_add_co_u32_e32 v12, vcc, s7, v12
	v_ashrrev_i32_e32 v62, 2, v172
	s_nop 0
	v_addc_co_u32_e32 v13, vcc, 0, v13, vcc
	global_load_dwordx2 v[136:137], v[14:15], off offset:16
	global_load_dwordx2 v[134:135], v[14:15], off offset:32
	global_load_dwordx2 v[132:133], v[14:15], off offset:48
	global_load_dwordx2 v[130:131], v[14:15], off offset:64
	global_load_dwordx2 v[138:139], v[12:13], off offset:1536
	global_load_dwordx2 v[128:129], v[14:15], off offset:80
	global_load_dwordx2 v[126:127], v[14:15], off offset:96
	global_load_dwordx2 v[124:125], v[14:15], off offset:112
	v_add_u32_e32 v14, s19, v62
	v_mov_b64_e32 v[12:13], s[8:9]
	v_mad_i64_i32 v[12:13], s[8:9], v14, s63, v[12:13]
	v_and_b32_e32 v162, 3, v172
	s_mov_b64 s[8:9], 0x1a00
	v_lshl_add_u64 v[16:17], v[12:13], 0, s[8:9]
	v_lshlrev_b32_e32 v158, 8, v162
	v_mov_b32_e32 v159, v3
	v_lshl_add_u64 v[18:19], v[16:17], 0, v[158:159]
	s_waitcnt lgkmcnt(0)
	s_barrier
	global_load_dwordx4 v[56:59], v[18:19], off
	global_load_dwordx4 v[64:67], v[18:19], off offset:16
	global_load_dwordx4 v[174:177], v[18:19], off offset:32
	global_load_dwordx4 v[178:181], v[18:19], off offset:48
	global_load_dwordx4 v[52:55], v[18:19], off offset:112
	global_load_dwordx4 v[182:185], v[18:19], off offset:96
	global_load_dwordx4 v[186:189], v[18:19], off offset:80
	global_load_dwordx4 v[190:193], v[18:19], off offset:64
	global_load_dwordx4 v[36:39], v[18:19], off offset:176
	global_load_dwordx4 v[40:43], v[18:19], off offset:160
	global_load_dwordx4 v[44:47], v[18:19], off offset:144
	global_load_dwordx4 v[48:51], v[18:19], off offset:128
	global_load_dwordx4 v[12:15], v[18:19], off offset:240
	global_load_dwordx4 v[20:23], v[18:19], off offset:224
	global_load_dwordx4 v[24:27], v[18:19], off offset:208
	global_load_dwordx4 v[32:35], v[18:19], off offset:192
	s_lshl_b32 s26, s6, 9
	v_lshlrev_b32_e32 v28, 7, v162
	v_mov_b32_e32 v29, v3
	v_lshl_add_u64 v[16:17], v[16:17], 0, s[26:27]
	v_lshl_add_u64 v[60:61], v[16:17], 0, v[28:29]
	global_load_dwordx4 v[16:19], v[60:61], off offset:16
	global_load_dwordx4 v[28:31], v[60:61], off
	s_load_dwordx4 s[8:11], s[48:49], 0xb0
	s_load_dwordx2 s[54:55], s[48:49], 0xc8
	s_lshl_b32 s6, s6, 10
	v_mul_u32_u24_e32 v162, 0x4400, v162
	s_waitcnt lgkmcnt(0)
	s_add_u32 s8, s8, s6
	s_addc_u32 s9, s9, 0
	s_add_u32 s10, s10, s6
	s_addc_u32 s11, s11, 0
	s_mov_b32 s6, 0x3b000000
	s_waitcnt vmcnt(17)
; template <int CTRL> __device__ __forceinline__ float dpp_f(float x) { return __int_as_float(__builtin_amdgcn_update_dpp(0, __float_as_int(x), CTRL, 0xF, 0xF, true)); }
; __device__ __forceinline__ void cvt8(const u32x4 r, float (&f)[8]) { f[0] = bflo(r.x); f[1] = bfhi(r.x); f[2] = bflo(r.y); f[3] = bfhi(r.y); f[4] = bflo(r.z); f[5] = bfhi(r.z); f[6] = bflo(r.w); f[7] = bfhi(r.w); }
; __device__ __forceinline__ void gmlp_unit(Ctx& C, int l, int uidx) {
;     ...
;         float s = 0.f, q = 0.f;
; #pragma unroll
;         for (int c8 = 0; c8 < 16; ++c8) { float f[8]; cvt8(r1[c8], f);
; #pragma unroll
;             for (int j = 0; j < 8; ++j) { s += f[j]; q += f[j] * f[j]; } }
;         s += dpp_f<DPP_XOR1>(s); s += dpp_f<DPP_XOR2>(s); q += dpp_f<DPP_XOR1>(q); q += dpp_f<DPP_XOR2>(q);
	v_lshlrev_b32_e32 v63, 16, v56
	v_and_b32_e32 v56, 0xffff0000, v56
	v_add_f32_e32 v173, 0, v63
	v_lshlrev_b32_e32 v157, 16, v57
	v_add_f32_e32 v173, v173, v56
	v_mul_f32_e32 v56, v56, v56
	v_and_b32_e32 v57, 0xffff0000, v57
	v_fmac_f32_e32 v56, v63, v63
	v_add_f32_e32 v63, v173, v157
	v_lshlrev_b32_e32 v159, 16, v58
	v_fmac_f32_e32 v56, v157, v157
	v_add_f32_e32 v63, v63, v57
	v_and_b32_e32 v58, 0xffff0000, v58
	v_fmac_f32_e32 v56, v57, v57
	v_add_f32_e32 v57, v63, v159
	v_lshlrev_b32_e32 v164, 16, v59
	v_fmac_f32_e32 v56, v159, v159
	v_add_f32_e32 v57, v57, v58
	v_and_b32_e32 v59, 0xffff0000, v59
	v_fmac_f32_e32 v56, v58, v58
	v_add_f32_e32 v57, v57, v164
	v_fmac_f32_e32 v56, v164, v164
	v_add_f32_e32 v57, v57, v59
	s_waitcnt vmcnt(16)
	v_lshlrev_b32_e32 v58, 16, v64
	v_fmac_f32_e32 v56, v59, v59
	v_and_b32_e32 v59, 0xffff0000, v64
	v_add_f32_e32 v57, v57, v58
	v_lshlrev_b32_e32 v63, 16, v65
	v_fmac_f32_e32 v56, v58, v58
	v_add_f32_e32 v57, v57, v59
	v_and_b32_e32 v64, 0xffff0000, v65
	v_fmac_f32_e32 v56, v59, v59
	v_add_f32_e32 v57, v57, v63
	v_lshlrev_b32_e32 v65, 16, v66
	v_fmac_f32_e32 v56, v63, v63
	v_add_f32_e32 v57, v57, v64
	v_and_b32_e32 v66, 0xffff0000, v66
	v_fmac_f32_e32 v56, v64, v64
	v_add_f32_e32 v57, v57, v65
	v_lshlrev_b32_e32 v157, 16, v67
	v_fmac_f32_e32 v56, v65, v65
	v_add_f32_e32 v57, v57, v66
	v_and_b32_e32 v67, 0xffff0000, v67
	v_fmac_f32_e32 v56, v66, v66
	v_add_f32_e32 v57, v57, v157
	v_fmac_f32_e32 v56, v157, v157
	v_add_f32_e32 v57, v57, v67
	s_waitcnt vmcnt(15)
	v_lshlrev_b32_e32 v58, 16, v174
	v_fmac_f32_e32 v56, v67, v67
	v_and_b32_e32 v59, 0xffff0000, v174
	v_add_f32_e32 v57, v57, v58
	v_lshlrev_b32_e32 v63, 16, v175
	v_fmac_f32_e32 v56, v58, v58
	v_add_f32_e32 v57, v57, v59
	v_and_b32_e32 v64, 0xffff0000, v175
	v_fmac_f32_e32 v56, v59, v59
	v_add_f32_e32 v57, v57, v63
	v_lshlrev_b32_e32 v65, 16, v176
	v_fmac_f32_e32 v56, v63, v63
	v_add_f32_e32 v57, v57, v64
	v_and_b32_e32 v66, 0xffff0000, v176
	v_fmac_f32_e32 v56, v64, v64
	v_add_f32_e32 v57, v57, v65
	v_lshlrev_b32_e32 v67, 16, v177
	v_fmac_f32_e32 v56, v65, v65
	v_add_f32_e32 v57, v57, v66
	v_and_b32_e32 v157, 0xffff0000, v177
	v_fmac_f32_e32 v56, v66, v66
	v_add_f32_e32 v57, v57, v67
	v_fmac_f32_e32 v56, v67, v67
	v_add_f32_e32 v57, v57, v157
	s_waitcnt vmcnt(14)
	v_lshlrev_b32_e32 v58, 16, v178
	v_fmac_f32_e32 v56, v157, v157
	v_and_b32_e32 v59, 0xffff0000, v178
	v_add_f32_e32 v57, v57, v58
	v_lshlrev_b32_e32 v63, 16, v179
	v_fmac_f32_e32 v56, v58, v58
	v_add_f32_e32 v57, v57, v59
	v_and_b32_e32 v64, 0xffff0000, v179
	v_fmac_f32_e32 v56, v59, v59
	v_add_f32_e32 v57, v57, v63
	v_lshlrev_b32_e32 v65, 16, v180
	v_fmac_f32_e32 v56, v63, v63
	v_add_f32_e32 v57, v57, v64
	v_and_b32_e32 v66, 0xffff0000, v180
	v_fmac_f32_e32 v56, v64, v64
	v_add_f32_e32 v57, v57, v65
	v_lshlrev_b32_e32 v67, 16, v181
	v_fmac_f32_e32 v56, v65, v65
	v_add_f32_e32 v57, v57, v66
	v_and_b32_e32 v157, 0xffff0000, v181
	v_fmac_f32_e32 v56, v66, v66
	v_add_f32_e32 v57, v57, v67
	v_fmac_f32_e32 v56, v67, v67
	v_add_f32_e32 v57, v57, v157
	s_waitcnt vmcnt(10)
	v_lshlrev_b32_e32 v58, 16, v190
	v_fmac_f32_e32 v56, v157, v157
	v_and_b32_e32 v59, 0xffff0000, v190
	v_add_f32_e32 v57, v57, v58
	v_lshlrev_b32_e32 v63, 16, v191
	v_fmac_f32_e32 v56, v58, v58
	v_add_f32_e32 v57, v57, v59
	v_and_b32_e32 v64, 0xffff0000, v191
	v_fmac_f32_e32 v56, v59, v59
	v_add_f32_e32 v57, v57, v63
	v_lshlrev_b32_e32 v65, 16, v192
	v_fmac_f32_e32 v56, v63, v63
	v_add_f32_e32 v57, v57, v64
	v_and_b32_e32 v66, 0xffff0000, v192
	v_fmac_f32_e32 v56, v64, v64
	v_add_f32_e32 v57, v57, v65
	v_lshlrev_b32_e32 v67, 16, v193
	v_fmac_f32_e32 v56, v65, v65
	v_add_f32_e32 v57, v57, v66
	v_and_b32_e32 v157, 0xffff0000, v193
	v_fmac_f32_e32 v56, v66, v66
	v_add_f32_e32 v57, v57, v67
	v_fmac_f32_e32 v56, v67, v67
	v_add_f32_e32 v57, v57, v157
	v_lshlrev_b32_e32 v58, 16, v186
	v_fmac_f32_e32 v56, v157, v157
	v_and_b32_e32 v59, 0xffff0000, v186
	v_add_f32_e32 v57, v57, v58
	v_lshlrev_b32_e32 v63, 16, v187
	v_fmac_f32_e32 v56, v58, v58
	v_add_f32_e32 v57, v57, v59
	v_and_b32_e32 v64, 0xffff0000, v187
	v_fmac_f32_e32 v56, v59, v59
	v_add_f32_e32 v57, v57, v63
	v_lshlrev_b32_e32 v65, 16, v188
	v_fmac_f32_e32 v56, v63, v63
	v_add_f32_e32 v57, v57, v64
	v_and_b32_e32 v66, 0xffff0000, v188
	v_fmac_f32_e32 v56, v64, v64
	v_add_f32_e32 v57, v57, v65
	v_lshlrev_b32_e32 v67, 16, v189
	v_fmac_f32_e32 v56, v65, v65
	v_add_f32_e32 v57, v57, v66
	v_and_b32_e32 v157, 0xffff0000, v189
	v_fmac_f32_e32 v56, v66, v66
	v_add_f32_e32 v57, v57, v67
	v_fmac_f32_e32 v56, v67, v67
	v_add_f32_e32 v57, v57, v157
	v_lshlrev_b32_e32 v58, 16, v182
	v_fmac_f32_e32 v56, v157, v157
	v_and_b32_e32 v59, 0xffff0000, v182
	v_add_f32_e32 v57, v57, v58
	v_lshlrev_b32_e32 v63, 16, v183
	v_fmac_f32_e32 v56, v58, v58
	v_add_f32_e32 v57, v57, v59
	v_and_b32_e32 v64, 0xffff0000, v183
	v_fmac_f32_e32 v56, v59, v59
	v_add_f32_e32 v57, v57, v63
	v_lshlrev_b32_e32 v65, 16, v184
	v_fmac_f32_e32 v56, v63, v63
	v_add_f32_e32 v57, v57, v64
	v_and_b32_e32 v66, 0xffff0000, v184
	v_fmac_f32_e32 v56, v64, v64
	v_add_f32_e32 v57, v57, v65
	v_lshlrev_b32_e32 v67, 16, v185
	v_fmac_f32_e32 v56, v65, v65
	v_add_f32_e32 v57, v57, v66
	v_and_b32_e32 v157, 0xffff0000, v185
	v_fmac_f32_e32 v56, v66, v66
	v_add_f32_e32 v57, v57, v67
	v_fmac_f32_e32 v56, v67, v67
	v_add_f32_e32 v57, v57, v157
	v_lshlrev_b32_e32 v58, 16, v52
	v_fmac_f32_e32 v56, v157, v157
	v_and_b32_e32 v52, 0xffff0000, v52
	v_add_f32_e32 v57, v57, v58
	v_lshlrev_b32_e32 v59, 16, v53
	v_fmac_f32_e32 v56, v58, v58
	v_add_f32_e32 v57, v57, v52
	v_and_b32_e32 v53, 0xffff0000, v53
	v_fmac_f32_e32 v56, v52, v52
	v_add_f32_e32 v52, v57, v59
	v_lshlrev_b32_e32 v63, 16, v54
	v_fmac_f32_e32 v56, v59, v59
	v_add_f32_e32 v52, v52, v53
	v_and_b32_e32 v54, 0xffff0000, v54
	v_fmac_f32_e32 v56, v53, v53
	v_add_f32_e32 v52, v52, v63
	v_lshlrev_b32_e32 v64, 16, v55
	v_fmac_f32_e32 v56, v63, v63
	v_add_f32_e32 v52, v52, v54
	v_and_b32_e32 v55, 0xffff0000, v55
	v_fmac_f32_e32 v56, v54, v54
	v_add_f32_e32 v52, v52, v64
	v_fmac_f32_e32 v56, v64, v64
	v_add_f32_e32 v52, v52, v55
	s_waitcnt vmcnt(6)
; template <int CTRL> __device__ __forceinline__ float dpp_f(float x) { return __int_as_float(__builtin_amdgcn_update_dpp(0, __float_as_int(x), CTRL, 0xF, 0xF, true)); }
; __device__ __forceinline__ void cvt8(const u32x4 r, float (&f)[8]) { f[0] = bflo(r.x); f[1] = bfhi(r.x); f[2] = bflo(r.y); f[3] = bfhi(r.y); f[4] = bflo(r.z); f[5] = bfhi(r.z); f[6] = bflo(r.w); f[7] = bfhi(r.w); }
; __device__ __forceinline__ void gmlp_unit(Ctx& C, int l, int uidx) {
;     ...
;         for (int c8 = 0; c8 < 16; ++c8) { float f[8]; cvt8(r1[c8], f);
; #pragma unroll
;             for (int j = 0; j < 8; ++j) { s += f[j]; q += f[j] * f[j]; } }
;         s += dpp_f<DPP_XOR1>(s); s += dpp_f<DPP_XOR2>(s); q += dpp_f<DPP_XOR1>(q); q += dpp_f<DPP_XOR2>(q);
;         const float mean = s * (1.0f / 512.0f); const float var = fmaxf(q * (1.0f / 512.0f) - mean * mean, 0.f); const float rstd = 1.0f / sqrtf(var + LN_EPS);
;         const float* lg = INP(I_GLG) + l * 512 + 256 * hf + 64 * part; const float* lb = INP(I_GLB) + l * 512 + 256 * hf + 64 * part;
; #pragma unroll
;         for (int c8 = 0; c8 < 8; ++c8) { float f[8]; cvt8(r2[c8], f);
;             const f32x4 g0 = *(const f32x4*)(lg + 8 * c8), g1 = *(const f32x4*)(lg + 8 * c8 + 4), b0 = *(const f32x4*)(lb + 8 * c8), b1 = *(const f32x4*)(lb + 8 * c8 + 4);
	v_lshlrev_b32_e32 v53, 16, v48
	v_fmac_f32_e32 v56, v55, v55
	v_and_b32_e32 v48, 0xffff0000, v48
	v_add_f32_e32 v52, v52, v53
	v_lshlrev_b32_e32 v54, 16, v49
	v_fmac_f32_e32 v56, v53, v53
	v_add_f32_e32 v52, v52, v48
	v_and_b32_e32 v49, 0xffff0000, v49
	v_fmac_f32_e32 v56, v48, v48
	v_add_f32_e32 v48, v52, v54
	v_lshlrev_b32_e32 v55, 16, v50
	v_fmac_f32_e32 v56, v54, v54
	v_add_f32_e32 v48, v48, v49
	v_and_b32_e32 v50, 0xffff0000, v50
	v_fmac_f32_e32 v56, v49, v49
	v_add_f32_e32 v48, v48, v55
	v_lshlrev_b32_e32 v57, 16, v51
	v_fmac_f32_e32 v56, v55, v55
	v_add_f32_e32 v48, v48, v50
	v_and_b32_e32 v51, 0xffff0000, v51
	v_fmac_f32_e32 v56, v50, v50
	v_add_f32_e32 v48, v48, v57
	v_fmac_f32_e32 v56, v57, v57
	v_add_f32_e32 v48, v48, v51
	v_lshlrev_b32_e32 v49, 16, v44
	v_fmac_f32_e32 v56, v51, v51
	v_and_b32_e32 v44, 0xffff0000, v44
	v_add_f32_e32 v48, v48, v49
	v_lshlrev_b32_e32 v50, 16, v45
	v_fmac_f32_e32 v56, v49, v49
	v_add_f32_e32 v48, v48, v44
	v_and_b32_e32 v45, 0xffff0000, v45
	v_fmac_f32_e32 v56, v44, v44
	v_add_f32_e32 v44, v48, v50
	v_lshlrev_b32_e32 v51, 16, v46
	v_fmac_f32_e32 v56, v50, v50
	v_add_f32_e32 v44, v44, v45
	v_and_b32_e32 v46, 0xffff0000, v46
	v_fmac_f32_e32 v56, v45, v45
	v_add_f32_e32 v44, v44, v51
	v_lshlrev_b32_e32 v52, 16, v47
	v_fmac_f32_e32 v56, v51, v51
	v_add_f32_e32 v44, v44, v46
	v_and_b32_e32 v47, 0xffff0000, v47
	v_fmac_f32_e32 v56, v46, v46
	v_add_f32_e32 v44, v44, v52
	v_fmac_f32_e32 v56, v52, v52
	v_add_f32_e32 v44, v44, v47
	v_lshlrev_b32_e32 v45, 16, v40
	v_fmac_f32_e32 v56, v47, v47
	v_and_b32_e32 v40, 0xffff0000, v40
	v_add_f32_e32 v44, v44, v45
	v_lshlrev_b32_e32 v46, 16, v41
	v_fmac_f32_e32 v56, v45, v45
	v_add_f32_e32 v44, v44, v40
	v_and_b32_e32 v41, 0xffff0000, v41
	v_fmac_f32_e32 v56, v40, v40
	v_add_f32_e32 v40, v44, v46
	v_lshlrev_b32_e32 v47, 16, v42
	v_fmac_f32_e32 v56, v46, v46
	v_add_f32_e32 v40, v40, v41
	v_and_b32_e32 v42, 0xffff0000, v42
	v_fmac_f32_e32 v56, v41, v41
	v_add_f32_e32 v40, v40, v47
	v_lshlrev_b32_e32 v48, 16, v43
	v_fmac_f32_e32 v56, v47, v47
	v_add_f32_e32 v40, v40, v42
	v_and_b32_e32 v43, 0xffff0000, v43
	v_fmac_f32_e32 v56, v42, v42
	v_add_f32_e32 v40, v40, v48
	v_fmac_f32_e32 v56, v48, v48
	v_add_f32_e32 v40, v40, v43
	v_lshlrev_b32_e32 v41, 16, v36
	v_fmac_f32_e32 v56, v43, v43
	v_and_b32_e32 v36, 0xffff0000, v36
	v_add_f32_e32 v40, v40, v41
	v_lshlrev_b32_e32 v42, 16, v37
	v_fmac_f32_e32 v56, v41, v41
	v_add_f32_e32 v40, v40, v36
	v_and_b32_e32 v37, 0xffff0000, v37
	v_fmac_f32_e32 v56, v36, v36
	v_add_f32_e32 v36, v40, v42
	v_lshlrev_b32_e32 v43, 16, v38
	v_fmac_f32_e32 v56, v42, v42
	v_add_f32_e32 v36, v36, v37
	v_and_b32_e32 v38, 0xffff0000, v38
	v_fmac_f32_e32 v56, v37, v37
	v_add_f32_e32 v36, v36, v43
	v_lshlrev_b32_e32 v44, 16, v39
	v_fmac_f32_e32 v56, v43, v43
	v_add_f32_e32 v36, v36, v38
	v_and_b32_e32 v39, 0xffff0000, v39
	v_fmac_f32_e32 v56, v38, v38
	v_add_f32_e32 v36, v36, v44
	v_fmac_f32_e32 v56, v44, v44
	v_add_f32_e32 v36, v36, v39
	s_waitcnt vmcnt(2)
	v_lshlrev_b32_e32 v37, 16, v32
	v_fmac_f32_e32 v56, v39, v39
	v_and_b32_e32 v32, 0xffff0000, v32
	v_add_f32_e32 v36, v36, v37
	v_lshlrev_b32_e32 v38, 16, v33
	v_fmac_f32_e32 v56, v37, v37
	v_add_f32_e32 v36, v36, v32
	v_and_b32_e32 v33, 0xffff0000, v33
	v_fmac_f32_e32 v56, v32, v32
	v_add_f32_e32 v32, v36, v38
	v_lshlrev_b32_e32 v39, 16, v34
	v_fmac_f32_e32 v56, v38, v38
	v_add_f32_e32 v32, v32, v33
	v_and_b32_e32 v34, 0xffff0000, v34
	v_fmac_f32_e32 v56, v33, v33
	v_add_f32_e32 v32, v32, v39
	v_lshlrev_b32_e32 v40, 16, v35
	v_fmac_f32_e32 v56, v39, v39
	v_add_f32_e32 v32, v32, v34
	v_and_b32_e32 v35, 0xffff0000, v35
	v_fmac_f32_e32 v56, v34, v34
	v_add_f32_e32 v32, v32, v40
	v_fmac_f32_e32 v56, v40, v40
	v_add_f32_e32 v32, v32, v35
	v_lshlrev_b32_e32 v33, 16, v24
	v_fmac_f32_e32 v56, v35, v35
	v_and_b32_e32 v24, 0xffff0000, v24
	v_add_f32_e32 v32, v32, v33
	v_lshlrev_b32_e32 v34, 16, v25
	v_fmac_f32_e32 v56, v33, v33
	v_add_f32_e32 v32, v32, v24
	v_and_b32_e32 v25, 0xffff0000, v25
	v_fmac_f32_e32 v56, v24, v24
	v_add_f32_e32 v24, v32, v34
	v_lshlrev_b32_e32 v35, 16, v26
	v_fmac_f32_e32 v56, v34, v34
	v_add_f32_e32 v24, v24, v25
	v_and_b32_e32 v26, 0xffff0000, v26
	v_fmac_f32_e32 v56, v25, v25
	v_add_f32_e32 v24, v24, v35
	v_lshlrev_b32_e32 v36, 16, v27
	v_fmac_f32_e32 v56, v35, v35
	v_add_f32_e32 v24, v24, v26
	v_and_b32_e32 v27, 0xffff0000, v27
	v_fmac_f32_e32 v56, v26, v26
	v_add_f32_e32 v24, v24, v36
	v_fmac_f32_e32 v56, v36, v36
	v_add_f32_e32 v24, v24, v27
	v_lshlrev_b32_e32 v25, 16, v20
	v_fmac_f32_e32 v56, v27, v27
	v_and_b32_e32 v20, 0xffff0000, v20
	v_add_f32_e32 v24, v24, v25
	v_lshlrev_b32_e32 v26, 16, v21
	v_fmac_f32_e32 v56, v25, v25
	v_add_f32_e32 v24, v24, v20
	v_and_b32_e32 v21, 0xffff0000, v21
	v_fmac_f32_e32 v56, v20, v20
	v_add_f32_e32 v20, v24, v26
	v_lshlrev_b32_e32 v27, 16, v22
	v_fmac_f32_e32 v56, v26, v26
	v_add_f32_e32 v20, v20, v21
	v_and_b32_e32 v22, 0xffff0000, v22
	v_fmac_f32_e32 v56, v21, v21
	v_add_f32_e32 v20, v20, v27
	v_lshlrev_b32_e32 v32, 16, v23
	v_fmac_f32_e32 v56, v27, v27
	v_add_f32_e32 v20, v20, v22
	v_and_b32_e32 v23, 0xffff0000, v23
	v_fmac_f32_e32 v56, v22, v22
	v_add_f32_e32 v20, v20, v32
	v_fmac_f32_e32 v56, v32, v32
	v_add_f32_e32 v20, v20, v23
	v_lshlrev_b32_e32 v21, 16, v12
	v_fmac_f32_e32 v56, v23, v23
	v_and_b32_e32 v12, 0xffff0000, v12
	v_add_f32_e32 v20, v20, v21
	v_lshlrev_b32_e32 v22, 16, v13
	v_fmac_f32_e32 v56, v21, v21
	v_add_f32_e32 v20, v20, v12
	v_and_b32_e32 v13, 0xffff0000, v13
	v_fmac_f32_e32 v56, v12, v12
	v_add_f32_e32 v12, v20, v22
	v_lshlrev_b32_e32 v23, 16, v14
	v_add_f32_e32 v12, v12, v13
	v_and_b32_e32 v14, 0xffff0000, v14
	v_fmac_f32_e32 v56, v22, v22
	v_add_f32_e32 v12, v12, v23
	v_lshlrev_b32_e32 v24, 16, v15
	v_fmac_f32_e32 v56, v13, v13
	v_add_f32_e32 v12, v12, v14
	v_and_b32_e32 v15, 0xffff0000, v15
	v_fmac_f32_e32 v56, v23, v23
	v_add_f32_e32 v12, v12, v24
	v_fmac_f32_e32 v56, v14, v14
	v_add_f32_e32 v12, v12, v15
	global_load_dwordx4 v[174:177], v158, s[8:9] offset:2048
	global_load_dwordx4 v[178:181], v158, s[10:11] offset:2048
	v_fmac_f32_e32 v56, v24, v24
	v_add_f32_dpp v12, v12, v12 quad_perm:[1,0,3,2] row_mask:0xf bank_mask:0xf bound_ctrl:1
	v_fmac_f32_e32 v56, v15, v15
	global_load_dwordx4 v[44:47], v158, s[8:9] offset:2064
	global_load_dwordx4 v[48:51], v158, s[10:11] offset:2064
	v_add_f32_dpp v157, v12, v12 quad_perm:[2,3,0,1] row_mask:0xf bank_mask:0xf bound_ctrl:1
	v_add_f32_dpp v12, v56, v56 quad_perm:[1,0,3,2] row_mask:0xf bank_mask:0xf bound_ctrl:1
	v_mul_f32_e32 v13, 0x3b000000, v157
	v_mul_f32_e32 v13, v13, v13
	v_add_f32_dpp v12, v12, v12 quad_perm:[2,3,0,1] row_mask:0xf bank_mask:0xf bound_ctrl:1
	v_fma_f32 v12, v12, s6, -v13
	v_max_f32_e32 v12, 0, v12
	v_add_f32_e32 v12, 0x358637bd, v12
	s_mov_b32 s6, 0xf800000
	v_mul_f32_e32 v13, 0x4f800000, v12
	v_cmp_gt_f32_e32 vcc, s6, v12
	v_lshlrev_b32_e32 v164, 1, v62
	s_waitcnt vmcnt(4)
; #define LAS __attribute__((address_space(3)))
; __device__ __forceinline__ unsigned pk2(float lo, float hi) { f32x2 v = {lo, hi}; bf16x2_t b = __builtin_convertvector(v, bf16x2_t); return __builtin_bit_cast(unsigned, b); }
; __device__ __forceinline__ void cvt8(const u32x4 r, float (&f)[8]) { f[0] = bflo(r.x); f[1] = bfhi(r.x); f[2] = bflo(r.y); f[3] = bfhi(r.y); f[4] = bflo(r.z); f[5] = bfhi(r.z); f[6] = bflo(r.w); f[7] = bfhi(r.w); }
; __device__ __forceinline__ void gmlp_unit(Ctx& C, int l, int uidx) {
;     ...
;         const float mean = s * (1.0f / 512.0f); const float var = fmaxf(q * (1.0f / 512.0f) - mean * mean, 0.f); const float rstd = 1.0f / sqrtf(var + LN_EPS);
;         const float* lg = INP(I_GLG) + l * 512 + 256 * hf + 64 * part; const float* lb = INP(I_GLB) + l * 512 + 256 * hf + 64 * part;
; #pragma unroll
;         for (int c8 = 0; c8 < 8; ++c8) { float f[8]; cvt8(r2[c8], f);
;             const f32x4 g0 = *(const f32x4*)(lg + 8 * c8), g1 = *(const f32x4*)(lg + 8 * c8 + 4), b0 = *(const f32x4*)(lb + 8 * c8), b1 = *(const f32x4*)(lb + 8 * c8 + 4);
;             const float gg[8] = {g0[0], g0[1], g0[2], g0[3], g1[0], g1[1], g1[2], g1[3]}, bb[8] = {b0[0], b0[1], b0[2], b0[3], b1[0], b1[1], b1[2], b1[3]};
; #pragma unroll
;             for (int j = 0; j < 8; ++j) { const float vn = (f[j] - mean) * rstd * gg[j] + bb[j];
;                 *(LAS bf16*)(C.lds + (64 * part + 8 * c8 + j) * VS + tok * 2) = (bf16)(pk2(vn, 0.f) & 0xffffu); } }
	v_lshlrev_b32_e32 v173, 16, v28
	v_cndmask_b32_e32 v24, v12, v13, vcc
	v_sqrt_f32_e32 v25, v24
	global_load_dwordx4 v[36:39], v[60:61], off offset:48
	global_load_dwordx4 v[40:43], v[60:61], off offset:32
	global_load_dwordx4 v[12:15], v[60:61], off offset:112
	global_load_dwordx4 v[20:23], v[60:61], off offset:96
	v_and_b32_e32 v28, 0xffff0000, v28
	v_fmac_f32_e32 v28, 0xbb000000, v157
	v_add_u32_e32 v26, -1, v25
	v_fma_f32 v27, -v26, v25, v24
	v_cmp_ge_f32_e64 s[6:7], 0, v27
	v_add_u32_e32 v27, 1, v25
	v_lshlrev_b32_e32 v182, 16, v29
	v_cndmask_b32_e64 v26, v25, v26, s[6:7]
	v_fma_f32 v25, -v27, v25, v24
	v_cmp_lt_f32_e64 s[6:7], 0, v25
	v_add3_u32 v162, 0, v164, v162
	v_fmac_f32_e32 v182, 0xbb000000, v157
	v_cndmask_b32_e64 v25, v26, v27, s[6:7]
	v_mul_f32_e32 v26, 0x37800000, v25
	v_cndmask_b32_e32 v25, v25, v26, vcc
	v_cmp_class_f32_e32 vcc, v24, v163
	v_and_b32_e32 v29, 0xffff0000, v29
	v_fmac_f32_e32 v29, 0xbb000000, v157
	v_cndmask_b32_e32 v63, v25, v24, vcc
	v_div_scale_f32 v64, s[6:7], v63, v63, 1.0
	v_rcp_f32_e32 v65, v64
	global_load_dwordx4 v[52:55], v158, s[8:9] offset:2080
	global_load_dwordx4 v[56:59], v158, s[10:11] offset:2080
	global_load_dwordx4 v[24:27], v[60:61], off offset:80
	global_load_dwordx4 v[32:35], v[60:61], off offset:64
	v_lshlrev_b32_e32 v183, 16, v30
	v_fmac_f32_e32 v173, 0xbb000000, v157
	v_fma_f32 v60, -v64, v65, 1.0
	v_fmac_f32_e32 v65, v60, v65
	v_div_scale_f32 v60, vcc, 1.0, v63, 1.0
	v_mul_f32_e32 v61, v60, v65
	v_fma_f32 v66, -v64, v61, v60
	v_fmac_f32_e32 v61, v66, v65
	v_fma_f32 v60, -v64, v61, v60
	v_div_fmas_f32 v60, v60, v65, v61
	v_div_fixup_f32 v159, v60, v63, 1.0
	global_load_dwordx4 v[60:63], v158, s[8:9] offset:2096
	global_load_dwordx4 v[64:67], v158, s[10:11] offset:2096
	v_mul_f32_e32 v28, v28, v159
	v_fmac_f32_e32 v183, 0xbb000000, v157
	v_mul_f32_e32 v173, v173, v159
	v_and_b32_e32 v30, 0xffff0000, v30
	v_fmac_f32_e32 v30, 0xbb000000, v157
	v_lshlrev_b32_e32 v184, 16, v31
	v_fmac_f32_e32 v184, 0xbb000000, v157
	v_and_b32_e32 v31, 0xffff0000, v31
	v_fmac_f32_e32 v31, 0xbb000000, v157
	s_movk_i32 s6, 0x110
	s_waitcnt vmcnt(12)
	v_fma_f32 v28, v175, v28, v179
	v_cvt_pk_bf16_f32 v28, v28, s0
	ds_write_b16 v162, v28 offset:272
	v_mul_f32_e32 v28, v182, v159
	v_fma_f32 v28, v176, v28, v180
	v_cvt_pk_bf16_f32 v28, v28, s0
	ds_write_b16 v162, v28 offset:544
	v_mul_f32_e32 v28, v29, v159
	v_fmac_f32_e32 v181, v177, v28
	v_cvt_pk_bf16_f32 v28, v181, s0
	ds_write_b16 v162, v28 offset:816
	v_mul_f32_e32 v28, v183, v159
	v_fma_f32 v173, v174, v173, v178
	s_waitcnt vmcnt(10)
	v_fma_f32 v28, v44, v28, v48
	v_cvt_pk_bf16_f32 v173, v173, s0
	v_cvt_pk_bf16_f32 v28, v28, s0
	ds_write_b16 v162, v173
	ds_write_b16 v162, v28 offset:1088
	v_mul_f32_e32 v28, v30, v159
	global_load_dwordx4 v[174:177], v158, s[8:9] offset:2112
	global_load_dwordx4 v[178:181], v158, s[10:11] offset:2112
	v_fma_f32 v28, v45, v28, v49
	v_cvt_pk_bf16_f32 v28, v28, s0
	ds_write_b16 v162, v28 offset:1360
	v_mul_f32_e32 v28, v184, v159
	v_fma_f32 v28, v46, v28, v50
	v_cvt_pk_bf16_f32 v28, v28, s0
	ds_write_b16 v162, v28 offset:1632
	v_mul_f32_e32 v28, v31, v159
	v_fmac_f32_e32 v51, v47, v28
	v_cvt_pk_bf16_f32 v28, v51, s0
	ds_write_b16 v162, v28 offset:1904
	global_load_dwordx4 v[28:31], v158, s[8:9] offset:2128
	global_load_dwordx4 v[48:51], v158, s[10:11] offset:2128
	v_lshlrev_b32_e32 v44, 16, v16
	v_and_b32_e32 v16, 0xffff0000, v16
	v_fmac_f32_e32 v16, 0xbb000000, v157
	v_mul_f32_e32 v16, v16, v159
	v_lshlrev_b32_e32 v45, 16, v17
	v_fmac_f32_e32 v45, 0xbb000000, v157
	v_and_b32_e32 v17, 0xffff0000, v17
	v_fmac_f32_e32 v17, 0xbb000000, v157
	v_lshlrev_b32_e32 v46, 16, v18
	s_waitcnt vmcnt(8)
	v_fma_f32 v16, v53, v16, v57
	v_cvt_pk_bf16_f32 v16, v16, s0
	ds_write_b16 v162, v16 offset:2448
	v_mul_f32_e32 v16, v45, v159
	v_fma_f32 v16, v54, v16, v58
	v_cvt_pk_bf16_f32 v16, v16, s0
	ds_write_b16 v162, v16 offset:2720
	v_mul_f32_e32 v16, v17, v159
	v_fmac_f32_e32 v59, v55, v16
	v_fmac_f32_e32 v44, 0xbb000000, v157
	v_cvt_pk_bf16_f32 v16, v59, s0
	v_fmac_f32_e32 v46, 0xbb000000, v157
	v_mul_f32_e32 v44, v44, v159
	ds_write_b16 v162, v16 offset:2992
	v_mul_f32_e32 v16, v46, v159
	v_and_b32_e32 v18, 0xffff0000, v18
	v_fma_f32 v44, v52, v44, v56
	s_waitcnt vmcnt(4)
	v_fma_f32 v16, v60, v16, v64
	v_cvt_pk_bf16_f32 v44, v44, s0
	v_cvt_pk_bf16_f32 v16, v16, s0
	v_fmac_f32_e32 v18, 0xbb000000, v157
	ds_write_b16 v162, v44 offset:2176
	ds_write_b16 v162, v16 offset:3264
	v_mul_f32_e32 v16, v18, v159
	v_lshlrev_b32_e32 v47, 16, v19
	global_load_dwordx4 v[52:55], v158, s[8:9] offset:2144
	global_load_dwordx4 v[56:59], v158, s[10:11] offset:2144
	v_fma_f32 v16, v61, v16, v65
	v_cvt_pk_bf16_f32 v16, v16, s0
	v_fmac_f32_e32 v47, 0xbb000000, v157
	ds_write_b16 v162, v16 offset:3536
	v_mul_f32_e32 v16, v47, v159
	v_and_b32_e32 v19, 0xffff0000, v19
	v_fma_f32 v16, v62, v16, v66
	v_cvt_pk_bf16_f32 v16, v16, s0
	v_fmac_f32_e32 v19, 0xbb000000, v157
	ds_write_b16 v162, v16 offset:3808
	v_mul_f32_e32 v16, v19, v159
	v_fmac_f32_e32 v67, v63, v16
	v_cvt_pk_bf16_f32 v16, v67, s0
	ds_write_b16 v162, v16 offset:4080
	global_load_dwordx4 v[16:19], v158, s[8:9] offset:2160
	global_load_dwordx4 v[44:47], v158, s[10:11] offset:2160
	v_lshlrev_b32_e32 v60, 16, v40
	v_and_b32_e32 v40, 0xffff0000, v40
	v_fmac_f32_e32 v40, 0xbb000000, v157
	v_mul_f32_e32 v40, v40, v159
	v_lshlrev_b32_e32 v61, 16, v41
	v_fmac_f32_e32 v61, 0xbb000000, v157
	v_and_b32_e32 v41, 0xffff0000, v41
	v_fmac_f32_e32 v41, 0xbb000000, v157
	v_lshlrev_b32_e32 v62, 16, v42
	v_fmac_f32_e32 v60, 0xbb000000, v157
	v_fmac_f32_e32 v62, 0xbb000000, v157
	v_mul_f32_e32 v60, v60, v159
	v_and_b32_e32 v42, 0xffff0000, v42
	v_fmac_f32_e32 v42, 0xbb000000, v157
	v_lshlrev_b32_e32 v164, 16, v43
	v_fmac_f32_e32 v164, 0xbb000000, v157
	v_and_b32_e32 v43, 0xffff0000, v43
	s_waitcnt vmcnt(6)
; #define LAS __attribute__((address_space(3)))
; __device__ __forceinline__ unsigned pk2(float lo, float hi) { f32x2 v = {lo, hi}; bf16x2_t b = __builtin_convertvector(v, bf16x2_t); return __builtin_bit_cast(unsigned, b); }
; __device__ __forceinline__ void cvt8(const u32x4 r, float (&f)[8]) { f[0] = bflo(r.x); f[1] = bfhi(r.x); f[2] = bflo(r.y); f[3] = bfhi(r.y); f[4] = bflo(r.z); f[5] = bfhi(r.z); f[6] = bflo(r.w); f[7] = bfhi(r.w); }
; __device__ __forceinline__ void gmlp_unit(Ctx& C, int l, int uidx) {
;     ...
;         for (int c8 = 0; c8 < 8; ++c8) { float f[8]; cvt8(r2[c8], f);
;             const f32x4 g0 = *(const f32x4*)(lg + 8 * c8), g1 = *(const f32x4*)(lg + 8 * c8 + 4), b0 = *(const f32x4*)(lb + 8 * c8), b1 = *(const f32x4*)(lb + 8 * c8 + 4);
;             const float gg[8] = {g0[0], g0[1], g0[2], g0[3], g1[0], g1[1], g1[2], g1[3]}, bb[8] = {b0[0], b0[1], b0[2], b0[3], b1[0], b1[1], b1[2], b1[3]};
; #pragma unroll
;             for (int j = 0; j < 8; ++j) { const float vn = (f[j] - mean) * rstd * gg[j] + bb[j];
;                 *(LAS bf16*)(C.lds + (64 * part + 8 * c8 + j) * VS + tok * 2) = (bf16)(pk2(vn, 0.f) & 0xffffu); } }
	v_fma_f32 v40, v175, v40, v179
	v_cvt_pk_bf16_f32 v40, v40, s0
	ds_write_b16 v162, v40 offset:4624
	v_mul_f32_e32 v40, v61, v159
	v_fma_f32 v40, v176, v40, v180
	v_cvt_pk_bf16_f32 v40, v40, s0
	ds_write_b16 v162, v40 offset:4896
	v_mul_f32_e32 v40, v41, v159
	v_fmac_f32_e32 v181, v177, v40
	v_cvt_pk_bf16_f32 v40, v181, s0
	ds_write_b16 v162, v40 offset:5168
	v_mul_f32_e32 v40, v62, v159
	v_fma_f32 v60, v174, v60, v178
	s_waitcnt vmcnt(4)
	v_fma_f32 v28, v28, v40, v48
	v_cvt_pk_bf16_f32 v60, v60, s0
	v_cvt_pk_bf16_f32 v28, v28, s0
	ds_write_b16 v162, v60 offset:4352
	ds_write_b16 v162, v28 offset:5440
	v_mul_f32_e32 v28, v42, v159
	global_load_dwordx4 v[60:63], v158, s[8:9] offset:2176
	global_load_dwordx4 v[64:67], v158, s[10:11] offset:2176
	v_fma_f32 v28, v29, v28, v49
	v_cvt_pk_bf16_f32 v28, v28, s0
	ds_write_b16 v162, v28 offset:5712
	v_mul_f32_e32 v28, v164, v159
	v_fma_f32 v28, v30, v28, v50
	v_cvt_pk_bf16_f32 v28, v28, s0
	v_fmac_f32_e32 v43, 0xbb000000, v157
	ds_write_b16 v162, v28 offset:5984
	v_mul_f32_e32 v28, v43, v159
	v_fmac_f32_e32 v51, v31, v28
	v_cvt_pk_bf16_f32 v28, v51, s0
	ds_write_b16 v162, v28 offset:6256
	global_load_dwordx4 v[28:31], v158, s[8:9] offset:2192
	global_load_dwordx4 v[40:43], v158, s[10:11] offset:2192
	v_lshlrev_b32_e32 v48, 16, v36
	v_and_b32_e32 v36, 0xffff0000, v36
	v_fmac_f32_e32 v36, 0xbb000000, v157
	v_mul_f32_e32 v36, v36, v159
	v_lshlrev_b32_e32 v49, 16, v37
	v_fmac_f32_e32 v49, 0xbb000000, v157
	v_and_b32_e32 v37, 0xffff0000, v37
	v_fmac_f32_e32 v37, 0xbb000000, v157
	v_lshlrev_b32_e32 v50, 16, v38
	v_fmac_f32_e32 v50, 0xbb000000, v157
	v_fmac_f32_e32 v48, 0xbb000000, v157
	v_and_b32_e32 v164, 0xffff0000, v38
	v_mul_f32_e32 v38, v48, v159
	v_fmac_f32_e32 v164, 0xbb000000, v157
	s_waitcnt vmcnt(6)
	v_fma_f32 v36, v53, v36, v57
	v_cvt_pk_bf16_f32 v36, v36, s0
	ds_write_b16 v162, v36 offset:6800
	v_mul_f32_e32 v36, v49, v159
	v_fma_f32 v36, v54, v36, v58
	v_cvt_pk_bf16_f32 v36, v36, s0
	ds_write_b16 v162, v36 offset:7072
	v_mul_f32_e32 v36, v37, v159
	v_fmac_f32_e32 v59, v55, v36
	v_cvt_pk_bf16_f32 v36, v59, s0
	ds_write_b16 v162, v36 offset:7344
	v_mul_f32_e32 v36, v50, v159
	v_fma_f32 v38, v52, v38, v56
	v_cvt_pk_bf16_f32 v38, v38, s0
	v_lshlrev_b32_e32 v173, 16, v39
	s_waitcnt vmcnt(4)
	v_fma_f32 v16, v16, v36, v44
	v_cvt_pk_bf16_f32 v16, v16, s0
	ds_write_b16 v162, v16 offset:7616
	v_mul_f32_e32 v16, v164, v159
	ds_write_b16 v162, v38 offset:6528
	v_fma_f32 v16, v17, v16, v45
	v_and_b32_e32 v174, 0xffff0000, v39
	global_load_dwordx4 v[36:39], v158, s[8:9] offset:2208
	global_load_dwordx4 v[48:51], v158, s[10:11] offset:2208
	v_cvt_pk_bf16_f32 v16, v16, s0
	v_fmac_f32_e32 v173, 0xbb000000, v157
	ds_write_b16 v162, v16 offset:7888
	v_mul_f32_e32 v16, v173, v159
	v_fma_f32 v16, v18, v16, v46
	v_cvt_pk_bf16_f32 v16, v16, s0
	v_fmac_f32_e32 v174, 0xbb000000, v157
	ds_write_b16 v162, v16 offset:8160
	v_mul_f32_e32 v16, v174, v159
	v_fmac_f32_e32 v47, v19, v16
	v_cvt_pk_bf16_f32 v16, v47, s0
	ds_write_b16 v162, v16 offset:8432
	global_load_dwordx4 v[16:19], v158, s[8:9] offset:2224
	global_load_dwordx4 v[44:47], v158, s[10:11] offset:2224
	v_lshlrev_b32_e32 v52, 16, v32
	v_and_b32_e32 v32, 0xffff0000, v32
	v_fmac_f32_e32 v32, 0xbb000000, v157
	v_mul_f32_e32 v32, v32, v159
	v_lshlrev_b32_e32 v53, 16, v33
	v_fmac_f32_e32 v53, 0xbb000000, v157
	v_and_b32_e32 v33, 0xffff0000, v33
	v_fmac_f32_e32 v33, 0xbb000000, v157
	v_lshlrev_b32_e32 v54, 16, v34
	v_fmac_f32_e32 v52, 0xbb000000, v157
	v_fmac_f32_e32 v54, 0xbb000000, v157
	v_and_b32_e32 v56, 0xffff0000, v34
	v_mul_f32_e32 v34, v52, v159
	v_fmac_f32_e32 v56, 0xbb000000, v157
	v_lshlrev_b32_e32 v57, 16, v35
	v_and_b32_e32 v58, 0xffff0000, v35
	s_waitcnt vmcnt(6)
	v_fma_f32 v32, v61, v32, v65
	v_cvt_pk_bf16_f32 v32, v32, s0
	ds_write_b16 v162, v32 offset:8976
	v_mul_f32_e32 v32, v53, v159
	v_fma_f32 v32, v62, v32, v66
	v_cvt_pk_bf16_f32 v32, v32, s0
	ds_write_b16 v162, v32 offset:9248
	v_mul_f32_e32 v32, v33, v159
	v_fmac_f32_e32 v67, v63, v32
	v_cvt_pk_bf16_f32 v32, v67, s0
	ds_write_b16 v162, v32 offset:9520
	v_mul_f32_e32 v32, v54, v159
	v_fma_f32 v34, v60, v34, v64
	s_waitcnt vmcnt(4)
	v_fma_f32 v28, v28, v32, v40
	v_cvt_pk_bf16_f32 v34, v34, s0
	v_cvt_pk_bf16_f32 v28, v28, s0
	ds_write_b16 v162, v34 offset:8704
	ds_write_b16 v162, v28 offset:9792
	v_mul_f32_e32 v28, v56, v159
	global_load_dwordx4 v[32:35], v158, s[8:9] offset:2240
	global_load_dwordx4 v[52:55], v158, s[10:11] offset:2240
	v_fma_f32 v28, v29, v28, v41
	v_cvt_pk_bf16_f32 v28, v28, s0
	v_fmac_f32_e32 v57, 0xbb000000, v157
	ds_write_b16 v162, v28 offset:10064
	v_mul_f32_e32 v28, v57, v159
	v_fma_f32 v28, v30, v28, v42
	v_cvt_pk_bf16_f32 v28, v28, s0
	v_fmac_f32_e32 v58, 0xbb000000, v157
	ds_write_b16 v162, v28 offset:10336
	v_mul_f32_e32 v28, v58, v159
	v_fmac_f32_e32 v43, v31, v28
	v_cvt_pk_bf16_f32 v28, v43, s0
	ds_write_b16 v162, v28 offset:10608
	global_load_dwordx4 v[28:31], v158, s[8:9] offset:2256
	global_load_dwordx4 v[40:43], v158, s[10:11] offset:2256
	v_lshlrev_b32_e32 v56, 16, v24
	v_and_b32_e32 v24, 0xffff0000, v24
	v_fmac_f32_e32 v24, 0xbb000000, v157
	v_mul_f32_e32 v24, v24, v159
	v_lshlrev_b32_e32 v57, 16, v25
	v_fmac_f32_e32 v57, 0xbb000000, v157
	v_and_b32_e32 v25, 0xffff0000, v25
	v_fmac_f32_e32 v56, 0xbb000000, v157
	v_fmac_f32_e32 v25, 0xbb000000, v157
	v_lshlrev_b32_e32 v58, 16, v26
	v_and_b32_e32 v59, 0xffff0000, v26
	v_mul_f32_e32 v26, v56, v159
	v_fmac_f32_e32 v58, 0xbb000000, v157
	v_lshlrev_b32_e32 v60, 16, v27
	v_and_b32_e32 v61, 0xffff0000, v27
	v_fmac_f32_e32 v59, 0xbb000000, v157
	s_waitcnt vmcnt(6)
; #define LAS __attribute__((address_space(3)))
; __device__ __forceinline__ unsigned pk2(float lo, float hi) { f32x2 v = {lo, hi}; bf16x2_t b = __builtin_convertvector(v, bf16x2_t); return __builtin_bit_cast(unsigned, b); }
; template <int CTRL> __device__ __forceinline__ float dpp_f(float x) { return __int_as_float(__builtin_amdgcn_update_dpp(0, __float_as_int(x), CTRL, 0xF, 0xF, true)); }
; __device__ __forceinline__ void cvt8(const u32x4 r, float (&f)[8]) { f[0] = bflo(r.x); f[1] = bfhi(r.x); f[2] = bflo(r.y); f[3] = bfhi(r.y); f[4] = bflo(r.z); f[5] = bfhi(r.z); f[6] = bflo(r.w); f[7] = bfhi(r.w); }
; __device__ __forceinline__ void gmlp_unit(Ctx& C, int l, int uidx) {
;     ...
;         for (int c8 = 0; c8 < 16; ++c8) { float f[8]; cvt8(r1[c8], f);
; #pragma unroll
;             for (int j = 0; j < 8; ++j) { s += f[j]; q += f[j] * f[j]; } }
;         s += dpp_f<DPP_XOR1>(s); s += dpp_f<DPP_XOR2>(s); q += dpp_f<DPP_XOR1>(q); q += dpp_f<DPP_XOR2>(q);
;         const float mean = s * (1.0f / 512.0f); const float var = fmaxf(q * (1.0f / 512.0f) - mean * mean, 0.f); const float rstd = 1.0f / sqrtf(var + LN_EPS);
;         const float* lg = INP(I_GLG) + l * 512 + 256 * hf + 64 * part; const float* lb = INP(I_GLB) + l * 512 + 256 * hf + 64 * part;
; #pragma unroll
;         for (int c8 = 0; c8 < 8; ++c8) { float f[8]; cvt8(r2[c8], f);
;             const f32x4 g0 = *(const f32x4*)(lg + 8 * c8), g1 = *(const f32x4*)(lg + 8 * c8 + 4), b0 = *(const f32x4*)(lb + 8 * c8), b1 = *(const f32x4*)(lb + 8 * c8 + 4);
;             const float gg[8] = {g0[0], g0[1], g0[2], g0[3], g1[0], g1[1], g1[2], g1[3]}, bb[8] = {b0[0], b0[1], b0[2], b0[3], b1[0], b1[1], b1[2], b1[3]};
; #pragma unroll
;             for (int j = 0; j < 8; ++j) { const float vn = (f[j] - mean) * rstd * gg[j] + bb[j];
;                 *(LAS bf16*)(C.lds + (64 * part + 8 * c8 + j) * VS + tok * 2) = (bf16)(pk2(vn, 0.f) & 0xffffu); } }
;     }
;     __syncthreads();
	v_fma_f32 v24, v37, v24, v49
	v_cvt_pk_bf16_f32 v24, v24, s0
	ds_write_b16 v162, v24 offset:11152
	v_mul_f32_e32 v24, v57, v159
	v_fma_f32 v24, v38, v24, v50
	v_cvt_pk_bf16_f32 v24, v24, s0
	ds_write_b16 v162, v24 offset:11424
	v_mul_f32_e32 v24, v25, v159
	v_fma_f32 v26, v36, v26, v48
	v_fmac_f32_e32 v51, v39, v24
	v_cvt_pk_bf16_f32 v26, v26, s0
	v_cvt_pk_bf16_f32 v24, v51, s0
	v_mul_f32_e32 v48, v58, v159
	ds_write_b16 v162, v26 offset:10880
	ds_write_b16 v162, v24 offset:11696
	s_waitcnt vmcnt(4)
	v_fma_f32 v16, v16, v48, v44
	global_load_dwordx4 v[24:27], v158, s[8:9] offset:2272
	global_load_dwordx4 v[36:39], v158, s[10:11] offset:2272
	v_cvt_pk_bf16_f32 v16, v16, s0
	ds_write_b16 v162, v16 offset:11968
	v_mul_f32_e32 v16, v59, v159
	v_fma_f32 v16, v17, v16, v45
	v_cvt_pk_bf16_f32 v16, v16, s0
	v_fmac_f32_e32 v60, 0xbb000000, v157
	ds_write_b16 v162, v16 offset:12240
	v_mul_f32_e32 v16, v60, v159
	v_fma_f32 v16, v18, v16, v46
	v_cvt_pk_bf16_f32 v16, v16, s0
	v_fmac_f32_e32 v61, 0xbb000000, v157
	ds_write_b16 v162, v16 offset:12512
	v_mul_f32_e32 v16, v61, v159
	v_fmac_f32_e32 v47, v19, v16
	v_cvt_pk_bf16_f32 v48, v47, s0
	global_load_dwordx4 v[16:19], v158, s[8:9] offset:2288
	global_load_dwordx4 v[44:47], v158, s[10:11] offset:2288
	ds_write_b16 v162, v48 offset:12784
	v_lshlrev_b32_e32 v48, 16, v20
	v_and_b32_e32 v20, 0xffff0000, v20
	v_fmac_f32_e32 v20, 0xbb000000, v157
	v_mul_f32_e32 v20, v20, v159
	v_lshlrev_b32_e32 v49, 16, v21
	v_fmac_f32_e32 v49, 0xbb000000, v157
	v_and_b32_e32 v21, 0xffff0000, v21
	v_fmac_f32_e32 v21, 0xbb000000, v157
	v_lshlrev_b32_e32 v50, 16, v22
	v_fmac_f32_e32 v50, 0xbb000000, v157
	v_and_b32_e32 v22, 0xffff0000, v22
	v_fmac_f32_e32 v22, 0xbb000000, v157
	v_lshlrev_b32_e32 v51, 16, v23
	v_fmac_f32_e32 v51, 0xbb000000, v157
	v_and_b32_e32 v23, 0xffff0000, v23
	s_waitcnt vmcnt(6)
	v_fma_f32 v20, v33, v20, v53
	v_cvt_pk_bf16_f32 v20, v20, s0
	ds_write_b16 v162, v20 offset:13328
	v_mul_f32_e32 v20, v49, v159
	v_fma_f32 v20, v34, v20, v54
	v_cvt_pk_bf16_f32 v20, v20, s0
	ds_write_b16 v162, v20 offset:13600
	v_mul_f32_e32 v20, v21, v159
	v_fmac_f32_e32 v55, v35, v20
	v_cvt_pk_bf16_f32 v20, v55, s0
	ds_write_b16 v162, v20 offset:13872
	v_mul_f32_e32 v20, v50, v159
	v_fmac_f32_e32 v23, 0xbb000000, v157
	v_lshlrev_b32_e32 v21, 16, v13
	s_waitcnt vmcnt(4)
	v_fma_f32 v20, v28, v20, v40
	v_cvt_pk_bf16_f32 v20, v20, s0
	ds_write_b16 v162, v20 offset:14144
	v_mul_f32_e32 v20, v22, v159
	v_fma_f32 v20, v29, v20, v41
	v_cvt_pk_bf16_f32 v20, v20, s0
	ds_write_b16 v162, v20 offset:14416
	v_mul_f32_e32 v20, v51, v159
	v_fma_f32 v20, v30, v20, v42
	v_cvt_pk_bf16_f32 v20, v20, s0
	ds_write_b16 v162, v20 offset:14688
	v_mul_f32_e32 v20, v23, v159
	v_fmac_f32_e32 v43, v31, v20
	v_cvt_pk_bf16_f32 v20, v43, s0
	ds_write_b16 v162, v20 offset:14960
	v_lshlrev_b32_e32 v20, 16, v12
	v_and_b32_e32 v12, 0xffff0000, v12
	v_fmac_f32_e32 v12, 0xbb000000, v157
	v_mul_f32_e32 v12, v12, v159
	v_fmac_f32_e32 v21, 0xbb000000, v157
	v_and_b32_e32 v13, 0xffff0000, v13
	v_fmac_f32_e32 v13, 0xbb000000, v157
	v_lshlrev_b32_e32 v22, 16, v14
	v_fmac_f32_e32 v22, 0xbb000000, v157
	v_and_b32_e32 v14, 0xffff0000, v14
	v_fmac_f32_e32 v14, 0xbb000000, v157
	v_lshlrev_b32_e32 v23, 16, v15
	v_fmac_f32_e32 v23, 0xbb000000, v157
	v_and_b32_e32 v15, 0xffff0000, v15
	v_fmac_f32_e32 v15, 0xbb000000, v157
	v_fmac_f32_e32 v48, 0xbb000000, v157
	v_fmac_f32_e32 v20, 0xbb000000, v157
	v_mul_f32_e32 v48, v48, v159
	s_waitcnt vmcnt(2)
	v_fma_f32 v12, v25, v12, v37
	v_cvt_pk_bf16_f32 v12, v12, s0
	ds_write_b16 v162, v12 offset:15504
	v_mul_f32_e32 v12, v21, v159
	v_fma_f32 v12, v26, v12, v38
	v_cvt_pk_bf16_f32 v12, v12, s0
	ds_write_b16 v162, v12 offset:15776
	v_mul_f32_e32 v12, v13, v159
	v_fmac_f32_e32 v39, v27, v12
	v_cvt_pk_bf16_f32 v12, v39, s0
	ds_write_b16 v162, v12 offset:16048
	v_mul_f32_e32 v12, v22, v159
	v_mul_f32_e32 v20, v20, v159
	v_fma_f32 v32, v32, v48, v52
	v_fma_f32 v20, v24, v20, v36
	v_cvt_pk_bf16_f32 v32, v32, s0
	s_waitcnt vmcnt(0)
	v_fma_f32 v12, v16, v12, v44
	v_cvt_pk_bf16_f32 v12, v12, s0
	ds_write_b16 v162, v12 offset:16320
	v_mul_f32_e32 v12, v14, v159
	v_fma_f32 v12, v17, v12, v45
	v_cvt_pk_bf16_f32 v12, v12, s0
	ds_write_b16 v162, v12 offset:16592
	v_mul_f32_e32 v12, v23, v159
	v_fma_f32 v12, v18, v12, v46
	v_cvt_pk_bf16_f32 v12, v12, s0
	ds_write_b16 v162, v12 offset:16864
	v_mul_f32_e32 v12, v15, v159
	v_fmac_f32_e32 v47, v19, v12
	v_cvt_pk_bf16_f32 v12, v47, s0
	ds_write_b16 v162, v12 offset:17136
	v_lshl_or_b32 v12, s34, 6, v161
	v_cvt_pk_bf16_f32 v20, v20, s0
	v_mul_lo_u32 v12, v12, s6
	ds_write_b16 v162, v32 offset:13056
	ds_write_b16 v162, v20 offset:15232
	v_add3_u32 v162, 0, v156, v12
	s_waitcnt lgkmcnt(0)
	s_barrier
; #define LAS __attribute__((address_space(3)))
; __device__ __forceinline__ unsigned pk2(float lo, float hi) { f32x2 v = {lo, hi}; bf16x2_t b = __builtin_convertvector(v, bf16x2_t); return __builtin_bit_cast(unsigned, b); }
; __device__ __forceinline__ float bflo(unsigned w) { return __uint_as_float(w << 16); }
; __device__ __forceinline__ float bfhi(unsigned w) { return __uint_as_float(w & 0xffff0000u); }
; #define MFMA32(a, b, c) __builtin_amdgcn_mfma_f32_32x32x16_bf16((a), (b), (c), 0, 0, 0)
; __device__ __forceinline__ void gmlp_unit(Ctx& C, int l, int uidx) {
;     ...
;     for (int s = 0; s < 8; ++s) {
;         bf16x8 Vf[2];
; #pragma unroll
;         for (int cb = 0; cb < 2; ++cb) Vf[cb] = *(const LAS bf16x8*)(C.lds + (64 * gl + 32 * cb + r32) * VS + (16 * s + 8 * h) * 2);
; #pragma unroll
;         for (int cb = 0; cb < 2; ++cb)
; #pragma unroll
;             for (int pb = 0; pb < 2; ++pb) acc[cb][pb] = MFMA32(Vf[cb], Wf[pb][s], acc[cb][pb]);
;     }
;     bf16* Y = WSP(bf16, WS_YCAT);
; #pragma unroll
;     for (int pb = 0; pb < 2; ++pb) { const int p = 64 * ph + 32 * pb + r32; const float bs = INP(I_GBS)[(l * 8 + g) * 128 + p];
;         bf16* yp = Y + (size_t)(row0 + p) * DM + 1536 + 64 * g + 4 * h;
; #pragma unroll
;         for (int cb = 0; cb < 2; ++cb)
; #pragma unroll
;             for (int rg = 0; rg < 4; ++rg) { const u32x2 uv = upre[pb][cb][rg];
;                 u32x2 w; w.x = pk2(bflo(uv.x) * (acc[cb][pb][4 * rg] + bs), bfhi(uv.x) * (acc[cb][pb][4 * rg + 1] + bs)); w.y = pk2(bflo(uv.y) * (acc[cb][pb][4 * rg + 2] + bs), bfhi(uv.y) * (acc[cb][pb][4 * rg + 3] + bs));
;                 *(u32x2*)(yp + 32 * cb + 8 * rg) = w; } }
	ds_read_b128 v[12:15], v162
	ds_read_b128 v[156:159], v162 offset:32
	s_waitcnt lgkmcnt(1)
	v_mfma_f32_32x32x16_bf16 v[52:67], v[12:15], v[4:7], 0
	s_lshl_b32 s6, s52, 7
	v_mfma_f32_32x32x16_bf16 v[20:35], v[12:15], v[8:11], 0
	ds_read_b128 v[12:15], v162 offset:8704
	ds_read_b128 v[174:177], v162 offset:8736
	s_waitcnt lgkmcnt(1)
	v_mfma_f32_32x32x16_bf16 v[36:51], v[12:15], v[4:7], 0
	v_mfma_f32_32x32x16_bf16 v[4:19], v[12:15], v[8:11], 0
	v_mfma_f32_32x32x16_bf16 v[52:67], v[156:159], v[116:119], v[52:67]
	v_mfma_f32_32x32x16_bf16 v[20:35], v[156:159], v[120:123], v[20:35]
	s_waitcnt lgkmcnt(0)
	v_mfma_f32_32x32x16_bf16 v[36:51], v[174:177], v[116:119], v[36:51]
	v_mfma_f32_32x32x16_bf16 v[4:19], v[174:177], v[120:123], v[4:19]
	ds_read_b128 v[116:119], v162 offset:64
	ds_read_b128 v[120:123], v162 offset:96
	s_waitcnt lgkmcnt(1)
	v_mfma_f32_32x32x16_bf16 v[52:67], v[116:119], v[104:107], v[52:67]
	v_mfma_f32_32x32x16_bf16 v[20:35], v[116:119], v[112:115], v[20:35]
	ds_read_b128 v[116:119], v162 offset:8768
	ds_read_b128 v[156:159], v162 offset:8800
	s_waitcnt lgkmcnt(1)
	v_mfma_f32_32x32x16_bf16 v[36:51], v[116:119], v[104:107], v[36:51]
	v_mfma_f32_32x32x16_bf16 v[4:19], v[116:119], v[112:115], v[4:19]
	v_mfma_f32_32x32x16_bf16 v[52:67], v[120:123], v[100:103], v[52:67]
	v_mfma_f32_32x32x16_bf16 v[20:35], v[120:123], v[108:111], v[20:35]
	s_waitcnt lgkmcnt(0)
	v_mfma_f32_32x32x16_bf16 v[36:51], v[156:159], v[100:103], v[36:51]
	ds_read_b128 v[100:103], v162 offset:128
	ds_read_b128 v[104:107], v162 offset:160
	v_mfma_f32_32x32x16_bf16 v[4:19], v[156:159], v[108:111], v[4:19]
	s_waitcnt lgkmcnt(1)
	v_mfma_f32_32x32x16_bf16 v[52:67], v[100:103], v[88:91], v[52:67]
	v_mfma_f32_32x32x16_bf16 v[20:35], v[100:103], v[96:99], v[20:35]
	ds_read_b128 v[100:103], v162 offset:8832
	ds_read_b128 v[108:111], v162 offset:8864
	s_waitcnt lgkmcnt(1)
	v_mfma_f32_32x32x16_bf16 v[36:51], v[100:103], v[88:91], v[36:51]
	v_mfma_f32_32x32x16_bf16 v[4:19], v[100:103], v[96:99], v[4:19]
	v_mfma_f32_32x32x16_bf16 v[52:67], v[104:107], v[84:87], v[52:67]
	v_mfma_f32_32x32x16_bf16 v[20:35], v[104:107], v[92:95], v[20:35]
	s_waitcnt lgkmcnt(0)
	v_mfma_f32_32x32x16_bf16 v[36:51], v[108:111], v[84:87], v[36:51]
	ds_read_b128 v[84:87], v162 offset:192
	ds_read_b128 v[88:91], v162 offset:224
	v_mfma_f32_32x32x16_bf16 v[4:19], v[108:111], v[92:95], v[4:19]
	s_waitcnt lgkmcnt(1)
	v_mfma_f32_32x32x16_bf16 v[52:67], v[84:87], v[76:79], v[52:67]
	v_mfma_f32_32x32x16_bf16 v[20:35], v[84:87], v[80:83], v[20:35]
	ds_read_b128 v[84:87], v162 offset:8896
	ds_read_b128 v[92:95], v162 offset:8928
	s_waitcnt lgkmcnt(1)
	v_mfma_f32_32x32x16_bf16 v[4:19], v[84:87], v[80:83], v[4:19]
	v_or_b32_e32 v80, s18, v161
	v_lshlrev_b32_e32 v82, 16, v154
	v_and_b32_e32 v83, 0xffff0000, v154
	v_mfma_f32_32x32x16_bf16 v[36:51], v[84:87], v[76:79], v[36:51]
	v_or_b32_e32 v76, s6, v80
	v_ashrrev_i32_e32 v77, 31, v76
	v_lshl_add_u64 v[78:79], v[76:77], 2, s[54:55]
	global_load_dword v78, v[78:79], off
	s_ashr_i32 s6, s6, 31
	v_mov_b32_e32 v77, s6
	v_mfma_f32_32x32x16_bf16 v[52:67], v[88:91], v[72:75], v[52:67]
	s_waitcnt lgkmcnt(0)
	v_mfma_f32_32x32x16_bf16 v[36:51], v[92:95], v[72:75], v[36:51]
	v_or_b32_e32 v72, s19, v80
	v_lshlrev_b32_e32 v72, 12, v72
	v_mov_b32_e32 v73, v3
	v_lshl_add_u64 v[74:75], s[46:47], 0, v[72:73]
	v_lshl_add_u64 v[74:75], v[74:75], 0, s[50:51]
	v_lshl_add_u64 v[74:75], v[74:75], 0, v[2:3]
	v_lshl_add_u64 v[80:81], v[74:75], 0, s[36:37]
	v_mfma_f32_32x32x16_bf16 v[20:35], v[88:91], v[68:71], v[20:35]
	s_waitcnt vmcnt(0)
	s_nop 0
	v_add_f32_e64 v52, v52, v78
	v_add_f32_e64 v53, v53, v78
	v_mul_f32_e64 v52, v52, v82
	v_mul_f32_e64 v53, v53, v83
	v_lshlrev_b32_e32 v82, 16, v155
	v_and_b32_e32 v83, 0xffff0000, v155
	v_pk_add_f32 v[54:55], v[54:55], v[78:79] op_sel_hi:[1,0]
	v_cvt_pk_bf16_f32 v52, v52, v53
	v_pk_mul_f32 v[54:55], v[54:55], v[82:83]
	v_pk_add_f32 v[36:37], v[36:37], v[78:79] op_sel_hi:[1,0]
	v_cvt_pk_bf16_f32 v53, v54, v55
	v_add_co_u32_e32 v54, vcc, s69, v74
	v_pk_add_f32 v[38:39], v[38:39], v[78:79] op_sel_hi:[1,0]
	s_nop 0
	v_addc_co_u32_e32 v55, vcc, 0, v75, vcc
	global_store_dwordx2 v[54:55], v[52:53], off offset:3072
	v_lshlrev_b32_e32 v52, 16, v152
	v_and_b32_e32 v53, 0xffff0000, v152
	v_pk_add_f32 v[54:55], v[56:57], v[78:79] op_sel_hi:[1,0]
	v_pk_add_f32 v[56:57], v[58:59], v[78:79] op_sel_hi:[1,0]
	v_pk_mul_f32 v[52:53], v[54:55], v[52:53]
	v_lshlrev_b32_e32 v54, 16, v153
	v_and_b32_e32 v55, 0xffff0000, v153
	v_pk_mul_f32 v[54:55], v[56:57], v[54:55]
	v_cvt_pk_bf16_f32 v52, v52, v53
	v_cvt_pk_bf16_f32 v53, v54, v55
	global_store_dwordx2 v[80:81], v[52:53], off offset:16
	v_lshlrev_b32_e32 v52, 16, v150
	v_and_b32_e32 v53, 0xffff0000, v150
	v_pk_add_f32 v[54:55], v[60:61], v[78:79] op_sel_hi:[1,0]
	v_pk_add_f32 v[56:57], v[62:63], v[78:79] op_sel_hi:[1,0]
	v_pk_mul_f32 v[52:53], v[54:55], v[52:53]
	v_lshlrev_b32_e32 v54, 16, v151
	v_and_b32_e32 v55, 0xffff0000, v151
	v_pk_mul_f32 v[54:55], v[56:57], v[54:55]
	v_cvt_pk_bf16_f32 v52, v52, v53
	v_cvt_pk_bf16_f32 v53, v54, v55
	global_store_dwordx2 v[80:81], v[52:53], off offset:32
	v_lshlrev_b32_e32 v52, 16, v148
	v_and_b32_e32 v53, 0xffff0000, v148
	v_pk_add_f32 v[54:55], v[64:65], v[78:79] op_sel_hi:[1,0]
	v_pk_add_f32 v[56:57], v[66:67], v[78:79] op_sel_hi:[1,0]
	v_pk_mul_f32 v[52:53], v[54:55], v[52:53]
	v_lshlrev_b32_e32 v54, 16, v149
	v_and_b32_e32 v55, 0xffff0000, v149
	v_pk_mul_f32 v[54:55], v[56:57], v[54:55]
	v_cvt_pk_bf16_f32 v52, v52, v53
	v_cvt_pk_bf16_f32 v53, v54, v55
	global_store_dwordx2 v[80:81], v[52:53], off offset:48
	v_lshlrev_b32_e32 v52, 16, v146
	v_and_b32_e32 v53, 0xffff0000, v146
; __device__ __forceinline__ unsigned pk2(float lo, float hi) { f32x2 v = {lo, hi}; bf16x2_t b = __builtin_convertvector(v, bf16x2_t); return __builtin_bit_cast(unsigned, b); }
; __device__ __forceinline__ float bflo(unsigned w) { return __uint_as_float(w << 16); }
; __device__ __forceinline__ float bfhi(unsigned w) { return __uint_as_float(w & 0xffff0000u); }
; __device__ __forceinline__ void gmlp_unit(Ctx& C, int l, int uidx) {
;     ...
;     for (int pb = 0; pb < 2; ++pb) { const int p = 64 * ph + 32 * pb + r32; const float bs = INP(I_GBS)[(l * 8 + g) * 128 + p];
;         bf16* yp = Y + (size_t)(row0 + p) * DM + 1536 + 64 * g + 4 * h;
; #pragma unroll
;         for (int cb = 0; cb < 2; ++cb)
; #pragma unroll
;             for (int rg = 0; rg < 4; ++rg) { const u32x2 uv = upre[pb][cb][rg];
;                 u32x2 w; w.x = pk2(bflo(uv.x) * (acc[cb][pb][4 * rg] + bs), bfhi(uv.x) * (acc[cb][pb][4 * rg + 1] + bs)); w.y = pk2(bflo(uv.y) * (acc[cb][pb][4 * rg + 2] + bs), bfhi(uv.y) * (acc[cb][pb][4 * rg + 3] + bs));
;                 *(u32x2*)(yp + 32 * cb + 8 * rg) = w; } }
	v_pk_mul_f32 v[36:37], v[36:37], v[52:53]
	v_lshlrev_b32_e32 v52, 16, v147
	v_and_b32_e32 v53, 0xffff0000, v147
	v_pk_mul_f32 v[38:39], v[38:39], v[52:53]
	v_cvt_pk_bf16_f32 v36, v36, v37
	v_cvt_pk_bf16_f32 v37, v38, v39
	global_store_dwordx2 v[80:81], v[36:37], off offset:64
	v_lshlrev_b32_e32 v36, 16, v144
	v_and_b32_e32 v37, 0xffff0000, v144
	v_pk_add_f32 v[38:39], v[40:41], v[78:79] op_sel_hi:[1,0]
	v_pk_add_f32 v[40:41], v[42:43], v[78:79] op_sel_hi:[1,0]
	v_pk_mul_f32 v[36:37], v[38:39], v[36:37]
	v_lshlrev_b32_e32 v38, 16, v145
	v_and_b32_e32 v39, 0xffff0000, v145
	v_pk_mul_f32 v[38:39], v[40:41], v[38:39]
	v_cvt_pk_bf16_f32 v36, v36, v37
	v_cvt_pk_bf16_f32 v37, v38, v39
	global_store_dwordx2 v[80:81], v[36:37], off offset:80
	v_lshlrev_b32_e32 v36, 16, v142
	v_and_b32_e32 v37, 0xffff0000, v142
	v_pk_add_f32 v[38:39], v[44:45], v[78:79] op_sel_hi:[1,0]
	v_pk_add_f32 v[40:41], v[46:47], v[78:79] op_sel_hi:[1,0]
	v_pk_mul_f32 v[36:37], v[38:39], v[36:37]
	v_lshlrev_b32_e32 v38, 16, v143
	v_and_b32_e32 v39, 0xffff0000, v143
	v_pk_mul_f32 v[38:39], v[40:41], v[38:39]
	v_cvt_pk_bf16_f32 v36, v36, v37
	v_cvt_pk_bf16_f32 v37, v38, v39
	global_store_dwordx2 v[80:81], v[36:37], off offset:96
	v_lshlrev_b32_e32 v36, 16, v140
	v_and_b32_e32 v37, 0xffff0000, v140
	v_pk_add_f32 v[38:39], v[48:49], v[78:79] op_sel_hi:[1,0]
	v_pk_add_f32 v[40:41], v[50:51], v[78:79] op_sel_hi:[1,0]
	v_pk_mul_f32 v[36:37], v[38:39], v[36:37]
	v_lshlrev_b32_e32 v38, 16, v141
	v_and_b32_e32 v39, 0xffff0000, v141
	v_pk_mul_f32 v[38:39], v[40:41], v[38:39]
	v_cvt_pk_bf16_f32 v36, v36, v37
	v_cvt_pk_bf16_f32 v37, v38, v39
	global_store_dwordx2 v[80:81], v[36:37], off offset:112
	v_lshl_add_u64 v[36:37], v[76:77], 2, s[54:55]
	global_load_dword v36, v[36:37], off offset:128
	v_or_b32_e32 v38, 0x20000, v72
	v_mov_b32_e32 v39, v3
	v_lshl_add_u64 v[38:39], s[46:47], 0, v[38:39]
	v_lshlrev_b32_e32 v42, 16, v138
	v_and_b32_e32 v43, 0xffff0000, v138
	v_lshl_add_u64 v[38:39], v[38:39], 0, s[50:51]
	v_lshl_add_u64 v[38:39], v[38:39], 0, v[2:3]
	v_lshl_add_u64 v[40:41], v[38:39], 0, s[36:37]
	v_mfma_f32_32x32x16_bf16 v[4:19], v[92:95], v[68:71], v[4:19]
	s_waitcnt vmcnt(0)
	v_add_f32_e64 v20, v20, v36
	v_add_f32_e64 v21, v21, v36
	v_mul_f32_e64 v20, v20, v42
	v_mul_f32_e64 v21, v21, v43
	v_lshlrev_b32_e32 v42, 16, v139
	v_and_b32_e32 v43, 0xffff0000, v139
	v_pk_add_f32 v[22:23], v[22:23], v[36:37] op_sel_hi:[1,0]
	v_cvt_pk_bf16_f32 v20, v20, v21
	v_pk_mul_f32 v[22:23], v[22:23], v[42:43]
	s_nop 1
	v_pk_add_f32 v[4:5], v[4:5], v[36:37] op_sel_hi:[1,0]
	v_cvt_pk_bf16_f32 v21, v22, v23
	v_add_co_u32_e32 v22, vcc, s69, v38
	v_pk_add_f32 v[6:7], v[6:7], v[36:37] op_sel_hi:[1,0]
	s_nop 0
	v_addc_co_u32_e32 v23, vcc, 0, v39, vcc
	global_store_dwordx2 v[22:23], v[20:21], off offset:3072
	v_lshlrev_b32_e32 v20, 16, v136
	v_and_b32_e32 v21, 0xffff0000, v136
	v_pk_add_f32 v[22:23], v[24:25], v[36:37] op_sel_hi:[1,0]
	v_pk_add_f32 v[24:25], v[26:27], v[36:37] op_sel_hi:[1,0]
	v_pk_mul_f32 v[20:21], v[22:23], v[20:21]
	v_lshlrev_b32_e32 v22, 16, v137
	v_and_b32_e32 v23, 0xffff0000, v137
	v_pk_mul_f32 v[22:23], v[24:25], v[22:23]
	v_cvt_pk_bf16_f32 v20, v20, v21
	v_cvt_pk_bf16_f32 v21, v22, v23
	global_store_dwordx2 v[40:41], v[20:21], off offset:16
	v_lshlrev_b32_e32 v20, 16, v134
	v_and_b32_e32 v21, 0xffff0000, v134
	v_pk_add_f32 v[22:23], v[28:29], v[36:37] op_sel_hi:[1,0]
	v_pk_add_f32 v[24:25], v[30:31], v[36:37] op_sel_hi:[1,0]
	v_pk_mul_f32 v[20:21], v[22:23], v[20:21]
	v_lshlrev_b32_e32 v22, 16, v135
	v_and_b32_e32 v23, 0xffff0000, v135
	v_pk_mul_f32 v[22:23], v[24:25], v[22:23]
	v_cvt_pk_bf16_f32 v20, v20, v21
	v_cvt_pk_bf16_f32 v21, v22, v23
	global_store_dwordx2 v[40:41], v[20:21], off offset:32
	v_lshlrev_b32_e32 v20, 16, v132
	v_and_b32_e32 v21, 0xffff0000, v132
	v_pk_add_f32 v[22:23], v[32:33], v[36:37] op_sel_hi:[1,0]
	v_pk_add_f32 v[24:25], v[34:35], v[36:37] op_sel_hi:[1,0]
	v_pk_mul_f32 v[20:21], v[22:23], v[20:21]
	v_lshlrev_b32_e32 v22, 16, v133
	v_and_b32_e32 v23, 0xffff0000, v133
	v_pk_mul_f32 v[22:23], v[24:25], v[22:23]
	v_cvt_pk_bf16_f32 v20, v20, v21
	v_cvt_pk_bf16_f32 v21, v22, v23
	global_store_dwordx2 v[40:41], v[20:21], off offset:48
	v_lshlrev_b32_e32 v20, 16, v130
	v_and_b32_e32 v21, 0xffff0000, v130
	v_pk_mul_f32 v[4:5], v[4:5], v[20:21]
	v_lshlrev_b32_e32 v20, 16, v131
	v_and_b32_e32 v21, 0xffff0000, v131
	v_pk_mul_f32 v[6:7], v[6:7], v[20:21]
	v_cvt_pk_bf16_f32 v4, v4, v5
	v_cvt_pk_bf16_f32 v5, v6, v7
	global_store_dwordx2 v[40:41], v[4:5], off offset:64
	v_lshlrev_b32_e32 v4, 16, v128
	v_and_b32_e32 v5, 0xffff0000, v128
	v_pk_add_f32 v[6:7], v[8:9], v[36:37] op_sel_hi:[1,0]
	v_pk_add_f32 v[8:9], v[10:11], v[36:37] op_sel_hi:[1,0]
	v_pk_mul_f32 v[4:5], v[6:7], v[4:5]
	v_lshlrev_b32_e32 v6, 16, v129
	v_and_b32_e32 v7, 0xffff0000, v129
	v_pk_mul_f32 v[6:7], v[8:9], v[6:7]
	v_cvt_pk_bf16_f32 v4, v4, v5
	v_cvt_pk_bf16_f32 v5, v6, v7
	global_store_dwordx2 v[40:41], v[4:5], off offset:80
	v_lshlrev_b32_e32 v4, 16, v126
	v_and_b32_e32 v5, 0xffff0000, v126
	v_pk_add_f32 v[6:7], v[12:13], v[36:37] op_sel_hi:[1,0]
	v_pk_add_f32 v[8:9], v[14:15], v[36:37] op_sel_hi:[1,0]
	v_pk_mul_f32 v[4:5], v[6:7], v[4:5]
	v_lshlrev_b32_e32 v6, 16, v127
	v_and_b32_e32 v7, 0xffff0000, v127
	v_pk_mul_f32 v[6:7], v[8:9], v[6:7]
	v_cvt_pk_bf16_f32 v4, v4, v5
	v_cvt_pk_bf16_f32 v5, v6, v7
	global_store_dwordx2 v[40:41], v[4:5], off offset:96
	v_lshlrev_b32_e32 v4, 16, v124
	v_and_b32_e32 v5, 0xffff0000, v124
	v_pk_add_f32 v[6:7], v[16:17], v[36:37] op_sel_hi:[1,0]
	v_pk_add_f32 v[8:9], v[18:19], v[36:37] op_sel_hi:[1,0]
	v_pk_mul_f32 v[4:5], v[6:7], v[4:5]
	v_lshlrev_b32_e32 v6, 16, v125
	v_and_b32_e32 v7, 0xffff0000, v125
	v_pk_mul_f32 v[6:7], v[8:9], v[6:7]
	v_cvt_pk_bf16_f32 v4, v4, v5
	v_cvt_pk_bf16_f32 v5, v6, v7
	global_store_dwordx2 v[40:41], v[4:5], off offset:112

.LBB0_1973:
	s_waitcnt vmcnt(0) lgkmcnt(0)
	s_barrier
	s_and_saveexec_b64 s[6:7], s[4:5]
	s_cbranch_execz .LBB0_1706
	v_add_u32_e32 v2, s3, v243
	v_cmp_eq_u32_e32 vcc, -1, v170
	s_nop 1
	v_cndmask_b32_e32 v170, v170, v2, vcc
	v_mov_b32_e32 v2, s85
	ds_write_b32 v2, v170
	v_mov_b32_e32 v2, s86
	ds_write_b32 v2, v171
	s_branch .LBB0_1706

.LBB0_2126:
	s_and_b64 vcc, exec, s[10:11]
	s_cbranch_vccz .LBB0_2136
	v_mov_b32_e32 v130, 0x900
	s_and_saveexec_b64 s[6:7], s[4:5]
	s_cbranch_execz .LBB0_2131
	s_mov_b64 s[10:11], exec
	v_mbcnt_lo_u32_b32 v2, s10, 0
	v_mbcnt_hi_u32_b32 v2, s11, v2
	v_cmp_eq_u32_e32 vcc, 0, v2
	s_and_saveexec_b64 s[8:9], vcc
	s_cbranch_execz .LBB0_2130
	s_bcnt1_i32_b64 s10, s[10:11]
	v_mov_b32_e32 v3, s10
	global_atomic_add v243, v163, v3, s[26:27] sc0

; #define GAS __attribute__((address_space(1)))
; __device__ __forceinline__ void tr_load(const TrBlk& t, int wave, int lane, f32x4 (&v)[16]) {
; #pragma unroll
;     for (int i = 0; i < 16; ++i) v[i] = __builtin_nontemporal_load((const f32x4 GAS*)((const char GAS*)t.src + (size_t)(16 * wave + i) * t.N * 4 + 16u * lane));
; }
.LBB0_2152:
	s_ashr_i32 s24, s87, 6
	s_add_u32 s10, s10, s56
	s_addc_u32 s11, s11, s57
	s_and_b64 s[56:57], s[6:7], exec
	s_cselect_b32 s19, s80, 0x1b200000
	s_and_b64 s[52:53], s[52:53], exec
	s_cselect_b32 s19, 0x2200000, s19
	s_and_b64 s[52:53], s[54:55], exec
	s_cselect_b32 s19, 0x400000, s19
	s_add_u32 s56, s48, s19
	s_addc_u32 s57, s49, 0
	s_cmp_eq_u32 s18, 2
	s_cselect_b64 s[52:53], -1, 0
	s_and_b64 s[52:53], s[12:13], s[52:53]
	s_and_b64 s[52:53], s[52:53], exec
	s_cselect_b32 s19, s79, 0x800
	s_add_i32 s97, s97, 32
	s_and_b64 s[52:53], s[12:13], exec
	s_cselect_b32 s52, s97, 1
	s_mul_i32 s58, s19, s52
	s_mul_hi_i32 s59, s19, s52
	s_and_b64 s[52:53], s[6:7], exec
	s_cselect_b32 s60, 0x600, s76
	s_and_b64 s[52:53], s[54:55], exec
	s_cselect_b32 s52, 0xf00, s60
	s_mul_i32 s53, s59, s52
	s_mul_hi_u32 s54, s58, s52
	s_add_i32 s54, s54, s53
	s_mul_i32 s52, s58, s52
	s_add_u32 s52, s56, s52
	s_mul_i32 s96, s96, 48
	s_addc_u32 s53, s57, s54
	s_sub_i32 s54, s95, s96
	s_and_b64 s[12:13], s[12:13], exec
	s_cselect_b32 s54, s54, s94
	s_abs_i32 s55, s93
	v_cvt_f32_u32_e32 v2, s55
	s_sub_i32 s56, 0, s55
	s_abs_i32 s13, s54
	s_xor_b32 s12, s54, s93
	v_rcp_iflag_f32_e32 v2, v2
	s_ashr_i32 s12, s12, 31
	s_load_dwordx2 s[10:11], s[10:11], 0x0
	s_mul_i32 s59, s59, s35
	v_mul_f32_e32 v2, 0x4f7ffffe, v2
	v_cvt_u32_f32_e32 v2, v2
	s_mul_i32 s91, s91, 48
	v_and_b32_e32 v133, 63, v131
	v_lshlrev_b32_e32 v132, 4, v133
	v_readfirstlane_b32 s57, v2
	s_mul_i32 s56, s56, s57
	s_mul_hi_u32 s56, s57, s56
	s_add_i32 s57, s57, s56
	s_mul_hi_u32 s56, s13, s57
	s_mul_i32 s57, s56, s55
	s_sub_i32 s13, s13, s57
	s_add_i32 s57, s56, 1
	s_sub_i32 s60, s13, s55
	s_cmp_ge_u32 s13, s55
	s_cselect_b32 s56, s57, s56
	s_cselect_b32 s13, s60, s13
	s_add_i32 s57, s56, 1
	s_cmp_ge_u32 s13, s55
	s_cselect_b32 s13, s57, s56
	s_xor_b32 s13, s13, s12
	s_sub_i32 s55, s13, s12
	s_lshl_b32 s56, s55, 7
	s_ashr_i32 s13, s56, 31
	s_add_u32 s12, s52, s56
	s_mul_hi_u32 s52, s58, s35
	s_addc_u32 s13, s53, s13
	s_add_i32 s53, s52, s59
	s_mul_i32 s52, s58, s35
	s_lshl_b64 s[52:53], s[52:53], 2
	s_waitcnt lgkmcnt(0)
	s_add_u32 s52, s10, s52
	s_addc_u32 s53, s11, s53
	s_mul_hi_i32 s11, s56, s35
	s_mul_i32 s10, s56, s35
	s_lshl_b64 s[10:11], s[10:11], 2
	s_add_u32 s56, s52, s10
	s_mul_i32 s55, s55, s93
	s_addc_u32 s57, s53, s11
	s_sub_i32 s10, s54, s55
	s_lshl_b32 s10, s10, 8
	s_ashr_i32 s11, s10, 31
	s_lshl_b64 s[52:53], s[10:11], 2
	s_add_u32 s52, s56, s52
	s_addc_u32 s53, s57, s53
	s_and_b64 s[54:55], s[8:9], exec
	s_cselect_b32 s11, s80, 0x1b200000
	s_and_b64 s[44:45], s[44:45], exec
	s_cselect_b32 s11, 0x2200000, s11
	s_and_b64 s[44:45], s[46:47], exec
	s_cselect_b32 s11, 0x400000, s11
	s_add_u32 s48, s48, s11
	s_addc_u32 s49, s49, 0
	s_cmp_eq_u32 s34, 2
	s_cselect_b64 s[44:45], -1, 0
	s_and_b64 s[44:45], s[42:43], s[44:45]
	s_and_b64 s[44:45], s[44:45], exec
	s_cselect_b32 s11, s79, 0x800
	s_add_i32 s92, s92, 32
	s_and_b64 s[44:45], s[42:43], exec
	s_cselect_b32 s44, s92, 1
	s_mul_i32 s54, s11, s44
	s_mul_hi_i32 s55, s11, s44
	s_and_b64 s[44:45], s[8:9], exec
	s_cselect_b32 s56, 0x600, s76
	s_and_b64 s[44:45], s[46:47], exec
	s_cselect_b32 s44, 0xf00, s56
	s_mul_i32 s45, s55, s44
	s_mul_hi_u32 s46, s54, s44
	s_add_i32 s46, s46, s45
	s_mul_i32 s44, s54, s44
	s_add_u32 s44, s48, s44
	s_addc_u32 s45, s49, s46
	s_sub_i32 s46, s90, s91
	s_and_b64 s[42:43], s[42:43], exec
	s_cselect_b32 s46, s46, s89
	s_abs_i32 s47, s88
	v_cvt_f32_u32_e32 v2, s47
	s_sub_i32 s48, 0, s47
	s_abs_i32 s43, s46
	s_xor_b32 s42, s46, s88
	v_rcp_iflag_f32_e32 v2, v2
	s_ashr_i32 s42, s42, 31
	s_mul_i32 s55, s55, s74
	v_mov_b32_e32 v134, 0
	v_mul_f32_e32 v2, 0x4f7ffffe, v2
	v_cvt_u32_f32_e32 v2, v2
	v_mov_b32_e32 v135, 0
	v_mov_b32_e32 v136, 0
	v_mov_b32_e32 v137, 0
	v_readfirstlane_b32 s49, v2
	s_mul_i32 s48, s48, s49
	s_mul_hi_u32 s48, s49, s48
	s_add_i32 s49, s49, s48
	s_mul_hi_u32 s48, s43, s49
	s_mul_i32 s49, s48, s47
	s_sub_i32 s43, s43, s49
	s_add_i32 s49, s48, 1
	s_sub_i32 s56, s43, s47
	s_cmp_ge_u32 s43, s47
	s_cselect_b32 s48, s49, s48
	s_cselect_b32 s43, s56, s43
	s_add_i32 s49, s48, 1
	s_cmp_ge_u32 s43, s47
	s_cselect_b32 s43, s49, s48
	s_xor_b32 s43, s43, s42
	s_sub_i32 s47, s43, s42
	s_lshl_b32 s48, s47, 7
	s_ashr_i32 s42, s48, 31
	s_add_u32 s44, s44, s48
	s_addc_u32 s45, s45, s42
	s_mul_hi_u32 s42, s54, s74
	s_add_i32 s43, s42, s55
	s_mul_i32 s42, s54, s74
	s_lshl_b64 s[42:43], s[42:43], 2
	s_add_u32 s49, s50, s42
	s_addc_u32 s50, s51, s43
	s_mul_hi_i32 s43, s48, s74
	s_mul_i32 s42, s48, s74
	s_lshl_b64 s[42:43], s[42:43], 2
	s_add_u32 s48, s49, s42
	s_mul_i32 s47, s47, s88
	s_addc_u32 s49, s50, s43
	s_sub_i32 s42, s46, s47
	s_lshl_b32 s42, s42, 8
	s_ashr_i32 s43, s42, 31
	s_lshl_b64 s[46:47], s[42:43], 2
	s_add_u32 s48, s48, s46
	s_addc_u32 s49, s49, s47
	s_and_b32 s50, s87, 0xffffffc0
	s_lshl_b32 s43, s24, 4
	s_mul_i32 s46, s50, s74
	s_mul_hi_i32 s47, s50, s74
	s_add_u32 s46, s48, s46
	s_addc_u32 s47, s49, s47
	s_or_b32 s51, s50, 4
	global_load_dwordx4 v[66:69], v132, s[46:47] nt
	s_mul_i32 s46, s51, s74
	s_mul_hi_i32 s47, s51, s74
	s_add_u32 s46, s48, s46
	s_addc_u32 s47, s49, s47
	s_or_b32 s54, s50, 8
	global_load_dwordx4 v[70:73], v132, s[46:47] nt
	s_mul_i32 s46, s54, s74
	s_mul_hi_i32 s47, s54, s74
	s_add_u32 s46, s48, s46
	s_addc_u32 s47, s49, s47
	s_or_b32 s55, s50, 12
	global_load_dwordx4 v[74:77], v132, s[46:47] nt
	s_mul_i32 s46, s55, s74
	s_mul_hi_i32 s47, s55, s74
	s_add_u32 s46, s48, s46
	s_addc_u32 s47, s49, s47
	s_or_b32 s56, s50, 16
	global_load_dwordx4 v[82:85], v132, s[46:47] nt
	s_mul_i32 s46, s56, s74
	s_mul_hi_i32 s47, s56, s74
	s_add_u32 s46, s48, s46
	s_addc_u32 s47, s49, s47
; #define LAS __attribute__((address_space(3)))
; #define GAS __attribute__((address_space(1)))
; __device__ __forceinline__ unsigned pk4_fp8(float a, float b, float c, float d) { int p = 0; p = __builtin_amdgcn_cvt_pk_fp8_f32(a, b, p, false); p = __builtin_amdgcn_cvt_pk_fp8_f32(c, d, p, true); return (unsigned)p; }
; #define WG_BAR() do { LDS_WAIT(); __builtin_amdgcn_s_barrier(); asm volatile("" ::: "memory"); } while (0)
; __device__ __forceinline__ void tr_load(const TrBlk& t, int wave, int lane, f32x4 (&v)[16]) {
; #pragma unroll
;     for (int i = 0; i < 16; ++i) v[i] = __builtin_nontemporal_load((const f32x4 GAS*)((const char GAS*)t.src + (size_t)(16 * wave + i) * t.N * 4 + 16u * lane));
; }
; __device__ __forceinline__ void tr_pack(LAS unsigned char* buf, int wave, int lane, const f32x4 (&v)[16]) {
; #pragma unroll
;     for (int j = 0; j < 4; ++j) { u32x4 o;
; #pragma unroll
;         for (int w = 0; w < 4; ++w) o[w] = pk4_fp8(64.f * v[4 * w][j], 64.f * v[4 * w + 1][j], 64.f * v[4 * w + 2][j], 64.f * v[4 * w + 3][j]);
;         *(LAS u32x4*)(buf + (4 * lane + j) * TRP + 16 * wave) = o; }
; }
; __device__ __forceinline__ void tr_flush(const TrBlk& t, const LAS unsigned char* buf, int wave, int lane) {
; #pragma unroll
;     for (int tt = 0; tt < 4; ++tt) { const int nl = 32 * wave + 8 * tt + (lane >> 3), n = 256 * t.nb + nl;
;         const u32x4 o = *(const LAS u32x4*)(buf + nl * TRP + 16 * (lane & 7));
;         const int drow = t.gu ? ((n >> 7) * 256 + (n & 127) + 128 * t.which) : n;
;         __builtin_nontemporal_store(o, (u32x4 GAS*)(t.dst + (size_t)drow * t.K + 16 * (lane & 7))); }
; }
; template <int NBK> __device__ __forceinline__ void tr_blocks(Ctx& C, int L, int b0) {
;     f32x4 r0[16], r1[16], r2[16];
;     LAS unsigned char* buf0 = C.lds; LAS unsigned char* buf1 = C.lds + TRBUF;
;     const TrBlk t0 = tr_decode(C, L, b0), t1 = tr_decode(C, L, b0 + (NBK > 1 ? 1 : 0)), t2 = tr_decode(C, L, b0 + (NBK > 2 ? 2 : 0)), t3 = tr_decode(C, L, b0 + (NBK > 3 ? 3 : 0));
;     tr_load(t0, C.wave, C.lane, r0); if (NBK > 1) tr_load(t1, C.wave, C.lane, r1); if (NBK > 2) tr_load(t2, C.wave, C.lane, r2);
;     WG_BAR();
;     tr_pack(buf0, C.wave, C.lane, r0);
	s_or_b32 s57, s50, 20
	global_load_dwordx4 v[78:81], v132, s[46:47] nt
	s_mul_i32 s46, s57, s74
	s_mul_hi_i32 s47, s57, s74
	s_add_u32 s46, s48, s46
	s_addc_u32 s47, s49, s47
	s_or_b32 s58, s50, 24
	global_load_dwordx4 v[86:89], v132, s[46:47] nt
	s_mul_i32 s46, s58, s74
	s_mul_hi_i32 s47, s58, s74
	s_add_u32 s46, s48, s46
	s_addc_u32 s47, s49, s47
	s_or_b32 s59, s50, 28
	global_load_dwordx4 v[94:97], v132, s[46:47] nt
	s_mul_i32 s46, s59, s74
	s_mul_hi_i32 s47, s59, s74
	s_add_u32 s46, s48, s46
	s_addc_u32 s47, s49, s47
	s_or_b32 s60, s50, 32
	global_load_dwordx4 v[102:105], v132, s[46:47] nt
	s_mul_i32 s46, s60, s74
	s_mul_hi_i32 s47, s60, s74
	s_add_u32 s46, s48, s46
	s_addc_u32 s47, s49, s47
	s_or_b32 s61, s50, 36
	global_load_dwordx4 v[90:93], v132, s[46:47] nt
	s_mul_i32 s46, s61, s74
	s_mul_hi_i32 s47, s61, s74
	s_add_u32 s46, s48, s46
	s_addc_u32 s47, s49, s47
	s_or_b32 s87, s50, 40
	global_load_dwordx4 v[98:101], v132, s[46:47] nt
	s_mul_i32 s46, s87, s74
	s_mul_hi_i32 s47, s87, s74
	s_add_u32 s46, s48, s46
	s_addc_u32 s47, s49, s47
	s_or_b32 s88, s50, 44
	global_load_dwordx4 v[106:109], v132, s[46:47] nt
	s_mul_i32 s46, s88, s74
	s_mul_hi_i32 s47, s88, s74
	s_add_u32 s46, s48, s46
	s_addc_u32 s47, s49, s47
	s_or_b32 s89, s50, 48
	global_load_dwordx4 v[114:117], v132, s[46:47] nt
	s_mul_i32 s46, s89, s74
	s_mul_hi_i32 s47, s89, s74
	s_add_u32 s46, s48, s46
	s_addc_u32 s47, s49, s47
	s_or_b32 s90, s50, 52
	global_load_dwordx4 v[110:113], v132, s[46:47] nt
	s_mul_i32 s46, s90, s74
	s_mul_hi_i32 s47, s90, s74
	s_add_u32 s46, s48, s46
	s_addc_u32 s47, s49, s47
	s_or_b32 s91, s50, 56
	global_load_dwordx4 v[118:121], v132, s[46:47] nt
	s_mul_i32 s46, s91, s74
	s_mul_hi_i32 s47, s91, s74
	s_add_u32 s46, s48, s46
	s_addc_u32 s47, s49, s47
	s_or_b32 s92, s50, 60
	global_load_dwordx4 v[122:125], v132, s[46:47] nt
	s_mul_i32 s46, s92, s74
	s_mul_hi_i32 s47, s92, s74
	s_add_u32 s46, s48, s46
	s_addc_u32 s47, s49, s47
	global_load_dwordx4 v[126:129], v132, s[46:47] nt
	s_mul_hi_i32 s47, s50, s35
	s_mul_i32 s50, s50, s35
	s_add_u32 s46, s52, s50
	s_addc_u32 s47, s53, s47
	global_load_dwordx4 v[2:5], v132, s[46:47] nt
	s_mul_hi_i32 s47, s51, s35
	s_mul_i32 s51, s51, s35
	s_add_u32 s46, s52, s51
	s_addc_u32 s47, s53, s47
	global_load_dwordx4 v[6:9], v132, s[46:47] nt
	s_mul_hi_i32 s47, s54, s35
	s_mul_i32 s54, s54, s35
	s_add_u32 s46, s52, s54
	s_addc_u32 s47, s53, s47
	global_load_dwordx4 v[10:13], v132, s[46:47] nt
	s_mul_hi_i32 s47, s55, s35
	s_mul_i32 s55, s55, s35
	s_add_u32 s46, s52, s55
	s_addc_u32 s47, s53, s47
	global_load_dwordx4 v[18:21], v132, s[46:47] nt
	s_mul_hi_i32 s47, s56, s35
	s_mul_i32 s56, s56, s35
	s_add_u32 s46, s52, s56
	s_addc_u32 s47, s53, s47
	global_load_dwordx4 v[14:17], v132, s[46:47] nt
	s_mul_hi_i32 s47, s57, s35
	s_mul_i32 s57, s57, s35
	s_add_u32 s46, s52, s57
	s_addc_u32 s47, s53, s47
	global_load_dwordx4 v[26:29], v132, s[46:47] nt
	s_mul_hi_i32 s47, s58, s35
	s_mul_i32 s58, s58, s35
	s_add_u32 s46, s52, s58
	s_addc_u32 s47, s53, s47
	global_load_dwordx4 v[30:33], v132, s[46:47] nt
	s_mul_hi_i32 s47, s59, s35
	s_mul_i32 s59, s59, s35
	s_add_u32 s46, s52, s59
	s_addc_u32 s47, s53, s47
	global_load_dwordx4 v[42:45], v132, s[46:47] nt
	s_mul_hi_i32 s47, s60, s35
	s_mul_i32 s60, s60, s35
	s_add_u32 s46, s52, s60
	s_addc_u32 s47, s53, s47
	global_load_dwordx4 v[22:25], v132, s[46:47] nt
	s_mul_hi_i32 s47, s61, s35
	s_mul_i32 s61, s61, s35
	s_add_u32 s46, s52, s61
	s_addc_u32 s47, s53, s47
	global_load_dwordx4 v[34:37], v132, s[46:47] nt
	s_mul_hi_i32 s47, s87, s35
	s_mul_i32 s87, s87, s35
	s_add_u32 s46, s52, s87
	s_addc_u32 s47, s53, s47
	global_load_dwordx4 v[38:41], v132, s[46:47] nt
	s_mul_hi_i32 s47, s88, s35
	s_mul_i32 s88, s88, s35
	s_add_u32 s46, s52, s88
	s_addc_u32 s47, s53, s47
	global_load_dwordx4 v[50:53], v132, s[46:47] nt
	s_mul_hi_i32 s47, s89, s35
	s_mul_i32 s89, s89, s35
	s_add_u32 s46, s52, s89
	s_addc_u32 s47, s53, s47
	global_load_dwordx4 v[46:49], v132, s[46:47] nt
	s_mul_hi_i32 s47, s90, s35
	s_mul_i32 s90, s90, s35
	s_add_u32 s46, s52, s90
	s_waitcnt vmcnt(0)
	v_mul_f32_e32 v66, 0x42800000, v66
	v_mul_f32_e32 v70, 0x42800000, v70
	s_addc_u32 s47, s53, s47
	v_cvt_pk_fp8_f32 v134, v66, v70
	v_mul_f32_e32 v66, 0x42800000, v78
	v_mul_f32_e32 v70, 0x42800000, v86
	global_load_dwordx4 v[54:57], v132, s[46:47] nt
	s_mul_hi_i32 s47, s91, s35
	s_mul_i32 s91, s91, s35
	v_cvt_pk_fp8_f32 v135, v66, v70
	v_mul_f32_e32 v66, 0x42800000, v90
	v_mul_f32_e32 v70, 0x42800000, v98
	s_add_u32 s46, s52, s91
	v_cvt_pk_fp8_f32 v136, v66, v70
	v_mul_f32_e32 v66, 0x42800000, v110
	v_mul_f32_e32 v70, 0x42800000, v118
	s_addc_u32 s47, s53, s47
	v_mul_f32_e32 v74, 0x42800000, v74
	v_mul_f32_e32 v82, 0x42800000, v82
	v_cvt_pk_fp8_f32 v137, v66, v70
	global_load_dwordx4 v[58:61], v132, s[46:47] nt
	s_mul_hi_i32 s47, s92, s35
	s_mul_i32 s92, s92, s35
	v_cvt_pk_fp8_f32 v134, v74, v82 op_sel:[0,0,1]
	v_mul_f32_e32 v74, 0x42800000, v94
	v_mul_f32_e32 v78, 0x42800000, v102
	s_add_u32 s46, s52, s92
	v_cvt_pk_fp8_f32 v135, v74, v78 op_sel:[0,0,1]
	v_mul_f32_e32 v74, 0x42800000, v106
	v_mul_f32_e32 v78, 0x42800000, v114
	s_addc_u32 s47, s53, s47
	v_cvt_pk_fp8_f32 v136, v74, v78 op_sel:[0,0,1]
	v_mul_f32_e32 v74, 0x42800000, v122
	v_mul_f32_e32 v78, 0x42800000, v126
	global_load_dwordx4 v[62:65], v132, s[46:47] nt
	v_cvt_pk_fp8_f32 v137, v74, v78 op_sel:[0,0,1]
	s_add_i32 s35, s43, 0
	v_mov_b32_e32 v66, s35
	s_movk_i32 s35, 0x240
	v_mad_u32_u24 v66, v133, s35, v66
	s_waitcnt lgkmcnt(0)
	s_barrier
; #define LAS __attribute__((address_space(3)))
; #define GAS __attribute__((address_space(1)))
; __device__ __forceinline__ unsigned pk4_fp8(float a, float b, float c, float d) { int p = 0; p = __builtin_amdgcn_cvt_pk_fp8_f32(a, b, p, false); p = __builtin_amdgcn_cvt_pk_fp8_f32(c, d, p, true); return (unsigned)p; }
; #define WG_BAR() do { LDS_WAIT(); __builtin_amdgcn_s_barrier(); asm volatile("" ::: "memory"); } while (0)
; __device__ __forceinline__ void tr_pack(LAS unsigned char* buf, int wave, int lane, const f32x4 (&v)[16]) {
; #pragma unroll
;     for (int j = 0; j < 4; ++j) { u32x4 o;
; #pragma unroll
;         for (int w = 0; w < 4; ++w) o[w] = pk4_fp8(64.f * v[4 * w][j], 64.f * v[4 * w + 1][j], 64.f * v[4 * w + 2][j], 64.f * v[4 * w + 3][j]);
;         *(LAS u32x4*)(buf + (4 * lane + j) * TRP + 16 * wave) = o; }
; }
; __device__ __forceinline__ void tr_flush(const TrBlk& t, const LAS unsigned char* buf, int wave, int lane) {
; #pragma unroll
;     for (int tt = 0; tt < 4; ++tt) { const int nl = 32 * wave + 8 * tt + (lane >> 3), n = 256 * t.nb + nl;
;         const u32x4 o = *(const LAS u32x4*)(buf + nl * TRP + 16 * (lane & 7));
;         const int drow = t.gu ? ((n >> 7) * 256 + (n & 127) + 128 * t.which) : n;
;         __builtin_nontemporal_store(o, (u32x4 GAS*)(t.dst + (size_t)drow * t.K + 16 * (lane & 7))); }
; }
; template <int NBK> __device__ __forceinline__ void tr_blocks(Ctx& C, int L, int b0) {
;     f32x4 r0[16], r1[16], r2[16];
;     LAS unsigned char* buf0 = C.lds; LAS unsigned char* buf1 = C.lds + TRBUF;
;     const TrBlk t0 = tr_decode(C, L, b0), t1 = tr_decode(C, L, b0 + (NBK > 1 ? 1 : 0)), t2 = tr_decode(C, L, b0 + (NBK > 2 ? 2 : 0)), t3 = tr_decode(C, L, b0 + (NBK > 3 ? 3 : 0));
;     tr_load(t0, C.wave, C.lane, r0); if (NBK > 1) tr_load(t1, C.wave, C.lane, r1); if (NBK > 2) tr_load(t2, C.wave, C.lane, r2);
;     WG_BAR();
;     tr_pack(buf0, C.wave, C.lane, r0);
;     if (NBK > 3) tr_load(t3, C.wave, C.lane, r0);
;     WG_BAR(); tr_flush(t0, buf0, C.wave, C.lane);
;     if (NBK > 1) { tr_pack(buf1, C.wave, C.lane, r1); WG_BAR(); tr_flush(t1, buf1, C.wave, C.lane); }
	ds_write_b128 v66, v[134:137]
	v_mul_f32_e32 v67, 0x42800000, v67
	v_mul_f32_e32 v70, 0x42800000, v71
	v_mov_b32_e32 v134, 0
	v_cvt_pk_fp8_f32 v134, v67, v70
	v_mul_f32_e32 v67, 0x42800000, v79
	v_mul_f32_e32 v70, 0x42800000, v87
	v_mov_b32_e32 v135, 0
	v_cvt_pk_fp8_f32 v135, v67, v70
	v_mul_f32_e32 v67, 0x42800000, v91
	v_mul_f32_e32 v70, 0x42800000, v99
	v_mov_b32_e32 v136, 0
	v_cvt_pk_fp8_f32 v136, v67, v70
	v_mul_f32_e32 v67, 0x42800000, v111
	v_mul_f32_e32 v70, 0x42800000, v119
	v_mov_b32_e32 v137, 0
	v_mul_f32_e32 v71, 0x42800000, v75
	v_mul_f32_e32 v74, 0x42800000, v83
	v_cvt_pk_fp8_f32 v137, v67, v70
	v_cvt_pk_fp8_f32 v134, v71, v74 op_sel:[0,0,1]
	v_mul_f32_e32 v71, 0x42800000, v95
	v_mul_f32_e32 v74, 0x42800000, v103
	v_cvt_pk_fp8_f32 v135, v71, v74 op_sel:[0,0,1]
	v_mul_f32_e32 v71, 0x42800000, v107
	v_mul_f32_e32 v74, 0x42800000, v115
	v_cvt_pk_fp8_f32 v136, v71, v74 op_sel:[0,0,1]
	v_mul_f32_e32 v71, 0x42800000, v123
	v_mul_f32_e32 v74, 0x42800000, v127
	v_cvt_pk_fp8_f32 v137, v71, v74 op_sel:[0,0,1]
	v_mul_f32_e32 v67, 0x42800000, v68
	v_mul_f32_e32 v68, 0x42800000, v72
	v_mul_f32_e32 v70, 0x42800000, v76
	ds_write_b128 v66, v[134:137] offset:144
	v_mov_b32_e32 v134, 0
	v_cvt_pk_fp8_f32 v134, v67, v68
	v_mul_f32_e32 v67, 0x42800000, v80
	v_mul_f32_e32 v68, 0x42800000, v88
	v_mov_b32_e32 v135, 0
	v_cvt_pk_fp8_f32 v135, v67, v68
	v_mul_f32_e32 v67, 0x42800000, v92
	v_mul_f32_e32 v68, 0x42800000, v100
	v_mov_b32_e32 v136, 0
	v_cvt_pk_fp8_f32 v136, v67, v68
	v_mul_f32_e32 v67, 0x42800000, v112
	v_mul_f32_e32 v68, 0x42800000, v120
	v_mov_b32_e32 v137, 0
	v_mul_f32_e32 v71, 0x42800000, v84
	v_cvt_pk_fp8_f32 v137, v67, v68
	v_mul_f32_e32 v67, 0x42800000, v69
	v_mul_f32_e32 v69, 0x42800000, v73
	v_mov_b32_e32 v68, 0
	v_cvt_pk_fp8_f32 v134, v70, v71 op_sel:[0,0,1]
	v_mul_f32_e32 v70, 0x42800000, v96
	v_mul_f32_e32 v71, 0x42800000, v104
	v_cvt_pk_fp8_f32 v68, v67, v69
	v_cvt_pk_fp8_f32 v135, v70, v71 op_sel:[0,0,1]
	v_mul_f32_e32 v70, 0x42800000, v108
	v_mul_f32_e32 v71, 0x42800000, v116
	v_cvt_pk_fp8_f32 v136, v70, v71 op_sel:[0,0,1]
	v_mul_f32_e32 v70, 0x42800000, v124
	v_mul_f32_e32 v71, 0x42800000, v128
	v_cvt_pk_fp8_f32 v137, v70, v71 op_sel:[0,0,1]
	v_mul_f32_e32 v70, 0x42800000, v77
	v_mul_f32_e32 v71, 0x42800000, v85
	v_cvt_pk_fp8_f32 v68, v70, v71 op_sel:[0,0,1]
	v_mul_f32_e32 v67, 0x42800000, v81
	v_mul_f32_e32 v70, 0x42800000, v89
	v_mov_b32_e32 v69, 0
	v_cvt_pk_fp8_f32 v69, v67, v70
	v_mul_f32_e32 v71, 0x42800000, v97
	v_mul_f32_e32 v72, 0x42800000, v105
	v_mul_f32_e32 v67, 0x42800000, v93
	v_cvt_pk_fp8_f32 v69, v71, v72 op_sel:[0,0,1]
	v_mul_f32_e32 v71, 0x42800000, v101
	v_mov_b32_e32 v70, 0
	v_cvt_pk_fp8_f32 v70, v67, v71
	v_mul_f32_e32 v72, 0x42800000, v109
	v_mul_f32_e32 v73, 0x42800000, v117
	v_mul_f32_e32 v67, 0x42800000, v113
	v_cvt_pk_fp8_f32 v70, v72, v73 op_sel:[0,0,1]
	v_mul_f32_e32 v72, 0x42800000, v121
	v_mov_b32_e32 v71, 0
	v_cvt_pk_fp8_f32 v71, v67, v72
	v_mul_f32_e32 v73, 0x42800000, v125
	v_mul_f32_e32 v74, 0x42800000, v129
	s_lshl_b32 s24, s24, 5
	v_cvt_pk_fp8_f32 v71, v73, v74 op_sel:[0,0,1]
	v_bfe_u32 v67, v131, 3, 3
	v_or_b32_e32 v76, s24, v67
	s_movk_i32 s35, 0x90
	ds_write_b128 v66, v[134:137] offset:288
	ds_write_b128 v66, v[68:71] offset:432
	v_and_b32_e32 v162, 0x70, v132
	v_add_u32_e32 v72, s42, v76
	v_mul_lo_u32 v68, v76, s35
	s_waitcnt lgkmcnt(0)
	s_barrier
	v_add3_u32 v77, 0, v162, v68
	v_lshlrev_b32_e32 v73, 1, v72
	v_bitop3_b32 v67, s24, v211, v67 bitop3:0xc8
	s_lshl_b32 s24, s34, 7
	ds_read_b128 v[68:71], v77
	v_and_b32_e32 v73, 0xffffff00, v73
	v_or_b32_e32 v74, s24, v67
	v_add_u32_e32 v73, v74, v73
	v_cndmask_b32_e64 v74, v72, v73, s[8:9]
	v_mov_b64_e32 v[72:73], s[44:45]
	v_mad_i64_i32 v[74:75], s[34:35], s11, v74, v[72:73]
	v_lshl_add_u64 v[74:75], v[74:75], 0, v[162:163]
	v_or_b32_e32 v78, 8, v76
	s_waitcnt lgkmcnt(0)
	global_store_dwordx4 v[74:75], v[68:71], off nt
	v_add_u32_e32 v74, s42, v78
	v_lshlrev_b32_e32 v75, 1, v74
	v_bitop3_b32 v79, v76, s81, 8 bitop3:0xc8
	ds_read_b128 v[68:71], v77 offset:1152
	v_and_b32_e32 v75, 0xffffff00, v75
	v_or_b32_e32 v80, s24, v79
	v_add_u32_e32 v75, v80, v75
	v_cndmask_b32_e64 v74, v74, v75, s[8:9]
	v_mad_i64_i32 v[74:75], s[34:35], s11, v74, v[72:73]
	v_lshl_add_u64 v[74:75], v[74:75], 0, v[162:163]
	v_or_b32_e32 v80, 16, v76
	s_waitcnt lgkmcnt(0)
	global_store_dwordx4 v[74:75], v[68:71], off nt
	v_add_u32_e32 v74, s42, v80
	v_lshlrev_b32_e32 v75, 1, v74
	v_bitop3_b32 v81, v76, s82, 16 bitop3:0xc8
	ds_read_b128 v[68:71], v77 offset:2304
	v_and_b32_e32 v75, 0xffffff00, v75
	v_or_b32_e32 v82, s24, v81
	v_add_u32_e32 v75, v82, v75
	v_cndmask_b32_e64 v74, v74, v75, s[8:9]
	v_mad_i64_i32 v[74:75], s[34:35], s11, v74, v[72:73]
	v_lshl_add_u64 v[74:75], v[74:75], 0, v[162:163]
	s_waitcnt lgkmcnt(0)
	global_store_dwordx4 v[74:75], v[68:71], off nt
	v_or_b32_e32 v74, 24, v76
	v_add_u32_e32 v75, s42, v74
	s_movk_i32 s34, 0x7f
	v_lshlrev_b32_e32 v82, 1, v75
	v_bitop3_b32 v83, v76, s34, 24 bitop3:0xc8
	ds_read_b128 v[68:71], v77 offset:3456
	v_and_b32_e32 v82, 0xffffff00, v82
	v_or_b32_e32 v84, s24, v83
	v_add_u32_e32 v82, v84, v82
	v_cndmask_b32_e64 v75, v75, v82, s[8:9]
	v_mad_i64_i32 v[72:73], s[8:9], s11, v75, v[72:73]
	v_lshl_add_u64 v[72:73], v[72:73], 0, v[162:163]
	s_waitcnt lgkmcnt(0)
	global_store_dwordx4 v[72:73], v[68:71], off nt
	v_mul_f32_e32 v2, 0x42800000, v2
	v_mul_f32_e32 v6, 0x42800000, v6
	v_mov_b32_e32 v68, v163
	v_cvt_pk_fp8_f32 v68, v2, v6
	v_mul_f32_e32 v2, 0x42800000, v14
	v_mul_f32_e32 v6, 0x42800000, v26
	v_mov_b32_e32 v69, v163
	v_cvt_pk_fp8_f32 v69, v2, v6
	v_mul_f32_e32 v2, 0x42800000, v22
	v_mul_f32_e32 v6, 0x42800000, v34
	v_mov_b32_e32 v70, v163
	v_cvt_pk_fp8_f32 v70, v2, v6
	v_mul_f32_e32 v2, 0x42800000, v46
	s_waitcnt vmcnt(6)
; #define LAS __attribute__((address_space(3)))
; #define GAS __attribute__((address_space(1)))
; __device__ __forceinline__ unsigned pk4_fp8(float a, float b, float c, float d) { int p = 0; p = __builtin_amdgcn_cvt_pk_fp8_f32(a, b, p, false); p = __builtin_amdgcn_cvt_pk_fp8_f32(c, d, p, true); return (unsigned)p; }
; #define WG_BAR() do { LDS_WAIT(); __builtin_amdgcn_s_barrier(); asm volatile("" ::: "memory"); } while (0)
; __device__ __forceinline__ void tr_pack(LAS unsigned char* buf, int wave, int lane, const f32x4 (&v)[16]) {
; #pragma unroll
;     for (int j = 0; j < 4; ++j) { u32x4 o;
; #pragma unroll
;         for (int w = 0; w < 4; ++w) o[w] = pk4_fp8(64.f * v[4 * w][j], 64.f * v[4 * w + 1][j], 64.f * v[4 * w + 2][j], 64.f * v[4 * w + 3][j]);
;         *(LAS u32x4*)(buf + (4 * lane + j) * TRP + 16 * wave) = o; }
; }
; __device__ __forceinline__ void tr_flush(const TrBlk& t, const LAS unsigned char* buf, int wave, int lane) {
; #pragma unroll
;     for (int tt = 0; tt < 4; ++tt) { const int nl = 32 * wave + 8 * tt + (lane >> 3), n = 256 * t.nb + nl;
;         const u32x4 o = *(const LAS u32x4*)(buf + nl * TRP + 16 * (lane & 7));
;         const int drow = t.gu ? ((n >> 7) * 256 + (n & 127) + 128 * t.which) : n;
;         __builtin_nontemporal_store(o, (u32x4 GAS*)(t.dst + (size_t)drow * t.K + 16 * (lane & 7))); }
; }
; template <int NBK> __device__ __forceinline__ void tr_blocks(Ctx& C, int L, int b0) {
;     f32x4 r0[16], r1[16], r2[16];
;     LAS unsigned char* buf0 = C.lds; LAS unsigned char* buf1 = C.lds + TRBUF;
;     const TrBlk t0 = tr_decode(C, L, b0), t1 = tr_decode(C, L, b0 + (NBK > 1 ? 1 : 0)), t2 = tr_decode(C, L, b0 + (NBK > 2 ? 2 : 0)), t3 = tr_decode(C, L, b0 + (NBK > 3 ? 3 : 0));
;     tr_load(t0, C.wave, C.lane, r0); if (NBK > 1) tr_load(t1, C.wave, C.lane, r1); if (NBK > 2) tr_load(t2, C.wave, C.lane, r2);
;     WG_BAR();
;     tr_pack(buf0, C.wave, C.lane, r0);
;     if (NBK > 3) tr_load(t3, C.wave, C.lane, r0);
;     WG_BAR(); tr_flush(t0, buf0, C.wave, C.lane);
;     if (NBK > 1) { tr_pack(buf1, C.wave, C.lane, r1); WG_BAR(); tr_flush(t1, buf1, C.wave, C.lane); }
	v_mul_f32_e32 v6, 0x42800000, v54
	v_mov_b32_e32 v71, v163
	v_mul_f32_e32 v10, 0x42800000, v10
	v_mul_f32_e32 v18, 0x42800000, v18
	v_cvt_pk_fp8_f32 v71, v2, v6
	v_cvt_pk_fp8_f32 v68, v10, v18 op_sel:[0,0,1]
	v_mul_f32_e32 v10, 0x42800000, v30
	v_mul_f32_e32 v14, 0x42800000, v42
	v_cvt_pk_fp8_f32 v69, v10, v14 op_sel:[0,0,1]
	v_mul_f32_e32 v10, 0x42800000, v38
	v_mul_f32_e32 v14, 0x42800000, v50
	v_cvt_pk_fp8_f32 v70, v10, v14 op_sel:[0,0,1]
	s_waitcnt vmcnt(5)
	v_mul_f32_e32 v10, 0x42800000, v58
	s_waitcnt vmcnt(4)
	v_mul_f32_e32 v14, 0x42800000, v62
	v_cvt_pk_fp8_f32 v71, v10, v14 op_sel:[0,0,1]
	v_mul_f32_e32 v2, 0x42800000, v3
	v_mul_f32_e32 v3, 0x42800000, v7
	v_mul_f32_e32 v6, 0x42800000, v11
	ds_write_b128 v66, v[68:71] offset:36864
	v_mov_b32_e32 v68, v163
	v_cvt_pk_fp8_f32 v68, v2, v3
	v_mul_f32_e32 v2, 0x42800000, v15
	v_mul_f32_e32 v3, 0x42800000, v27
	v_mov_b32_e32 v69, v163
	v_cvt_pk_fp8_f32 v69, v2, v3
	v_mul_f32_e32 v2, 0x42800000, v23
	v_mul_f32_e32 v3, 0x42800000, v35
	v_mov_b32_e32 v70, v163
	v_cvt_pk_fp8_f32 v70, v2, v3
	v_mul_f32_e32 v2, 0x42800000, v47
	v_mul_f32_e32 v3, 0x42800000, v55
	v_mov_b32_e32 v71, v163
	v_mul_f32_e32 v7, 0x42800000, v19
	v_cvt_pk_fp8_f32 v71, v2, v3
	v_cvt_pk_fp8_f32 v68, v6, v7 op_sel:[0,0,1]
	v_mul_f32_e32 v6, 0x42800000, v31
	v_mul_f32_e32 v7, 0x42800000, v43
	v_cvt_pk_fp8_f32 v69, v6, v7 op_sel:[0,0,1]
	v_mul_f32_e32 v6, 0x42800000, v39
	v_mul_f32_e32 v7, 0x42800000, v51
	v_cvt_pk_fp8_f32 v70, v6, v7 op_sel:[0,0,1]
	v_mul_f32_e32 v6, 0x42800000, v59
	v_mul_f32_e32 v7, 0x42800000, v63
	v_cvt_pk_fp8_f32 v71, v6, v7 op_sel:[0,0,1]
	v_mul_f32_e32 v2, 0x42800000, v4
	v_mul_f32_e32 v3, 0x42800000, v8
	v_mul_f32_e32 v4, 0x42800000, v12
	ds_write_b128 v66, v[68:71] offset:37008
	v_mov_b32_e32 v68, v163
	v_cvt_pk_fp8_f32 v68, v2, v3
	v_mul_f32_e32 v2, 0x42800000, v16
	v_mul_f32_e32 v3, 0x42800000, v28
	v_mov_b32_e32 v69, v163
	v_cvt_pk_fp8_f32 v69, v2, v3
	v_mul_f32_e32 v2, 0x42800000, v24
	v_mul_f32_e32 v3, 0x42800000, v36
	v_mov_b32_e32 v70, v163
	v_cvt_pk_fp8_f32 v70, v2, v3
	v_mul_f32_e32 v2, 0x42800000, v48
	v_mul_f32_e32 v3, 0x42800000, v56
	v_mov_b32_e32 v71, v163
	v_mul_f32_e32 v6, 0x42800000, v20
	v_cvt_pk_fp8_f32 v71, v2, v3
	v_cvt_pk_fp8_f32 v68, v4, v6 op_sel:[0,0,1]
	v_mul_f32_e32 v4, 0x42800000, v32
	v_mul_f32_e32 v6, 0x42800000, v44
	v_cvt_pk_fp8_f32 v69, v4, v6 op_sel:[0,0,1]
	v_mul_f32_e32 v4, 0x42800000, v40
	v_mul_f32_e32 v6, 0x42800000, v52
	v_cvt_pk_fp8_f32 v70, v4, v6 op_sel:[0,0,1]
	v_mul_f32_e32 v4, 0x42800000, v60
	v_mul_f32_e32 v6, 0x42800000, v64
	v_cvt_pk_fp8_f32 v71, v4, v6 op_sel:[0,0,1]
	v_mul_f32_e32 v3, 0x42800000, v5
	v_mul_f32_e32 v4, 0x42800000, v9
	v_mov_b32_e32 v2, v163
	v_cvt_pk_fp8_f32 v2, v3, v4
	v_mul_f32_e32 v5, 0x42800000, v13
	v_mul_f32_e32 v6, 0x42800000, v21
	v_mul_f32_e32 v4, 0x42800000, v17
	v_cvt_pk_fp8_f32 v2, v5, v6 op_sel:[0,0,1]
	v_mul_f32_e32 v5, 0x42800000, v29
	v_mov_b32_e32 v3, v163
	v_cvt_pk_fp8_f32 v3, v4, v5
	v_mul_f32_e32 v6, 0x42800000, v33
	v_mul_f32_e32 v7, 0x42800000, v45
	v_mul_f32_e32 v5, 0x42800000, v25
	v_cvt_pk_fp8_f32 v3, v6, v7 op_sel:[0,0,1]
	v_mul_f32_e32 v6, 0x42800000, v37
	v_mov_b32_e32 v4, v163
	v_cvt_pk_fp8_f32 v4, v5, v6
	v_mul_f32_e32 v7, 0x42800000, v41
	v_mul_f32_e32 v8, 0x42800000, v53
	v_mul_f32_e32 v6, 0x42800000, v49
	v_cvt_pk_fp8_f32 v4, v7, v8 op_sel:[0,0,1]
	v_mul_f32_e32 v7, 0x42800000, v57
	v_mov_b32_e32 v5, v163
	v_cvt_pk_fp8_f32 v5, v6, v7
	v_mul_f32_e32 v8, 0x42800000, v61
	v_mul_f32_e32 v9, 0x42800000, v65
	ds_write_b128 v66, v[68:71] offset:37152
	v_cvt_pk_fp8_f32 v5, v8, v9 op_sel:[0,0,1]
	v_add_u32_e32 v6, s10, v76
	v_lshlrev_b32_e32 v7, 1, v6
	s_lshl_b32 s11, s18, 7
	ds_write_b128 v66, v[2:5] offset:37296
	s_waitcnt lgkmcnt(0)
	s_barrier
	ds_read_b128 v[2:5], v77 offset:36864
	v_and_b32_e32 v7, 0xffffff00, v7
	v_or_b32_e32 v8, s11, v67
	v_add_u32_e32 v7, v8, v7
	v_cndmask_b32_e64 v8, v6, v7, s[6:7]
	v_mov_b64_e32 v[6:7], s[12:13]
	v_mad_i64_i32 v[8:9], s[8:9], s19, v8, v[6:7]
	v_lshl_add_u64 v[8:9], v[8:9], 0, v[162:163]
	s_waitcnt lgkmcnt(0)
	global_store_dwordx4 v[8:9], v[2:5], off nt
	v_add_u32_e32 v8, s10, v78
	v_lshlrev_b32_e32 v9, 1, v8
	ds_read_b128 v[2:5], v77 offset:38016
	v_and_b32_e32 v9, 0xffffff00, v9
	v_or_b32_e32 v10, s11, v79
	v_add_u32_e32 v9, v10, v9
	v_cndmask_b32_e64 v8, v8, v9, s[6:7]
	v_mad_i64_i32 v[8:9], s[8:9], s19, v8, v[6:7]
	v_lshl_add_u64 v[8:9], v[8:9], 0, v[162:163]
	s_waitcnt lgkmcnt(0)
	global_store_dwordx4 v[8:9], v[2:5], off nt
	v_add_u32_e32 v8, s10, v80
	v_lshlrev_b32_e32 v9, 1, v8
	ds_read_b128 v[2:5], v77 offset:39168
	v_and_b32_e32 v9, 0xffffff00, v9
	v_or_b32_e32 v10, s11, v81
	v_add_u32_e32 v9, v10, v9
	v_cndmask_b32_e64 v8, v8, v9, s[6:7]
	v_mad_i64_i32 v[8:9], s[8:9], s19, v8, v[6:7]
	v_lshl_add_u64 v[8:9], v[8:9], 0, v[162:163]
	s_waitcnt lgkmcnt(0)
	global_store_dwordx4 v[8:9], v[2:5], off nt
	v_add_u32_e32 v8, s10, v74
	v_lshlrev_b32_e32 v9, 1, v8
	ds_read_b128 v[2:5], v77 offset:40320
	v_and_b32_e32 v9, 0xffffff00, v9
	v_or_b32_e32 v10, s11, v83
	v_add_u32_e32 v9, v10, v9
	v_cndmask_b32_e64 v8, v8, v9, s[6:7]
	v_mad_i64_i32 v[6:7], s[6:7], s19, v8, v[6:7]
	v_lshl_add_u64 v[6:7], v[6:7], 0, v[162:163]
	s_waitcnt lgkmcnt(0)
	global_store_dwordx4 v[6:7], v[2:5], off nt
	s_barrier
	s_and_saveexec_b64 s[6:7], s[4:5]
	s_cbranch_execz .LBB0_2028
	s_waitcnt vmcnt(8)
	v_add_u32_e32 v2, s3, v243
	v_cmp_eq_u32_e32 vcc, -1, v130
	s_nop 1
	v_cndmask_b32_e32 v130, v130, v2, vcc
	v_mov_b32_e32 v2, s83
	ds_write_b32 v2, v130
	s_branch .LBB0_2028

; __global__ void __launch_bounds__(512, 2) fwd_kernel(Args args) {
	.amdhsa_kernel _Z10fwd_kernel4Args
		.amdhsa_group_segment_fixed_size 0
		.amdhsa_private_segment_fixed_size 0
		.amdhsa_kernarg_size 560
		.amdhsa_user_sgpr_count 2
		.amdhsa_user_sgpr_dispatch_ptr 0
		.amdhsa_user_sgpr_queue_ptr 0
		.amdhsa_user_sgpr_kernarg_segment_ptr 1
		.amdhsa_user_sgpr_dispatch_id 0
		.amdhsa_user_sgpr_kernarg_preload_length 0
		.amdhsa_user_sgpr_kernarg_preload_offset 0
		.amdhsa_user_sgpr_private_segment_size 0
		.amdhsa_uses_dynamic_stack 0
		.amdhsa_enable_private_segment 0
		.amdhsa_system_sgpr_workgroup_id_x 1
		.amdhsa_system_sgpr_workgroup_id_y 0
		.amdhsa_system_sgpr_workgroup_id_z 0
		.amdhsa_system_sgpr_workgroup_info 0
		.amdhsa_system_vgpr_workitem_id 0
		.amdhsa_next_free_vgpr 244
		.amdhsa_next_free_sgpr 98
		.amdhsa_accum_offset 244
		.amdhsa_reserve_vcc 1
		.amdhsa_float_round_mode_32 0
		.amdhsa_float_round_mode_16_64 0
		.amdhsa_float_denorm_mode_32 3
		.amdhsa_float_denorm_mode_16_64 3
		.amdhsa_dx10_clamp 1
		.amdhsa_ieee_mode 1
		.amdhsa_fp16_overflow 0
		.amdhsa_tg_split 0
		.amdhsa_exception_fp_ieee_invalid_op 0
		.amdhsa_exception_fp_denorm_src 0
		.amdhsa_exception_fp_ieee_div_zero 0
		.amdhsa_exception_fp_ieee_overflow 0
		.amdhsa_exception_fp_ieee_underflow 0
		.amdhsa_exception_fp_ieee_inexact 0
		.amdhsa_exception_int_div_zero 0
	.end_amdhsa_kernel

; __global__ void __launch_bounds__(512, 2) fwd_kernel(Args args) {
amdhsa.kernels:
  - .agpr_count:     0
    .args:
      - .offset:         0
        .size:           304
        .value_kind:     by_value
      - .offset:         304
        .size:           4
        .value_kind:     hidden_block_count_x
      - .offset:         308
        .size:           4
        .value_kind:     hidden_block_count_y
      - .offset:         312
        .size:           4
        .value_kind:     hidden_block_count_z
      - .offset:         316
        .size:           2
        .value_kind:     hidden_group_size_x
      - .offset:         318
        .size:           2
        .value_kind:     hidden_group_size_y
      - .offset:         320
        .size:           2
        .value_kind:     hidden_group_size_z
      - .offset:         322
        .size:           2
        .value_kind:     hidden_remainder_x
      - .offset:         324
        .size:           2
        .value_kind:     hidden_remainder_y
      - .offset:         326
        .size:           2
        .value_kind:     hidden_remainder_z
      - .offset:         344
        .size:           8
        .value_kind:     hidden_global_offset_x
      - .offset:         352
        .size:           8
        .value_kind:     hidden_global_offset_y
      - .offset:         360
        .size:           8
        .value_kind:     hidden_global_offset_z
      - .offset:         368
        .size:           2
        .value_kind:     hidden_grid_dims
      - .offset:         424
        .size:           4
        .value_kind:     hidden_dynamic_lds_size
    .group_segment_fixed_size: 0
    .kernarg_segment_align: 8
    .kernarg_segment_size: 560
    .language:       OpenCL C
    .language_version:
      - 2
      - 0
    .max_flat_workgroup_size: 512
    .name:           _Z10fwd_kernel4Args
    .private_segment_fixed_size: 0
    .sgpr_count:     104
    .sgpr_spill_count: 12
    .symbol:         _Z10fwd_kernel4Args.kd
    .uniform_work_group_size: 1
    .uses_dynamic_stack: false
    .vgpr_count:     244
    .vgpr_spill_count: 0
    .wavefront_size: 64
